# E6 with every s_setprio removed (GEMM MMA blocks no longer raise priority; 496 lines deleted)
# speedup vs baseline: 1.0080x; 1.0080x over previous
.LBB0_259:
	s_waitcnt vmcnt(0)
	ds_read_b128 v[170:173], v161
	ds_read_b128 v[174:177], v161 offset:1024
	ds_read_b128 v[178:181], v161 offset:2048
	ds_read_b128 v[182:185], v161 offset:3072
	ds_read_b128 v[186:189], v165
	ds_read_b128 v[190:193], v165 offset:1024
	ds_read_b128 v[194:197], v165 offset:2048
	ds_read_b128 v[198:201], v165 offset:3072
	s_add_u32 s36, s30, 0x100
	s_addc_u32 s37, s31, 0
	s_cmp_eq_u32 s29, 12
	s_cselect_b32 s41, s25, s37
	s_cselect_b32 s40, s24, s36
	s_cselect_b32 s39, s27, s23
	s_cselect_b32 s38, s26, s21
	v_lshl_add_u64 v[150:151], s[30:31], 0, v[140:141]
	s_add_i32 m0, s53, 0xc000
	ds_read_b128 v[202:205], v169
	ds_read_b128 v[206:209], v169 offset:1024
	ds_read_b128 v[210:213], v169 offset:2048
	ds_read_b128 v[214:217], v169 offset:3072
	ds_read_b128 v[218:221], v169 offset:4096
	ds_read_b128 v[222:225], v169 offset:5120
	ds_read_b128 v[226:229], v169 offset:6144
	ds_read_b128 v[230:233], v169 offset:7168
	global_load_lds_dwordx4 v[150:151], off
	v_lshl_add_u64 v[150:151], s[30:31], 0, v[138:139]
	s_add_i32 m0, s53, 0xe000
	s_nop 0
	global_load_lds_dwordx4 v[150:151], off
	s_waitcnt vmcnt(8)
	s_waitcnt lgkmcnt(0)
	s_barrier
	s_waitcnt lgkmcnt(0)
	v_mfma_f32_16x16x32_bf16 v[124:127], v[170:173], v[202:205], v[124:127]
	v_mfma_f32_16x16x32_bf16 v[120:123], v[178:181], v[202:205], v[120:123]
	v_mfma_f32_16x16x32_bf16 v[112:115], v[170:173], v[210:213], v[112:115]
	v_mfma_f32_16x16x32_bf16 v[104:107], v[178:181], v[210:213], v[104:107]
	v_mfma_f32_16x16x32_bf16 v[96:99], v[170:173], v[218:221], v[96:99]
	v_mfma_f32_16x16x32_bf16 v[88:91], v[178:181], v[218:221], v[88:91]
	v_mfma_f32_16x16x32_bf16 v[80:83], v[170:173], v[226:229], v[80:83]
	v_mfma_f32_16x16x32_bf16 v[72:75], v[178:181], v[226:229], v[72:75]
	v_mfma_f32_16x16x32_bf16 v[124:127], v[174:177], v[206:209], v[124:127]
	v_mfma_f32_16x16x32_bf16 v[120:123], v[182:185], v[206:209], v[120:123]
	v_mfma_f32_16x16x32_bf16 v[112:115], v[174:177], v[214:217], v[112:115]
	v_mfma_f32_16x16x32_bf16 v[104:107], v[182:185], v[214:217], v[104:107]
	v_mfma_f32_16x16x32_bf16 v[96:99], v[174:177], v[222:225], v[96:99]
	v_mfma_f32_16x16x32_bf16 v[88:91], v[182:185], v[222:225], v[88:91]
	v_mfma_f32_16x16x32_bf16 v[80:83], v[174:177], v[230:233], v[80:83]
	v_mfma_f32_16x16x32_bf16 v[72:75], v[182:185], v[230:233], v[72:75]
	v_mfma_f32_16x16x32_bf16 v[116:119], v[186:189], v[202:205], v[116:119]
	v_mfma_f32_16x16x32_bf16 v[108:111], v[194:197], v[202:205], v[108:111]
	v_mfma_f32_16x16x32_bf16 v[100:103], v[186:189], v[210:213], v[100:103]
	v_mfma_f32_16x16x32_bf16 v[92:95], v[194:197], v[210:213], v[92:95]
	v_mfma_f32_16x16x32_bf16 v[84:87], v[186:189], v[218:221], v[84:87]
	v_mfma_f32_16x16x32_bf16 v[76:79], v[194:197], v[218:221], v[76:79]
	v_mfma_f32_16x16x32_bf16 v[68:71], v[186:189], v[226:229], v[68:71]
	v_mfma_f32_16x16x32_bf16 v[64:67], v[194:197], v[226:229], v[64:67]
	v_mfma_f32_16x16x32_bf16 v[116:119], v[190:193], v[206:209], v[116:119]
	v_mfma_f32_16x16x32_bf16 v[108:111], v[198:201], v[206:209], v[108:111]
	v_mfma_f32_16x16x32_bf16 v[100:103], v[190:193], v[214:217], v[100:103]
	v_mfma_f32_16x16x32_bf16 v[92:95], v[198:201], v[214:217], v[92:95]
	v_mfma_f32_16x16x32_bf16 v[84:87], v[190:193], v[222:225], v[84:87]
	v_mfma_f32_16x16x32_bf16 v[76:79], v[198:201], v[222:225], v[76:79]
	v_mfma_f32_16x16x32_bf16 v[68:71], v[190:193], v[230:233], v[68:71]
	v_mfma_f32_16x16x32_bf16 v[64:67], v[198:201], v[230:233], v[64:67]
	s_barrier
	s_add_i32 s30, s61, s50
	v_lshl_add_u64 v[150:151], s[38:39], 0, v[132:133]
	s_mov_b32 m0, s30
	ds_read_b128 v[202:205], v169 offset:16384
	ds_read_b128 v[206:209], v169 offset:17408
	ds_read_b128 v[210:213], v169 offset:18432
	ds_read_b128 v[214:217], v169 offset:19456
	ds_read_b128 v[218:221], v169 offset:20480
	ds_read_b128 v[222:225], v169 offset:21504
	ds_read_b128 v[226:229], v169 offset:22528
	ds_read_b128 v[230:233], v169 offset:23552
	global_load_lds_dwordx4 v[150:151], off
	s_add_i32 m0, s30, 0x2000
	s_add_u32 s30, s38, 0x40000
	v_lshl_add_u64 v[154:155], s[38:39], 0, v[128:129]
	s_addc_u32 s31, s39, 0
	s_add_i32 s64, s62, s50
	global_load_lds_dwordx4 v[154:155], off
	v_lshl_add_u64 v[158:159], s[30:31], 0, v[132:133]
	s_mov_b32 m0, s64
	v_lshl_add_u64 v[162:163], s[40:41], 0, v[130:131]
	global_load_lds_dwordx4 v[158:159], off
	v_lshl_add_u64 v[158:159], s[30:31], 0, v[128:129]
	s_add_i32 m0, s64, 0x2000
	s_nop 0
	global_load_lds_dwordx4 v[158:159], off
	v_lshl_add_u64 v[158:159], s[40:41], 0, v[134:135]
	s_mov_b32 m0, s53
	s_nop 0
	global_load_lds_dwordx4 v[158:159], off
	s_mov_b32 m0, s54
	s_nop 0
	global_load_lds_dwordx4 v[162:163], off
	s_waitcnt vmcnt(8)
	s_waitcnt lgkmcnt(0)
	s_barrier
	s_waitcnt lgkmcnt(0)
	v_mfma_f32_16x16x32_bf16 v[60:63], v[170:173], v[202:205], v[60:63]
	v_mfma_f32_16x16x32_bf16 v[56:59], v[178:181], v[202:205], v[56:59]
	v_mfma_f32_16x16x32_bf16 v[48:51], v[170:173], v[210:213], v[48:51]
	v_mfma_f32_16x16x32_bf16 v[40:43], v[178:181], v[210:213], v[40:43]
	v_mfma_f32_16x16x32_bf16 v[32:35], v[170:173], v[218:221], v[32:35]
	v_mfma_f32_16x16x32_bf16 v[24:27], v[178:181], v[218:221], v[24:27]
	v_mfma_f32_16x16x32_bf16 v[16:19], v[170:173], v[226:229], v[16:19]
	v_mfma_f32_16x16x32_bf16 v[8:11], v[178:181], v[226:229], v[8:11]
	v_mfma_f32_16x16x32_bf16 v[60:63], v[174:177], v[206:209], v[60:63]
	v_mfma_f32_16x16x32_bf16 v[56:59], v[182:185], v[206:209], v[56:59]
	v_mfma_f32_16x16x32_bf16 v[48:51], v[174:177], v[214:217], v[48:51]
	v_mfma_f32_16x16x32_bf16 v[40:43], v[182:185], v[214:217], v[40:43]
	v_mfma_f32_16x16x32_bf16 v[32:35], v[174:177], v[222:225], v[32:35]
	v_mfma_f32_16x16x32_bf16 v[24:27], v[182:185], v[222:225], v[24:27]
	v_mfma_f32_16x16x32_bf16 v[16:19], v[174:177], v[230:233], v[16:19]
	v_mfma_f32_16x16x32_bf16 v[8:11], v[182:185], v[230:233], v[8:11]
	v_mfma_f32_16x16x32_bf16 v[52:55], v[186:189], v[202:205], v[52:55]
	v_mfma_f32_16x16x32_bf16 v[44:47], v[194:197], v[202:205], v[44:47]
	v_mfma_f32_16x16x32_bf16 v[36:39], v[186:189], v[210:213], v[36:39]
	v_mfma_f32_16x16x32_bf16 v[28:31], v[194:197], v[210:213], v[28:31]
	v_mfma_f32_16x16x32_bf16 v[20:23], v[186:189], v[218:221], v[20:23]
	v_mfma_f32_16x16x32_bf16 v[12:15], v[194:197], v[218:221], v[12:15]
	v_mfma_f32_16x16x32_bf16 v[4:7], v[186:189], v[226:229], v[4:7]
	v_mfma_f32_16x16x32_bf16 v[0:3], v[194:197], v[226:229], v[0:3]
	v_mfma_f32_16x16x32_bf16 v[52:55], v[190:193], v[206:209], v[52:55]
	v_mfma_f32_16x16x32_bf16 v[44:47], v[198:201], v[206:209], v[44:47]
	v_mfma_f32_16x16x32_bf16 v[36:39], v[190:193], v[214:217], v[36:39]
	v_mfma_f32_16x16x32_bf16 v[28:31], v[198:201], v[214:217], v[28:31]
	v_mfma_f32_16x16x32_bf16 v[20:23], v[190:193], v[222:225], v[20:23]
	v_mfma_f32_16x16x32_bf16 v[12:15], v[198:201], v[222:225], v[12:15]
	v_mfma_f32_16x16x32_bf16 v[4:7], v[190:193], v[230:233], v[4:7]
	v_mfma_f32_16x16x32_bf16 v[0:3], v[198:201], v[230:233], v[0:3]
	s_barrier
	s_add_i32 s64, 0, 0x18000
	v_add_u32_e32 v136, s64, v149
	s_add_i32 s65, 0, 0x1c000
	ds_read_b128 v[170:173], v136
	ds_read_b128 v[174:177], v136 offset:1024
	ds_read_b128 v[178:181], v136 offset:2048
	ds_read_b128 v[182:185], v136 offset:3072
	v_add_u32_e32 v136, s65, v149
	ds_read_b128 v[186:189], v136
	ds_read_b128 v[190:193], v136 offset:1024
	ds_read_b128 v[194:197], v136 offset:2048
	ds_read_b128 v[198:201], v136 offset:3072
	s_add_u32 s30, s40, 0x40000
	s_addc_u32 s31, s41, 0
	s_mov_b32 m0, s55
	v_lshl_add_u64 v[166:167], s[30:31], 0, v[134:135]
	ds_read_b128 v[202:205], v169 offset:32768
	ds_read_b128 v[206:209], v169 offset:33792
	ds_read_b128 v[210:213], v169 offset:34816
	ds_read_b128 v[214:217], v169 offset:35840
	ds_read_b128 v[218:221], v169 offset:36864
	ds_read_b128 v[222:225], v169 offset:37888
	ds_read_b128 v[226:229], v169 offset:38912
	ds_read_b128 v[230:233], v169 offset:39936
	global_load_lds_dwordx4 v[166:167], off
	v_lshl_add_u64 v[166:167], s[30:31], 0, v[130:131]
	s_mov_b32 m0, s56
	s_nop 0
	global_load_lds_dwordx4 v[166:167], off
	s_waitcnt vmcnt(8)
	s_waitcnt lgkmcnt(0)
	s_barrier
	s_waitcnt lgkmcnt(0)
	v_mfma_f32_16x16x32_bf16 v[124:127], v[170:173], v[202:205], v[124:127]
	v_mfma_f32_16x16x32_bf16 v[120:123], v[178:181], v[202:205], v[120:123]
	v_mfma_f32_16x16x32_bf16 v[112:115], v[170:173], v[210:213], v[112:115]
	v_mfma_f32_16x16x32_bf16 v[104:107], v[178:181], v[210:213], v[104:107]
	v_mfma_f32_16x16x32_bf16 v[96:99], v[170:173], v[218:221], v[96:99]
	v_mfma_f32_16x16x32_bf16 v[88:91], v[178:181], v[218:221], v[88:91]
	v_mfma_f32_16x16x32_bf16 v[80:83], v[170:173], v[226:229], v[80:83]
	v_mfma_f32_16x16x32_bf16 v[72:75], v[178:181], v[226:229], v[72:75]
	v_mfma_f32_16x16x32_bf16 v[124:127], v[174:177], v[206:209], v[124:127]
	v_mfma_f32_16x16x32_bf16 v[120:123], v[182:185], v[206:209], v[120:123]
	v_mfma_f32_16x16x32_bf16 v[112:115], v[174:177], v[214:217], v[112:115]
	v_mfma_f32_16x16x32_bf16 v[104:107], v[182:185], v[214:217], v[104:107]
	v_mfma_f32_16x16x32_bf16 v[96:99], v[174:177], v[222:225], v[96:99]
	v_mfma_f32_16x16x32_bf16 v[88:91], v[182:185], v[222:225], v[88:91]
	v_mfma_f32_16x16x32_bf16 v[80:83], v[174:177], v[230:233], v[80:83]
	v_mfma_f32_16x16x32_bf16 v[72:75], v[182:185], v[230:233], v[72:75]
	v_mfma_f32_16x16x32_bf16 v[116:119], v[186:189], v[202:205], v[116:119]
	v_mfma_f32_16x16x32_bf16 v[108:111], v[194:197], v[202:205], v[108:111]
	v_mfma_f32_16x16x32_bf16 v[100:103], v[186:189], v[210:213], v[100:103]
	v_mfma_f32_16x16x32_bf16 v[92:95], v[194:197], v[210:213], v[92:95]
	v_mfma_f32_16x16x32_bf16 v[84:87], v[186:189], v[218:221], v[84:87]
	v_mfma_f32_16x16x32_bf16 v[76:79], v[194:197], v[218:221], v[76:79]
	v_mfma_f32_16x16x32_bf16 v[68:71], v[186:189], v[226:229], v[68:71]
	v_mfma_f32_16x16x32_bf16 v[64:67], v[194:197], v[226:229], v[64:67]
	v_mfma_f32_16x16x32_bf16 v[116:119], v[190:193], v[206:209], v[116:119]
	v_mfma_f32_16x16x32_bf16 v[108:111], v[198:201], v[206:209], v[108:111]
	v_mfma_f32_16x16x32_bf16 v[100:103], v[190:193], v[214:217], v[100:103]
	v_mfma_f32_16x16x32_bf16 v[92:95], v[198:201], v[214:217], v[92:95]
	v_mfma_f32_16x16x32_bf16 v[84:87], v[190:193], v[222:225], v[84:87]
	v_mfma_f32_16x16x32_bf16 v[76:79], v[198:201], v[222:225], v[76:79]
	v_mfma_f32_16x16x32_bf16 v[68:71], v[190:193], v[230:233], v[68:71]
	v_mfma_f32_16x16x32_bf16 v[64:67], v[198:201], v[230:233], v[64:67]
	s_barrier
	s_add_i32 s30, s64, s50
	v_lshl_add_u64 v[150:151], v[150:151], 0, s[16:17]
	s_mov_b32 m0, s30
	ds_read_b128 v[202:205], v169 offset:49152
	ds_read_b128 v[206:209], v169 offset:50176
	ds_read_b128 v[210:213], v169 offset:51200
	ds_read_b128 v[214:217], v169 offset:52224
	ds_read_b128 v[218:221], v169 offset:53248
	ds_read_b128 v[222:225], v169 offset:54272
	ds_read_b128 v[226:229], v169 offset:55296
	ds_read_b128 v[230:233], v169 offset:56320
	global_load_lds_dwordx4 v[150:151], off
	s_add_i32 m0, s30, 0x2000
	s_add_u32 s30, s38, 0x40080
	v_lshl_add_u64 v[150:151], v[154:155], 0, s[16:17]
	s_addc_u32 s31, s39, 0
	s_add_i32 s38, s65, s50
	global_load_lds_dwordx4 v[150:151], off
	v_lshl_add_u64 v[150:151], s[30:31], 0, v[132:133]
	s_mov_b32 m0, s38
	s_nop 0
	global_load_lds_dwordx4 v[150:151], off
	v_lshl_add_u64 v[150:151], s[30:31], 0, v[128:129]
	s_add_i32 m0, s38, 0x2000
	s_nop 0
	global_load_lds_dwordx4 v[150:151], off
	v_lshl_add_u64 v[150:151], v[158:159], 0, s[16:17]
	s_mov_b32 m0, s57
	s_nop 0
	global_load_lds_dwordx4 v[150:151], off
	v_lshl_add_u64 v[150:151], v[162:163], 0, s[16:17]
	s_mov_b32 m0, s58
	s_nop 0
	global_load_lds_dwordx4 v[150:151], off
	s_waitcnt vmcnt(8)
	s_waitcnt lgkmcnt(0)
	s_barrier
	s_waitcnt lgkmcnt(0)
	v_mfma_f32_16x16x32_bf16 v[60:63], v[170:173], v[202:205], v[60:63]
	v_mfma_f32_16x16x32_bf16 v[56:59], v[178:181], v[202:205], v[56:59]
	v_mfma_f32_16x16x32_bf16 v[48:51], v[170:173], v[210:213], v[48:51]
	v_mfma_f32_16x16x32_bf16 v[40:43], v[178:181], v[210:213], v[40:43]
	v_mfma_f32_16x16x32_bf16 v[32:35], v[170:173], v[218:221], v[32:35]
	v_mfma_f32_16x16x32_bf16 v[24:27], v[178:181], v[218:221], v[24:27]
	v_mfma_f32_16x16x32_bf16 v[16:19], v[170:173], v[226:229], v[16:19]
	v_mfma_f32_16x16x32_bf16 v[8:11], v[178:181], v[226:229], v[8:11]
	v_mfma_f32_16x16x32_bf16 v[60:63], v[174:177], v[206:209], v[60:63]
	v_mfma_f32_16x16x32_bf16 v[56:59], v[182:185], v[206:209], v[56:59]
	v_mfma_f32_16x16x32_bf16 v[48:51], v[174:177], v[214:217], v[48:51]
	v_mfma_f32_16x16x32_bf16 v[40:43], v[182:185], v[214:217], v[40:43]
	v_mfma_f32_16x16x32_bf16 v[32:35], v[174:177], v[222:225], v[32:35]
	v_mfma_f32_16x16x32_bf16 v[24:27], v[182:185], v[222:225], v[24:27]
	v_mfma_f32_16x16x32_bf16 v[16:19], v[174:177], v[230:233], v[16:19]
	v_mfma_f32_16x16x32_bf16 v[8:11], v[182:185], v[230:233], v[8:11]
	v_mfma_f32_16x16x32_bf16 v[52:55], v[186:189], v[202:205], v[52:55]
	v_mfma_f32_16x16x32_bf16 v[44:47], v[194:197], v[202:205], v[44:47]
	v_mfma_f32_16x16x32_bf16 v[36:39], v[186:189], v[210:213], v[36:39]
	v_mfma_f32_16x16x32_bf16 v[28:31], v[194:197], v[210:213], v[28:31]
	v_mfma_f32_16x16x32_bf16 v[20:23], v[186:189], v[218:221], v[20:23]
	v_mfma_f32_16x16x32_bf16 v[12:15], v[194:197], v[218:221], v[12:15]
	v_mfma_f32_16x16x32_bf16 v[4:7], v[186:189], v[226:229], v[4:7]
	v_mfma_f32_16x16x32_bf16 v[0:3], v[194:197], v[226:229], v[0:3]
	v_mfma_f32_16x16x32_bf16 v[52:55], v[190:193], v[206:209], v[52:55]
	v_mfma_f32_16x16x32_bf16 v[44:47], v[198:201], v[206:209], v[44:47]
	v_mfma_f32_16x16x32_bf16 v[36:39], v[190:193], v[214:217], v[36:39]
	v_mfma_f32_16x16x32_bf16 v[28:31], v[198:201], v[214:217], v[28:31]
	v_mfma_f32_16x16x32_bf16 v[20:23], v[190:193], v[222:225], v[20:23]
	v_mfma_f32_16x16x32_bf16 v[12:15], v[198:201], v[222:225], v[12:15]
	v_mfma_f32_16x16x32_bf16 v[4:7], v[190:193], v[230:233], v[4:7]
	v_mfma_f32_16x16x32_bf16 v[0:3], v[198:201], v[230:233], v[0:3]
	s_barrier
	s_add_i32 s29, s29, 2
	s_add_u32 s21, s21, 0x100
	s_addc_u32 s23, s23, 0
	s_cmp_gt_u32 s29, 13
	s_mov_b64 s[30:31], s[36:37]
	s_cbranch_scc0 .LBB0_259
	s_and_b64 vcc, exec, s[18:19]
	s_cbranch_vccz .LBB0_262
	s_barrier

.LBB0_430:
	ds_read_b128 v[112:115], v245
	ds_read_b128 v[116:119], v245 offset:1024
	ds_read_b128 v[124:127], v245 offset:2048
	ds_read_b128 v[128:131], v245 offset:3072
	ds_read_b128 v[136:139], v246
	ds_read_b128 v[140:143], v246 offset:1024
	ds_read_b128 v[148:151], v246 offset:2048
	ds_read_b128 v[156:159], v246 offset:3072
	s_add_u32 s36, s30, 0x100
	s_addc_u32 s37, s31, 0
	s_cmp_eq_u32 s64, 12
	s_cselect_b32 s41, s27, s37
	s_cselect_b32 s40, s26, s36
	s_cselect_b32 s39, s29, s25
	s_cselect_b32 s38, s28, s23
	v_lshl_add_u64 v[208:209], s[30:31], 0, v[202:203]
	s_add_i32 m0, s51, 0xc000
	ds_read_b128 v[160:163], v247
	ds_read_b128 v[164:167], v247 offset:1024
	ds_read_b128 v[168:171], v247 offset:2048
	ds_read_b128 v[172:175], v247 offset:3072
	ds_read_b128 v[176:179], v247 offset:4096
	ds_read_b128 v[180:183], v247 offset:5120
	ds_read_b128 v[184:187], v247 offset:6144
	ds_read_b128 v[188:191], v247 offset:7168
	global_load_lds_dwordx4 v[208:209], off
	v_lshl_add_u64 v[208:209], s[30:31], 0, v[200:201]
	s_add_i32 m0, s51, 0xe000
	s_nop 0
	global_load_lds_dwordx4 v[208:209], off
	s_waitcnt vmcnt(8)
	s_waitcnt lgkmcnt(0)
	s_barrier
	s_waitcnt lgkmcnt(0)
	v_mfma_f32_16x16x32_bf16 v[152:155], v[112:115], v[160:163], v[152:155]
	v_mfma_f32_16x16x32_bf16 v[144:147], v[124:127], v[160:163], v[144:147]
	v_mfma_f32_16x16x32_bf16 v[108:111], v[112:115], v[168:171], v[108:111]
	v_mfma_f32_16x16x32_bf16 v[104:107], v[124:127], v[168:171], v[104:107]
	v_mfma_f32_16x16x32_bf16 v[92:95], v[112:115], v[176:179], v[92:95]
	v_mfma_f32_16x16x32_bf16 v[88:91], v[124:127], v[176:179], v[88:91]
	v_mfma_f32_16x16x32_bf16 v[76:79], v[112:115], v[184:187], v[76:79]
	v_mfma_f32_16x16x32_bf16 v[72:75], v[124:127], v[184:187], v[72:75]
	v_mfma_f32_16x16x32_bf16 v[152:155], v[116:119], v[164:167], v[152:155]
	v_mfma_f32_16x16x32_bf16 v[144:147], v[128:131], v[164:167], v[144:147]
	v_mfma_f32_16x16x32_bf16 v[108:111], v[116:119], v[172:175], v[108:111]
	v_mfma_f32_16x16x32_bf16 v[104:107], v[128:131], v[172:175], v[104:107]
	v_mfma_f32_16x16x32_bf16 v[92:95], v[116:119], v[180:183], v[92:95]
	v_mfma_f32_16x16x32_bf16 v[88:91], v[128:131], v[180:183], v[88:91]
	v_mfma_f32_16x16x32_bf16 v[76:79], v[116:119], v[188:191], v[76:79]
	v_mfma_f32_16x16x32_bf16 v[72:75], v[128:131], v[188:191], v[72:75]
	v_mfma_f32_16x16x32_bf16 v[132:135], v[136:139], v[160:163], v[132:135]
	v_mfma_f32_16x16x32_bf16 v[120:123], v[148:151], v[160:163], v[120:123]
	v_mfma_f32_16x16x32_bf16 v[100:103], v[136:139], v[168:171], v[100:103]
	v_mfma_f32_16x16x32_bf16 v[96:99], v[148:151], v[168:171], v[96:99]
	v_mfma_f32_16x16x32_bf16 v[84:87], v[136:139], v[176:179], v[84:87]
	v_mfma_f32_16x16x32_bf16 v[80:83], v[148:151], v[176:179], v[80:83]
	v_mfma_f32_16x16x32_bf16 v[68:71], v[136:139], v[184:187], v[68:71]
	v_mfma_f32_16x16x32_bf16 v[64:67], v[148:151], v[184:187], v[64:67]
	v_mfma_f32_16x16x32_bf16 v[132:135], v[140:143], v[164:167], v[132:135]
	v_mfma_f32_16x16x32_bf16 v[120:123], v[156:159], v[164:167], v[120:123]
	v_mfma_f32_16x16x32_bf16 v[100:103], v[140:143], v[172:175], v[100:103]
	v_mfma_f32_16x16x32_bf16 v[96:99], v[156:159], v[172:175], v[96:99]
	v_mfma_f32_16x16x32_bf16 v[84:87], v[140:143], v[180:183], v[84:87]
	v_mfma_f32_16x16x32_bf16 v[80:83], v[156:159], v[180:183], v[80:83]
	v_mfma_f32_16x16x32_bf16 v[68:71], v[140:143], v[188:191], v[68:71]
	v_mfma_f32_16x16x32_bf16 v[64:67], v[156:159], v[188:191], v[64:67]
	s_barrier
	s_add_i32 s30, s60, s50
	v_lshl_add_u64 v[208:209], s[38:39], 0, v[194:195]
	s_mov_b32 m0, s30
	ds_read_b128 v[160:163], v247 offset:16384
	ds_read_b128 v[164:167], v247 offset:17408
	ds_read_b128 v[168:171], v247 offset:18432
	ds_read_b128 v[172:175], v247 offset:19456
	ds_read_b128 v[176:179], v247 offset:20480
	ds_read_b128 v[180:183], v247 offset:21504
	ds_read_b128 v[184:187], v247 offset:22528
	ds_read_b128 v[188:191], v247 offset:23552
	global_load_lds_dwordx4 v[208:209], off
	s_add_i32 m0, s30, 0x2000
	s_add_u32 s30, s38, 0x40000
	v_lshl_add_u64 v[210:211], s[38:39], 0, v[198:199]
	s_addc_u32 s31, s39, 0
	s_add_i32 s65, s61, s50
	global_load_lds_dwordx4 v[210:211], off
	v_lshl_add_u64 v[212:213], s[30:31], 0, v[194:195]
	s_mov_b32 m0, s65
	v_lshl_add_u64 v[214:215], s[40:41], 0, v[196:197]
	global_load_lds_dwordx4 v[212:213], off
	v_lshl_add_u64 v[212:213], s[30:31], 0, v[198:199]
	s_add_i32 m0, s65, 0x2000
	s_nop 0
	global_load_lds_dwordx4 v[212:213], off
	v_lshl_add_u64 v[212:213], s[40:41], 0, v[192:193]
	s_mov_b32 m0, s51
	s_nop 0
	global_load_lds_dwordx4 v[212:213], off
	s_mov_b32 m0, s52
	s_nop 0
	global_load_lds_dwordx4 v[214:215], off
	s_waitcnt vmcnt(8)
	s_waitcnt lgkmcnt(0)
	s_barrier
	s_waitcnt lgkmcnt(0)
	v_mfma_f32_16x16x32_bf16 v[60:63], v[112:115], v[160:163], v[60:63]
	v_mfma_f32_16x16x32_bf16 v[56:59], v[124:127], v[160:163], v[56:59]
	v_mfma_f32_16x16x32_bf16 v[44:47], v[112:115], v[168:171], v[44:47]
	v_mfma_f32_16x16x32_bf16 v[40:43], v[124:127], v[168:171], v[40:43]
	v_mfma_f32_16x16x32_bf16 v[28:31], v[112:115], v[176:179], v[28:31]
	v_mfma_f32_16x16x32_bf16 v[24:27], v[124:127], v[176:179], v[24:27]
	v_mfma_f32_16x16x32_bf16 v[12:15], v[112:115], v[184:187], v[12:15]
	v_mfma_f32_16x16x32_bf16 v[8:11], v[124:127], v[184:187], v[8:11]
	v_mfma_f32_16x16x32_bf16 v[60:63], v[116:119], v[164:167], v[60:63]
	v_mfma_f32_16x16x32_bf16 v[56:59], v[128:131], v[164:167], v[56:59]
	v_mfma_f32_16x16x32_bf16 v[44:47], v[116:119], v[172:175], v[44:47]
	v_mfma_f32_16x16x32_bf16 v[40:43], v[128:131], v[172:175], v[40:43]
	v_mfma_f32_16x16x32_bf16 v[28:31], v[116:119], v[180:183], v[28:31]
	v_mfma_f32_16x16x32_bf16 v[24:27], v[128:131], v[180:183], v[24:27]
	v_mfma_f32_16x16x32_bf16 v[12:15], v[116:119], v[188:191], v[12:15]
	v_mfma_f32_16x16x32_bf16 v[8:11], v[128:131], v[188:191], v[8:11]
	v_mfma_f32_16x16x32_bf16 v[52:55], v[136:139], v[160:163], v[52:55]
	v_mfma_f32_16x16x32_bf16 v[48:51], v[148:151], v[160:163], v[48:51]
	v_mfma_f32_16x16x32_bf16 v[36:39], v[136:139], v[168:171], v[36:39]
	v_mfma_f32_16x16x32_bf16 v[32:35], v[148:151], v[168:171], v[32:35]
	v_mfma_f32_16x16x32_bf16 v[20:23], v[136:139], v[176:179], v[20:23]
	v_mfma_f32_16x16x32_bf16 v[16:19], v[148:151], v[176:179], v[16:19]
	v_mfma_f32_16x16x32_bf16 v[4:7], v[136:139], v[184:187], v[4:7]
	v_mfma_f32_16x16x32_bf16 v[0:3], v[148:151], v[184:187], v[0:3]
	v_mfma_f32_16x16x32_bf16 v[52:55], v[140:143], v[164:167], v[52:55]
	v_mfma_f32_16x16x32_bf16 v[48:51], v[156:159], v[164:167], v[48:51]
	v_mfma_f32_16x16x32_bf16 v[36:39], v[140:143], v[172:175], v[36:39]
	v_mfma_f32_16x16x32_bf16 v[32:35], v[156:159], v[172:175], v[32:35]
	v_mfma_f32_16x16x32_bf16 v[20:23], v[140:143], v[180:183], v[20:23]
	v_mfma_f32_16x16x32_bf16 v[16:19], v[156:159], v[180:183], v[16:19]
	v_mfma_f32_16x16x32_bf16 v[4:7], v[140:143], v[188:191], v[4:7]
	v_mfma_f32_16x16x32_bf16 v[0:3], v[156:159], v[188:191], v[0:3]
	s_barrier
	s_add_i32 s65, 0, 0x18000
	s_add_i32 s66, 0, 0x1c000
	v_add_u32_e32 v128, s65, v241
	v_add_u32_e32 v156, s66, v241
	ds_read_b128 v[112:115], v128
	ds_read_b128 v[116:119], v128 offset:1024
	ds_read_b128 v[124:127], v128 offset:2048
	ds_read_b128 v[128:131], v128 offset:3072
	ds_read_b128 v[136:139], v156
	ds_read_b128 v[140:143], v156 offset:1024
	ds_read_b128 v[148:151], v156 offset:2048
	ds_read_b128 v[156:159], v156 offset:3072
	s_add_u32 s30, s40, 0x40000
	s_addc_u32 s31, s41, 0
	s_mov_b32 m0, s53
	v_lshl_add_u64 v[216:217], s[30:31], 0, v[192:193]
	ds_read_b128 v[160:163], v247 offset:32768
	ds_read_b128 v[164:167], v247 offset:33792
	ds_read_b128 v[168:171], v247 offset:34816
	ds_read_b128 v[172:175], v247 offset:35840
	ds_read_b128 v[176:179], v247 offset:36864
	ds_read_b128 v[180:183], v247 offset:37888
	ds_read_b128 v[184:187], v247 offset:38912
	ds_read_b128 v[188:191], v247 offset:39936
	global_load_lds_dwordx4 v[216:217], off
	v_lshl_add_u64 v[216:217], s[30:31], 0, v[196:197]
	s_mov_b32 m0, s54
	s_nop 0
	global_load_lds_dwordx4 v[216:217], off
	s_waitcnt vmcnt(8)
	s_waitcnt lgkmcnt(0)
	s_barrier
	s_waitcnt lgkmcnt(0)
	v_mfma_f32_16x16x32_bf16 v[152:155], v[112:115], v[160:163], v[152:155]
	v_mfma_f32_16x16x32_bf16 v[144:147], v[124:127], v[160:163], v[144:147]
	v_mfma_f32_16x16x32_bf16 v[108:111], v[112:115], v[168:171], v[108:111]
	v_mfma_f32_16x16x32_bf16 v[104:107], v[124:127], v[168:171], v[104:107]
	v_mfma_f32_16x16x32_bf16 v[92:95], v[112:115], v[176:179], v[92:95]
	v_mfma_f32_16x16x32_bf16 v[88:91], v[124:127], v[176:179], v[88:91]
	v_mfma_f32_16x16x32_bf16 v[76:79], v[112:115], v[184:187], v[76:79]
	v_mfma_f32_16x16x32_bf16 v[72:75], v[124:127], v[184:187], v[72:75]
	v_mfma_f32_16x16x32_bf16 v[152:155], v[116:119], v[164:167], v[152:155]
	v_mfma_f32_16x16x32_bf16 v[144:147], v[128:131], v[164:167], v[144:147]
	v_mfma_f32_16x16x32_bf16 v[108:111], v[116:119], v[172:175], v[108:111]
	v_mfma_f32_16x16x32_bf16 v[104:107], v[128:131], v[172:175], v[104:107]
	v_mfma_f32_16x16x32_bf16 v[92:95], v[116:119], v[180:183], v[92:95]
	v_mfma_f32_16x16x32_bf16 v[88:91], v[128:131], v[180:183], v[88:91]
	v_mfma_f32_16x16x32_bf16 v[76:79], v[116:119], v[188:191], v[76:79]
	v_mfma_f32_16x16x32_bf16 v[72:75], v[128:131], v[188:191], v[72:75]
	v_mfma_f32_16x16x32_bf16 v[132:135], v[136:139], v[160:163], v[132:135]
	v_mfma_f32_16x16x32_bf16 v[120:123], v[148:151], v[160:163], v[120:123]
	v_mfma_f32_16x16x32_bf16 v[100:103], v[136:139], v[168:171], v[100:103]
	v_mfma_f32_16x16x32_bf16 v[96:99], v[148:151], v[168:171], v[96:99]
	v_mfma_f32_16x16x32_bf16 v[84:87], v[136:139], v[176:179], v[84:87]
	v_mfma_f32_16x16x32_bf16 v[80:83], v[148:151], v[176:179], v[80:83]
	v_mfma_f32_16x16x32_bf16 v[68:71], v[136:139], v[184:187], v[68:71]
	v_mfma_f32_16x16x32_bf16 v[64:67], v[148:151], v[184:187], v[64:67]
	v_mfma_f32_16x16x32_bf16 v[132:135], v[140:143], v[164:167], v[132:135]
	v_mfma_f32_16x16x32_bf16 v[120:123], v[156:159], v[164:167], v[120:123]
	v_mfma_f32_16x16x32_bf16 v[100:103], v[140:143], v[172:175], v[100:103]
	v_mfma_f32_16x16x32_bf16 v[96:99], v[156:159], v[172:175], v[96:99]
	v_mfma_f32_16x16x32_bf16 v[84:87], v[140:143], v[180:183], v[84:87]
	v_mfma_f32_16x16x32_bf16 v[80:83], v[156:159], v[180:183], v[80:83]
	v_mfma_f32_16x16x32_bf16 v[68:71], v[140:143], v[188:191], v[68:71]
	v_mfma_f32_16x16x32_bf16 v[64:67], v[156:159], v[188:191], v[64:67]
	s_barrier
	s_add_i32 s30, s65, s50
	v_lshl_add_u64 v[208:209], v[208:209], 0, s[18:19]
	s_mov_b32 m0, s30
	ds_read_b128 v[160:163], v247 offset:49152
	ds_read_b128 v[164:167], v247 offset:50176
	ds_read_b128 v[168:171], v247 offset:51200
	ds_read_b128 v[172:175], v247 offset:52224
	ds_read_b128 v[176:179], v247 offset:53248
	ds_read_b128 v[180:183], v247 offset:54272
	ds_read_b128 v[184:187], v247 offset:55296
	ds_read_b128 v[188:191], v247 offset:56320
	global_load_lds_dwordx4 v[208:209], off
	s_add_i32 m0, s30, 0x2000
	s_add_u32 s30, s38, 0x40080
	v_lshl_add_u64 v[208:209], v[210:211], 0, s[18:19]
	s_addc_u32 s31, s39, 0
	s_add_i32 s38, s66, s50
	global_load_lds_dwordx4 v[208:209], off
	v_lshl_add_u64 v[208:209], s[30:31], 0, v[194:195]
	s_mov_b32 m0, s38
	s_nop 0
	global_load_lds_dwordx4 v[208:209], off
	v_lshl_add_u64 v[208:209], s[30:31], 0, v[198:199]
	s_add_i32 m0, s38, 0x2000
	s_nop 0
	global_load_lds_dwordx4 v[208:209], off
	v_lshl_add_u64 v[208:209], v[212:213], 0, s[18:19]
	s_mov_b32 m0, s56
	s_nop 0
	global_load_lds_dwordx4 v[208:209], off
	v_lshl_add_u64 v[208:209], v[214:215], 0, s[18:19]
	s_mov_b32 m0, s57
	s_nop 0
	global_load_lds_dwordx4 v[208:209], off
	s_waitcnt vmcnt(8)
	s_waitcnt lgkmcnt(0)
	s_barrier
	s_waitcnt lgkmcnt(0)
	v_mfma_f32_16x16x32_bf16 v[60:63], v[112:115], v[160:163], v[60:63]
	v_mfma_f32_16x16x32_bf16 v[56:59], v[124:127], v[160:163], v[56:59]
	v_mfma_f32_16x16x32_bf16 v[44:47], v[112:115], v[168:171], v[44:47]
	v_mfma_f32_16x16x32_bf16 v[40:43], v[124:127], v[168:171], v[40:43]
	v_mfma_f32_16x16x32_bf16 v[28:31], v[112:115], v[176:179], v[28:31]
	v_mfma_f32_16x16x32_bf16 v[24:27], v[124:127], v[176:179], v[24:27]
	v_mfma_f32_16x16x32_bf16 v[12:15], v[112:115], v[184:187], v[12:15]
	v_mfma_f32_16x16x32_bf16 v[8:11], v[124:127], v[184:187], v[8:11]
	v_mfma_f32_16x16x32_bf16 v[60:63], v[116:119], v[164:167], v[60:63]
	v_mfma_f32_16x16x32_bf16 v[56:59], v[128:131], v[164:167], v[56:59]
	v_mfma_f32_16x16x32_bf16 v[44:47], v[116:119], v[172:175], v[44:47]
	v_mfma_f32_16x16x32_bf16 v[40:43], v[128:131], v[172:175], v[40:43]
	v_mfma_f32_16x16x32_bf16 v[28:31], v[116:119], v[180:183], v[28:31]
	v_mfma_f32_16x16x32_bf16 v[24:27], v[128:131], v[180:183], v[24:27]
	v_mfma_f32_16x16x32_bf16 v[12:15], v[116:119], v[188:191], v[12:15]
	v_mfma_f32_16x16x32_bf16 v[8:11], v[128:131], v[188:191], v[8:11]
	v_mfma_f32_16x16x32_bf16 v[52:55], v[136:139], v[160:163], v[52:55]
	v_mfma_f32_16x16x32_bf16 v[48:51], v[148:151], v[160:163], v[48:51]
	v_mfma_f32_16x16x32_bf16 v[36:39], v[136:139], v[168:171], v[36:39]
	v_mfma_f32_16x16x32_bf16 v[32:35], v[148:151], v[168:171], v[32:35]
	v_mfma_f32_16x16x32_bf16 v[20:23], v[136:139], v[176:179], v[20:23]
	v_mfma_f32_16x16x32_bf16 v[16:19], v[148:151], v[176:179], v[16:19]
	v_mfma_f32_16x16x32_bf16 v[4:7], v[136:139], v[184:187], v[4:7]
	v_mfma_f32_16x16x32_bf16 v[0:3], v[148:151], v[184:187], v[0:3]
	v_mfma_f32_16x16x32_bf16 v[52:55], v[140:143], v[164:167], v[52:55]
	v_mfma_f32_16x16x32_bf16 v[48:51], v[156:159], v[164:167], v[48:51]
	v_mfma_f32_16x16x32_bf16 v[36:39], v[140:143], v[172:175], v[36:39]
	v_mfma_f32_16x16x32_bf16 v[32:35], v[156:159], v[172:175], v[32:35]
	v_mfma_f32_16x16x32_bf16 v[20:23], v[140:143], v[180:183], v[20:23]
	v_mfma_f32_16x16x32_bf16 v[16:19], v[156:159], v[180:183], v[16:19]
	v_mfma_f32_16x16x32_bf16 v[4:7], v[140:143], v[188:191], v[4:7]
	v_mfma_f32_16x16x32_bf16 v[0:3], v[156:159], v[188:191], v[0:3]
	s_barrier
	s_add_i32 s64, s64, 2
	s_add_u32 s23, s23, 0x100
	s_addc_u32 s25, s25, 0
	s_cmp_gt_u32 s64, 13
	s_mov_b64 s[30:31], s[36:37]
	s_cbranch_scc0 .LBB0_430
	s_and_b64 vcc, exec, s[20:21]
	s_cbranch_vccz .LBB0_433
	s_barrier

.LBB0_545:
	v_add_u32_e32 v85, s63, v83
	s_add_u32 s38, s22, s36
	ds_read_b128 v[86:89], v85
	ds_read_b128 v[90:93], v85 offset:1024
	ds_read_b128 v[94:97], v85 offset:2048
	ds_read_b128 v[98:101], v85 offset:3072
	s_addc_u32 s39, s23, s37
	s_add_u32 s38, s38, 0x100
	s_addc_u32 s39, s39, 0
	s_add_u32 s68, s21, s36
	s_addc_u32 s69, s66, s37
	s_cmpk_eq_i32 s36, 0x700
	s_cselect_b32 s41, s25, s39
	s_cselect_b32 s40, s24, s38
	s_cselect_b32 s39, s27, s69
	s_cselect_b32 s38, s26, s68
	v_lshl_add_u64 v[134:135], v[78:79], 0, s[36:37]
	s_add_i32 m0, s9, 0xc000
	ds_read_b128 v[102:105], v84
	ds_read_b128 v[106:109], v84 offset:1024
	ds_read_b128 v[110:113], v84 offset:2048
	ds_read_b128 v[114:117], v84 offset:3072
	ds_read_b128 v[118:121], v84 offset:4096
	ds_read_b128 v[122:125], v84 offset:5120
	ds_read_b128 v[126:129], v84 offset:6144
	ds_read_b128 v[130:133], v84 offset:7168
	global_load_lds_dwordx4 v[134:135], off
	v_lshl_add_u64 v[134:135], v[76:77], 0, s[36:37]
	s_add_i32 m0, s9, 0xe000
	s_nop 0
	global_load_lds_dwordx4 v[134:135], off
	s_waitcnt vmcnt(8)
	s_waitcnt lgkmcnt(0)
	s_barrier
	s_waitcnt lgkmcnt(0)
	v_mfma_f32_16x16x32_bf16 v[60:63], v[86:89], v[102:105], v[60:63]
	v_mfma_f32_16x16x32_bf16 v[56:59], v[94:97], v[102:105], v[56:59]
	v_mfma_f32_16x16x32_bf16 v[52:55], v[86:89], v[110:113], v[52:55]
	v_mfma_f32_16x16x32_bf16 v[48:51], v[94:97], v[110:113], v[48:51]
	v_mfma_f32_16x16x32_bf16 v[44:47], v[86:89], v[118:121], v[44:47]
	v_mfma_f32_16x16x32_bf16 v[40:43], v[94:97], v[118:121], v[40:43]
	v_mfma_f32_16x16x32_bf16 v[36:39], v[86:89], v[126:129], v[36:39]
	v_mfma_f32_16x16x32_bf16 v[32:35], v[94:97], v[126:129], v[32:35]
	v_mfma_f32_16x16x32_bf16 v[60:63], v[90:93], v[106:109], v[60:63]
	v_mfma_f32_16x16x32_bf16 v[56:59], v[98:101], v[106:109], v[56:59]
	v_mfma_f32_16x16x32_bf16 v[52:55], v[90:93], v[114:117], v[52:55]
	v_mfma_f32_16x16x32_bf16 v[48:51], v[98:101], v[114:117], v[48:51]
	v_mfma_f32_16x16x32_bf16 v[44:47], v[90:93], v[122:125], v[44:47]
	v_mfma_f32_16x16x32_bf16 v[40:43], v[98:101], v[122:125], v[40:43]
	v_mfma_f32_16x16x32_bf16 v[36:39], v[90:93], v[130:133], v[36:39]
	v_mfma_f32_16x16x32_bf16 v[32:35], v[98:101], v[130:133], v[32:35]
	s_barrier
	s_add_i32 s68, s63, s50
	v_lshl_add_u64 v[134:135], s[38:39], 0, v[64:65]
	s_mov_b32 m0, s68
	ds_read_b128 v[102:105], v84 offset:16384
	ds_read_b128 v[106:109], v84 offset:17408
	ds_read_b128 v[110:113], v84 offset:18432
	ds_read_b128 v[114:117], v84 offset:19456
	ds_read_b128 v[118:121], v84 offset:20480
	ds_read_b128 v[122:125], v84 offset:21504
	ds_read_b128 v[126:129], v84 offset:22528
	ds_read_b128 v[130:133], v84 offset:23552
	global_load_lds_dwordx4 v[134:135], off
	s_add_i32 m0, s68, 0x2000
	s_add_u32 s68, s38, 0x40000
	v_lshl_add_u64 v[136:137], s[38:39], 0, v[66:67]
	s_addc_u32 s69, s39, 0
	global_load_lds_dwordx4 v[136:137], off
	v_lshl_add_u64 v[138:139], s[68:69], 0, v[64:65]
	s_mov_b32 m0, s53
	v_lshl_add_u64 v[140:141], s[40:41], 0, v[66:67]
	global_load_lds_dwordx4 v[138:139], off
	v_lshl_add_u64 v[138:139], s[68:69], 0, v[66:67]
	s_mov_b32 m0, s54
	s_nop 0
	global_load_lds_dwordx4 v[138:139], off
	v_lshl_add_u64 v[138:139], s[40:41], 0, v[64:65]
	s_mov_b32 m0, s9
	s_nop 0
	global_load_lds_dwordx4 v[138:139], off
	s_mov_b32 m0, s56
	s_nop 0
	global_load_lds_dwordx4 v[140:141], off
	s_waitcnt vmcnt(8)
	s_waitcnt lgkmcnt(0)
	s_barrier
	s_waitcnt lgkmcnt(0)
	v_mfma_f32_16x16x32_bf16 v[28:31], v[86:89], v[102:105], v[28:31]
	v_mfma_f32_16x16x32_bf16 v[24:27], v[94:97], v[102:105], v[24:27]
	v_mfma_f32_16x16x32_bf16 v[20:23], v[86:89], v[110:113], v[20:23]
	v_mfma_f32_16x16x32_bf16 v[16:19], v[94:97], v[110:113], v[16:19]
	v_mfma_f32_16x16x32_bf16 v[12:15], v[86:89], v[118:121], v[12:15]
	v_mfma_f32_16x16x32_bf16 v[8:11], v[94:97], v[118:121], v[8:11]
	v_mfma_f32_16x16x32_bf16 v[4:7], v[86:89], v[126:129], v[4:7]
	v_mfma_f32_16x16x32_bf16 v[0:3], v[94:97], v[126:129], v[0:3]
	v_mfma_f32_16x16x32_bf16 v[28:31], v[90:93], v[106:109], v[28:31]
	v_mfma_f32_16x16x32_bf16 v[24:27], v[98:101], v[106:109], v[24:27]
	v_mfma_f32_16x16x32_bf16 v[20:23], v[90:93], v[114:117], v[20:23]
	v_mfma_f32_16x16x32_bf16 v[16:19], v[98:101], v[114:117], v[16:19]
	v_mfma_f32_16x16x32_bf16 v[12:15], v[90:93], v[122:125], v[12:15]
	v_mfma_f32_16x16x32_bf16 v[8:11], v[98:101], v[122:125], v[8:11]
	v_mfma_f32_16x16x32_bf16 v[4:7], v[90:93], v[130:133], v[4:7]
	v_mfma_f32_16x16x32_bf16 v[0:3], v[98:101], v[130:133], v[0:3]
	s_barrier
	s_add_i32 s68, 0, 0x18000
	v_add_u32_e32 v85, s68, v83
	ds_read_b128 v[86:89], v85
	ds_read_b128 v[90:93], v85 offset:1024
	ds_read_b128 v[94:97], v85 offset:2048
	ds_read_b128 v[98:101], v85 offset:3072
	s_add_u32 s40, s40, 0x40000
	s_addc_u32 s41, s41, 0
	s_mov_b32 m0, s57
	v_lshl_add_u64 v[142:143], s[40:41], 0, v[64:65]
	ds_read_b128 v[102:105], v84 offset:32768
	ds_read_b128 v[106:109], v84 offset:33792
	ds_read_b128 v[110:113], v84 offset:34816
	ds_read_b128 v[114:117], v84 offset:35840
	ds_read_b128 v[118:121], v84 offset:36864
	ds_read_b128 v[122:125], v84 offset:37888
	ds_read_b128 v[126:129], v84 offset:38912
	ds_read_b128 v[130:133], v84 offset:39936
	global_load_lds_dwordx4 v[142:143], off
	v_lshl_add_u64 v[142:143], s[40:41], 0, v[66:67]
	s_mov_b32 m0, s58
	s_nop 0
	global_load_lds_dwordx4 v[142:143], off
	s_waitcnt vmcnt(8)
	s_waitcnt lgkmcnt(0)
	s_barrier
	s_waitcnt lgkmcnt(0)
	v_mfma_f32_16x16x32_bf16 v[60:63], v[86:89], v[102:105], v[60:63]
	v_mfma_f32_16x16x32_bf16 v[56:59], v[94:97], v[102:105], v[56:59]
	v_mfma_f32_16x16x32_bf16 v[52:55], v[86:89], v[110:113], v[52:55]
	v_mfma_f32_16x16x32_bf16 v[48:51], v[94:97], v[110:113], v[48:51]
	v_mfma_f32_16x16x32_bf16 v[44:47], v[86:89], v[118:121], v[44:47]
	v_mfma_f32_16x16x32_bf16 v[40:43], v[94:97], v[118:121], v[40:43]
	v_mfma_f32_16x16x32_bf16 v[36:39], v[86:89], v[126:129], v[36:39]
	v_mfma_f32_16x16x32_bf16 v[32:35], v[94:97], v[126:129], v[32:35]
	v_mfma_f32_16x16x32_bf16 v[60:63], v[90:93], v[106:109], v[60:63]
	v_mfma_f32_16x16x32_bf16 v[56:59], v[98:101], v[106:109], v[56:59]
	v_mfma_f32_16x16x32_bf16 v[52:55], v[90:93], v[114:117], v[52:55]
	v_mfma_f32_16x16x32_bf16 v[48:51], v[98:101], v[114:117], v[48:51]
	v_mfma_f32_16x16x32_bf16 v[44:47], v[90:93], v[122:125], v[44:47]
	v_mfma_f32_16x16x32_bf16 v[40:43], v[98:101], v[122:125], v[40:43]
	v_mfma_f32_16x16x32_bf16 v[36:39], v[90:93], v[130:133], v[36:39]
	v_mfma_f32_16x16x32_bf16 v[32:35], v[98:101], v[130:133], v[32:35]
	s_barrier
	s_add_i32 s40, s68, s50
	v_lshl_add_u64 v[134:135], v[134:135], 0, s[16:17]
	s_mov_b32 m0, s40
	ds_read_b128 v[102:105], v84 offset:49152
	ds_read_b128 v[106:109], v84 offset:50176
	ds_read_b128 v[110:113], v84 offset:51200
	ds_read_b128 v[114:117], v84 offset:52224
	ds_read_b128 v[118:121], v84 offset:53248
	ds_read_b128 v[122:125], v84 offset:54272
	ds_read_b128 v[126:129], v84 offset:55296
	ds_read_b128 v[130:133], v84 offset:56320
	global_load_lds_dwordx4 v[134:135], off
	s_add_i32 m0, s40, 0x2000
	s_add_u32 s38, s38, 0x40080
	v_lshl_add_u64 v[134:135], v[136:137], 0, s[16:17]
	s_addc_u32 s39, s39, 0
	global_load_lds_dwordx4 v[134:135], off
	v_lshl_add_u64 v[134:135], s[38:39], 0, v[64:65]
	s_mov_b32 m0, s61
	s_nop 0
	global_load_lds_dwordx4 v[134:135], off
	v_lshl_add_u64 v[134:135], s[38:39], 0, v[66:67]
	s_mov_b32 m0, s62
	s_nop 0
	global_load_lds_dwordx4 v[134:135], off
	v_lshl_add_u64 v[134:135], v[138:139], 0, s[16:17]
	s_mov_b32 m0, s59
	s_nop 0
	global_load_lds_dwordx4 v[134:135], off
	v_lshl_add_u64 v[134:135], v[140:141], 0, s[16:17]
	s_mov_b32 m0, s60
	s_nop 0
	global_load_lds_dwordx4 v[134:135], off
	s_waitcnt vmcnt(8)
	s_waitcnt lgkmcnt(0)
	s_barrier
	s_waitcnt lgkmcnt(0)
	v_mfma_f32_16x16x32_bf16 v[28:31], v[86:89], v[102:105], v[28:31]
	v_mfma_f32_16x16x32_bf16 v[24:27], v[94:97], v[102:105], v[24:27]
	v_mfma_f32_16x16x32_bf16 v[20:23], v[86:89], v[110:113], v[20:23]
	v_mfma_f32_16x16x32_bf16 v[16:19], v[94:97], v[110:113], v[16:19]
	v_mfma_f32_16x16x32_bf16 v[12:15], v[86:89], v[118:121], v[12:15]
	v_mfma_f32_16x16x32_bf16 v[8:11], v[94:97], v[118:121], v[8:11]
	v_mfma_f32_16x16x32_bf16 v[4:7], v[86:89], v[126:129], v[4:7]
	v_mfma_f32_16x16x32_bf16 v[0:3], v[94:97], v[126:129], v[0:3]
	v_mfma_f32_16x16x32_bf16 v[28:31], v[90:93], v[106:109], v[28:31]
	v_mfma_f32_16x16x32_bf16 v[24:27], v[98:101], v[106:109], v[24:27]
	v_mfma_f32_16x16x32_bf16 v[20:23], v[90:93], v[114:117], v[20:23]
	v_mfma_f32_16x16x32_bf16 v[16:19], v[98:101], v[114:117], v[16:19]
	v_mfma_f32_16x16x32_bf16 v[12:15], v[90:93], v[122:125], v[12:15]
	v_mfma_f32_16x16x32_bf16 v[8:11], v[98:101], v[122:125], v[8:11]
	v_mfma_f32_16x16x32_bf16 v[4:7], v[90:93], v[130:133], v[4:7]
	v_mfma_f32_16x16x32_bf16 v[0:3], v[98:101], v[130:133], v[0:3]
	s_barrier
	s_add_i32 s67, s67, 2
	s_add_u32 s36, s36, 0x100
	s_addc_u32 s37, s37, 0
	s_cmp_gt_u32 s67, 13
	s_cbranch_scc0 .LBB0_545
	s_and_b64 vcc, exec, s[18:19]
	s_cbranch_vccz .LBB0_548
	s_barrier

.LBB0_791:
	ds_read_b128 v[160:163], v152
	ds_read_b128 v[164:167], v152 offset:1024
	ds_read_b128 v[168:171], v152 offset:2048
	ds_read_b128 v[172:175], v152 offset:3072
	ds_read_b128 v[176:179], v153
	ds_read_b128 v[180:183], v153 offset:1024
	ds_read_b128 v[184:187], v153 offset:2048
	ds_read_b128 v[188:191], v153 offset:3072
	s_add_u32 s38, s30, s36
	s_addc_u32 s39, s31, s37
	s_add_u32 s40, s38, 0x100
	s_addc_u32 s41, s39, 0
	s_add_u32 s68, s23, s36
	s_addc_u32 s69, s66, s37
	s_cmpk_eq_i32 s36, 0x700
	s_cselect_b64 vcc, -1, 0
	s_and_b64 s[38:39], vcc, exec
	v_cndmask_b32_e32 v132, v138, v157, vcc
	s_cselect_b32 s41, s27, s41
	s_cselect_b32 s40, s26, s40
	v_cndmask_b32_e32 v224, v136, v156, vcc
	v_cndmask_b32_e32 v135, v134, v155, vcc
	v_cndmask_b32_e32 v141, v140, v158, vcc
	s_cselect_b32 s39, s25, s69
	s_cselect_b32 s38, s24, s68
	s_mov_b32 m0, s60
	v_lshl_add_u64 v[226:227], v[144:145], 0, s[36:37]
	ds_read_b128 v[192:195], v154
	ds_read_b128 v[196:199], v154 offset:1024
	ds_read_b128 v[200:203], v154 offset:2048
	ds_read_b128 v[204:207], v154 offset:3072
	ds_read_b128 v[208:211], v154 offset:4096
	ds_read_b128 v[212:215], v154 offset:5120
	ds_read_b128 v[216:219], v154 offset:6144
	ds_read_b128 v[220:223], v154 offset:7168
	global_load_lds_dwordx4 v[226:227], off
	v_lshl_add_u64 v[226:227], v[142:143], 0, s[36:37]
	s_add_i32 m0, s50, 0xe000
	s_nop 0
	global_load_lds_dwordx4 v[226:227], off
	s_waitcnt vmcnt(8)
	s_waitcnt lgkmcnt(0)
	s_barrier
	s_waitcnt lgkmcnt(0)
	v_mfma_f32_16x16x32_bf16 v[116:119], v[160:163], v[192:195], v[116:119]
	v_mfma_f32_16x16x32_bf16 v[112:115], v[168:171], v[192:195], v[112:115]
	v_mfma_f32_16x16x32_bf16 v[108:111], v[160:163], v[200:203], v[108:111]
	v_mfma_f32_16x16x32_bf16 v[104:107], v[168:171], v[200:203], v[104:107]
	v_mfma_f32_16x16x32_bf16 v[92:95], v[160:163], v[208:211], v[92:95]
	v_mfma_f32_16x16x32_bf16 v[88:91], v[168:171], v[208:211], v[88:91]
	v_mfma_f32_16x16x32_bf16 v[76:79], v[160:163], v[216:219], v[76:79]
	v_mfma_f32_16x16x32_bf16 v[72:75], v[168:171], v[216:219], v[72:75]
	v_mfma_f32_16x16x32_bf16 v[116:119], v[164:167], v[196:199], v[116:119]
	v_mfma_f32_16x16x32_bf16 v[112:115], v[172:175], v[196:199], v[112:115]
	v_mfma_f32_16x16x32_bf16 v[108:111], v[164:167], v[204:207], v[108:111]
	v_mfma_f32_16x16x32_bf16 v[104:107], v[172:175], v[204:207], v[104:107]
	v_mfma_f32_16x16x32_bf16 v[92:95], v[164:167], v[212:215], v[92:95]
	v_mfma_f32_16x16x32_bf16 v[88:91], v[172:175], v[212:215], v[88:91]
	v_mfma_f32_16x16x32_bf16 v[76:79], v[164:167], v[220:223], v[76:79]
	v_mfma_f32_16x16x32_bf16 v[72:75], v[172:175], v[220:223], v[72:75]
	v_mfma_f32_16x16x32_bf16 v[124:127], v[176:179], v[192:195], v[124:127]
	v_mfma_f32_16x16x32_bf16 v[120:123], v[184:187], v[192:195], v[120:123]
	v_mfma_f32_16x16x32_bf16 v[100:103], v[176:179], v[200:203], v[100:103]
	v_mfma_f32_16x16x32_bf16 v[96:99], v[184:187], v[200:203], v[96:99]
	v_mfma_f32_16x16x32_bf16 v[84:87], v[176:179], v[208:211], v[84:87]
	v_mfma_f32_16x16x32_bf16 v[80:83], v[184:187], v[208:211], v[80:83]
	v_mfma_f32_16x16x32_bf16 v[68:71], v[176:179], v[216:219], v[68:71]
	v_mfma_f32_16x16x32_bf16 v[64:67], v[184:187], v[216:219], v[64:67]
	v_mfma_f32_16x16x32_bf16 v[124:127], v[180:183], v[196:199], v[124:127]
	v_mfma_f32_16x16x32_bf16 v[120:123], v[188:191], v[196:199], v[120:123]
	v_mfma_f32_16x16x32_bf16 v[100:103], v[180:183], v[204:207], v[100:103]
	v_mfma_f32_16x16x32_bf16 v[96:99], v[188:191], v[204:207], v[96:99]
	v_mfma_f32_16x16x32_bf16 v[84:87], v[180:183], v[212:215], v[84:87]
	v_mfma_f32_16x16x32_bf16 v[80:83], v[188:191], v[212:215], v[80:83]
	v_mfma_f32_16x16x32_bf16 v[68:71], v[180:183], v[220:223], v[68:71]
	v_mfma_f32_16x16x32_bf16 v[64:67], v[188:191], v[220:223], v[64:67]
	s_barrier
	s_add_i32 s68, s57, s29
	v_lshl_add_u64 v[226:227], s[38:39], 0, v[128:129]
	s_mov_b32 m0, s68
	ds_read_b128 v[192:195], v154 offset:16384
	ds_read_b128 v[196:199], v154 offset:17408
	ds_read_b128 v[200:203], v154 offset:18432
	ds_read_b128 v[204:207], v154 offset:19456
	ds_read_b128 v[208:211], v154 offset:20480
	ds_read_b128 v[212:215], v154 offset:21504
	ds_read_b128 v[216:219], v154 offset:22528
	ds_read_b128 v[220:223], v154 offset:23552
	global_load_lds_dwordx4 v[226:227], off
	s_add_i32 m0, s68, 0x2000
	s_add_u32 s68, s38, 0x40000
	v_lshl_add_u64 v[228:229], s[38:39], 0, v[130:131]
	s_addc_u32 s69, s39, 0
	s_add_i32 s70, s58, s29
	global_load_lds_dwordx4 v[228:229], off
	v_lshl_add_u64 v[230:231], s[68:69], 0, v[128:129]
	s_mov_b32 m0, s70
	v_mov_b32_e32 v225, v133
	global_load_lds_dwordx4 v[230:231], off
	v_lshl_add_u64 v[230:231], s[68:69], 0, v[130:131]
	s_add_i32 m0, s70, 0x2000
	s_nop 0
	global_load_lds_dwordx4 v[230:231], off
	s_mov_b32 m0, s50
	v_lshl_add_u64 v[230:231], s[40:41], 0, v[132:133]
	global_load_lds_dwordx4 v132, s[40:41]
	s_mov_b32 m0, s51
	s_nop 0
	global_load_lds_dwordx4 v224, s[40:41]
	s_waitcnt vmcnt(8)
	s_waitcnt lgkmcnt(0)
	v_lshl_add_u64 v[224:225], s[40:41], 0, v[224:225]
	s_barrier
	s_waitcnt lgkmcnt(0)
	v_mfma_f32_16x16x32_bf16 v[60:63], v[160:163], v[192:195], v[60:63]
	v_mfma_f32_16x16x32_bf16 v[56:59], v[168:171], v[192:195], v[56:59]
	v_mfma_f32_16x16x32_bf16 v[44:47], v[160:163], v[200:203], v[44:47]
	v_mfma_f32_16x16x32_bf16 v[40:43], v[168:171], v[200:203], v[40:43]
	v_mfma_f32_16x16x32_bf16 v[28:31], v[160:163], v[208:211], v[28:31]
	v_mfma_f32_16x16x32_bf16 v[24:27], v[168:171], v[208:211], v[24:27]
	v_mfma_f32_16x16x32_bf16 v[12:15], v[160:163], v[216:219], v[12:15]
	v_mfma_f32_16x16x32_bf16 v[8:11], v[168:171], v[216:219], v[8:11]
	v_mfma_f32_16x16x32_bf16 v[60:63], v[164:167], v[196:199], v[60:63]
	v_mfma_f32_16x16x32_bf16 v[56:59], v[172:175], v[196:199], v[56:59]
	v_mfma_f32_16x16x32_bf16 v[44:47], v[164:167], v[204:207], v[44:47]
	v_mfma_f32_16x16x32_bf16 v[40:43], v[172:175], v[204:207], v[40:43]
	v_mfma_f32_16x16x32_bf16 v[28:31], v[164:167], v[212:215], v[28:31]
	v_mfma_f32_16x16x32_bf16 v[24:27], v[172:175], v[212:215], v[24:27]
	v_mfma_f32_16x16x32_bf16 v[12:15], v[164:167], v[220:223], v[12:15]
	v_mfma_f32_16x16x32_bf16 v[8:11], v[172:175], v[220:223], v[8:11]
	v_mfma_f32_16x16x32_bf16 v[52:55], v[176:179], v[192:195], v[52:55]
	v_mfma_f32_16x16x32_bf16 v[48:51], v[184:187], v[192:195], v[48:51]
	v_mfma_f32_16x16x32_bf16 v[36:39], v[176:179], v[200:203], v[36:39]
	v_mfma_f32_16x16x32_bf16 v[32:35], v[184:187], v[200:203], v[32:35]
	v_mfma_f32_16x16x32_bf16 v[20:23], v[176:179], v[208:211], v[20:23]
	v_mfma_f32_16x16x32_bf16 v[16:19], v[184:187], v[208:211], v[16:19]
	v_mfma_f32_16x16x32_bf16 v[4:7], v[176:179], v[216:219], v[4:7]
	v_mfma_f32_16x16x32_bf16 v[0:3], v[184:187], v[216:219], v[0:3]
	v_mfma_f32_16x16x32_bf16 v[52:55], v[180:183], v[196:199], v[52:55]
	v_mfma_f32_16x16x32_bf16 v[48:51], v[188:191], v[196:199], v[48:51]
	v_mfma_f32_16x16x32_bf16 v[36:39], v[180:183], v[204:207], v[36:39]
	v_mfma_f32_16x16x32_bf16 v[32:35], v[188:191], v[204:207], v[32:35]
	v_mfma_f32_16x16x32_bf16 v[20:23], v[180:183], v[212:215], v[20:23]
	v_mfma_f32_16x16x32_bf16 v[16:19], v[188:191], v[212:215], v[16:19]
	v_mfma_f32_16x16x32_bf16 v[4:7], v[180:183], v[220:223], v[4:7]
	v_mfma_f32_16x16x32_bf16 v[0:3], v[188:191], v[220:223], v[0:3]
	s_barrier
	s_add_i32 s68, 0, 0x18000
	v_add_u32_e32 v132, s68, v139
	s_add_i32 s69, 0, 0x1c000
	ds_read_b128 v[160:163], v132
	ds_read_b128 v[164:167], v132 offset:1024
	ds_read_b128 v[168:171], v132 offset:2048
	ds_read_b128 v[172:175], v132 offset:3072
	v_add_u32_e32 v132, s69, v139
	ds_read_b128 v[176:179], v132
	ds_read_b128 v[180:183], v132 offset:1024
	ds_read_b128 v[184:187], v132 offset:2048
	ds_read_b128 v[188:191], v132 offset:3072
	s_mov_b32 m0, s52
	ds_read_b128 v[192:195], v154 offset:32768
	ds_read_b128 v[196:199], v154 offset:33792
	ds_read_b128 v[200:203], v154 offset:34816
	ds_read_b128 v[204:207], v154 offset:35840
	ds_read_b128 v[208:211], v154 offset:36864
	ds_read_b128 v[212:215], v154 offset:37888
	ds_read_b128 v[216:219], v154 offset:38912
	ds_read_b128 v[220:223], v154 offset:39936
	global_load_lds_dwordx4 v135, s[40:41]
	s_mov_b32 m0, s53
	s_nop 0
	global_load_lds_dwordx4 v141, s[40:41]
	s_waitcnt vmcnt(8)
	s_waitcnt lgkmcnt(0)
	s_barrier
	s_waitcnt lgkmcnt(0)
	v_mfma_f32_16x16x32_bf16 v[116:119], v[160:163], v[192:195], v[116:119]
	v_mfma_f32_16x16x32_bf16 v[112:115], v[168:171], v[192:195], v[112:115]
	v_mfma_f32_16x16x32_bf16 v[108:111], v[160:163], v[200:203], v[108:111]
	v_mfma_f32_16x16x32_bf16 v[104:107], v[168:171], v[200:203], v[104:107]
	v_mfma_f32_16x16x32_bf16 v[92:95], v[160:163], v[208:211], v[92:95]
	v_mfma_f32_16x16x32_bf16 v[88:91], v[168:171], v[208:211], v[88:91]
	v_mfma_f32_16x16x32_bf16 v[76:79], v[160:163], v[216:219], v[76:79]
	v_mfma_f32_16x16x32_bf16 v[72:75], v[168:171], v[216:219], v[72:75]
	v_mfma_f32_16x16x32_bf16 v[116:119], v[164:167], v[196:199], v[116:119]
	v_mfma_f32_16x16x32_bf16 v[112:115], v[172:175], v[196:199], v[112:115]
	v_mfma_f32_16x16x32_bf16 v[108:111], v[164:167], v[204:207], v[108:111]
	v_mfma_f32_16x16x32_bf16 v[104:107], v[172:175], v[204:207], v[104:107]
	v_mfma_f32_16x16x32_bf16 v[92:95], v[164:167], v[212:215], v[92:95]
	v_mfma_f32_16x16x32_bf16 v[88:91], v[172:175], v[212:215], v[88:91]
	v_mfma_f32_16x16x32_bf16 v[76:79], v[164:167], v[220:223], v[76:79]
	v_mfma_f32_16x16x32_bf16 v[72:75], v[172:175], v[220:223], v[72:75]
	v_mfma_f32_16x16x32_bf16 v[124:127], v[176:179], v[192:195], v[124:127]
	v_mfma_f32_16x16x32_bf16 v[120:123], v[184:187], v[192:195], v[120:123]
	v_mfma_f32_16x16x32_bf16 v[100:103], v[176:179], v[200:203], v[100:103]
	v_mfma_f32_16x16x32_bf16 v[96:99], v[184:187], v[200:203], v[96:99]
	v_mfma_f32_16x16x32_bf16 v[84:87], v[176:179], v[208:211], v[84:87]
	v_mfma_f32_16x16x32_bf16 v[80:83], v[184:187], v[208:211], v[80:83]
	v_mfma_f32_16x16x32_bf16 v[68:71], v[176:179], v[216:219], v[68:71]
	v_mfma_f32_16x16x32_bf16 v[64:67], v[184:187], v[216:219], v[64:67]
	v_mfma_f32_16x16x32_bf16 v[124:127], v[180:183], v[196:199], v[124:127]
	v_mfma_f32_16x16x32_bf16 v[120:123], v[188:191], v[196:199], v[120:123]
	v_mfma_f32_16x16x32_bf16 v[100:103], v[180:183], v[204:207], v[100:103]
	v_mfma_f32_16x16x32_bf16 v[96:99], v[188:191], v[204:207], v[96:99]
	v_mfma_f32_16x16x32_bf16 v[84:87], v[180:183], v[212:215], v[84:87]
	v_mfma_f32_16x16x32_bf16 v[80:83], v[188:191], v[212:215], v[80:83]
	v_mfma_f32_16x16x32_bf16 v[68:71], v[180:183], v[220:223], v[68:71]
	v_mfma_f32_16x16x32_bf16 v[64:67], v[188:191], v[220:223], v[64:67]
	s_barrier
	s_add_i32 s40, s68, s29
	v_lshl_add_u64 v[226:227], v[226:227], 0, s[18:19]
	s_mov_b32 m0, s40
	ds_read_b128 v[192:195], v154 offset:49152
	ds_read_b128 v[196:199], v154 offset:50176
	ds_read_b128 v[200:203], v154 offset:51200
	ds_read_b128 v[204:207], v154 offset:52224
	ds_read_b128 v[208:211], v154 offset:53248
	ds_read_b128 v[212:215], v154 offset:54272
	ds_read_b128 v[216:219], v154 offset:55296
	ds_read_b128 v[220:223], v154 offset:56320
	global_load_lds_dwordx4 v[226:227], off
	s_add_i32 m0, s40, 0x2000
	s_add_u32 s38, s38, 0x40080
	v_lshl_add_u64 v[226:227], v[228:229], 0, s[18:19]
	s_addc_u32 s39, s39, 0
	s_add_i32 s40, s69, s29
	global_load_lds_dwordx4 v[226:227], off
	v_lshl_add_u64 v[226:227], s[38:39], 0, v[128:129]
	s_mov_b32 m0, s40
	v_lshl_add_u64 v[224:225], v[224:225], 0, s[18:19]
	global_load_lds_dwordx4 v[226:227], off
	v_lshl_add_u64 v[226:227], s[38:39], 0, v[130:131]
	s_add_i32 m0, s40, 0x2000
	s_nop 0
	global_load_lds_dwordx4 v[226:227], off
	v_lshl_add_u64 v[226:227], v[230:231], 0, s[18:19]
	s_mov_b32 m0, s55
	s_nop 0
	global_load_lds_dwordx4 v[226:227], off
	s_mov_b32 m0, s56
	s_nop 0
	global_load_lds_dwordx4 v[224:225], off
	s_waitcnt vmcnt(8)
	s_waitcnt lgkmcnt(0)
	s_barrier
	s_waitcnt lgkmcnt(0)
	v_mfma_f32_16x16x32_bf16 v[60:63], v[160:163], v[192:195], v[60:63]
	v_mfma_f32_16x16x32_bf16 v[56:59], v[168:171], v[192:195], v[56:59]
	v_mfma_f32_16x16x32_bf16 v[44:47], v[160:163], v[200:203], v[44:47]
	v_mfma_f32_16x16x32_bf16 v[40:43], v[168:171], v[200:203], v[40:43]
	v_mfma_f32_16x16x32_bf16 v[28:31], v[160:163], v[208:211], v[28:31]
	v_mfma_f32_16x16x32_bf16 v[24:27], v[168:171], v[208:211], v[24:27]
	v_mfma_f32_16x16x32_bf16 v[12:15], v[160:163], v[216:219], v[12:15]
	v_mfma_f32_16x16x32_bf16 v[8:11], v[168:171], v[216:219], v[8:11]
	v_mfma_f32_16x16x32_bf16 v[60:63], v[164:167], v[196:199], v[60:63]
	v_mfma_f32_16x16x32_bf16 v[56:59], v[172:175], v[196:199], v[56:59]
	v_mfma_f32_16x16x32_bf16 v[44:47], v[164:167], v[204:207], v[44:47]
	v_mfma_f32_16x16x32_bf16 v[40:43], v[172:175], v[204:207], v[40:43]
	v_mfma_f32_16x16x32_bf16 v[28:31], v[164:167], v[212:215], v[28:31]
	v_mfma_f32_16x16x32_bf16 v[24:27], v[172:175], v[212:215], v[24:27]
	v_mfma_f32_16x16x32_bf16 v[12:15], v[164:167], v[220:223], v[12:15]
	v_mfma_f32_16x16x32_bf16 v[8:11], v[172:175], v[220:223], v[8:11]
	v_mfma_f32_16x16x32_bf16 v[52:55], v[176:179], v[192:195], v[52:55]
	v_mfma_f32_16x16x32_bf16 v[48:51], v[184:187], v[192:195], v[48:51]
	v_mfma_f32_16x16x32_bf16 v[36:39], v[176:179], v[200:203], v[36:39]
	v_mfma_f32_16x16x32_bf16 v[32:35], v[184:187], v[200:203], v[32:35]
	v_mfma_f32_16x16x32_bf16 v[20:23], v[176:179], v[208:211], v[20:23]
	v_mfma_f32_16x16x32_bf16 v[16:19], v[184:187], v[208:211], v[16:19]
	v_mfma_f32_16x16x32_bf16 v[4:7], v[176:179], v[216:219], v[4:7]
	v_mfma_f32_16x16x32_bf16 v[0:3], v[184:187], v[216:219], v[0:3]
	v_mfma_f32_16x16x32_bf16 v[52:55], v[180:183], v[196:199], v[52:55]
	v_mfma_f32_16x16x32_bf16 v[48:51], v[188:191], v[196:199], v[48:51]
	v_mfma_f32_16x16x32_bf16 v[36:39], v[180:183], v[204:207], v[36:39]
	v_mfma_f32_16x16x32_bf16 v[32:35], v[188:191], v[204:207], v[32:35]
	v_mfma_f32_16x16x32_bf16 v[20:23], v[180:183], v[212:215], v[20:23]
	v_mfma_f32_16x16x32_bf16 v[16:19], v[188:191], v[212:215], v[16:19]
	v_mfma_f32_16x16x32_bf16 v[4:7], v[180:183], v[220:223], v[4:7]
	v_mfma_f32_16x16x32_bf16 v[0:3], v[188:191], v[220:223], v[0:3]
	s_barrier
	s_add_i32 s67, s67, 2
	s_add_u32 s36, s36, 0x100
	s_addc_u32 s37, s37, 0
	s_cmp_gt_u32 s67, 13
	s_cbranch_scc0 .LBB0_791
	s_and_b64 vcc, exec, s[20:21]
	s_cbranch_vccz .LBB0_794
	s_barrier

.LBB0_1068:
	ds_read_b128 v[8:11], v149
	ds_read_b128 v[12:15], v149 offset:1024
	ds_read_b128 v[16:19], v149 offset:2048
	ds_read_b128 v[20:23], v149 offset:3072
	ds_read_b128 v[24:27], v150
	ds_read_b128 v[28:31], v150 offset:1024
	ds_read_b128 v[32:35], v150 offset:2048
	ds_read_b128 v[36:39], v150 offset:3072
	s_add_u32 s68, s36, 0x18080
	s_addc_u32 s69, s37, 0
	s_mov_b32 m0, s62
	v_lshl_add_u64 v[64:65], s[68:69], 0, v[128:129]
	ds_read_b128 v[0:3], v140
	ds_read_b128 v[4:7], v140 offset:1024
	ds_read_b128 v[40:43], v140 offset:2048
	ds_read_b128 v[44:47], v140 offset:3072
	ds_read_b128 v[48:51], v140 offset:4096
	ds_read_b128 v[52:55], v140 offset:5120
	ds_read_b128 v[56:59], v140 offset:6144
	ds_read_b128 v[60:63], v140 offset:7168
	global_load_lds_dwordx4 v[64:65], off
	v_lshl_add_u64 v[64:65], s[68:69], 0, v[132:133]
	s_mov_b32 m0, s63
	s_nop 0
	global_load_lds_dwordx4 v[64:65], off
	s_waitcnt vmcnt(8)
	s_waitcnt lgkmcnt(0)
	s_barrier
	s_waitcnt lgkmcnt(0)
	v_mfma_f32_16x16x32_bf16 v[64:67], v[8:11], v[0:3], 0
	v_mfma_f32_16x16x32_bf16 v[68:71], v[16:19], v[0:3], 0
	v_mfma_f32_16x16x32_bf16 v[72:75], v[8:11], v[40:43], 0
	v_mfma_f32_16x16x32_bf16 v[76:79], v[16:19], v[40:43], 0
	v_mfma_f32_16x16x32_bf16 v[80:83], v[8:11], v[48:51], 0
	v_mfma_f32_16x16x32_bf16 v[84:87], v[16:19], v[48:51], 0
	v_mfma_f32_16x16x32_bf16 v[88:91], v[8:11], v[56:59], 0
	v_mfma_f32_16x16x32_bf16 v[92:95], v[16:19], v[56:59], 0
	v_mfma_f32_16x16x32_bf16 v[64:67], v[12:15], v[4:7], v[64:67]
	v_mfma_f32_16x16x32_bf16 v[68:71], v[20:23], v[4:7], v[68:71]
	v_mfma_f32_16x16x32_bf16 v[72:75], v[12:15], v[44:47], v[72:75]
	v_mfma_f32_16x16x32_bf16 v[76:79], v[20:23], v[44:47], v[76:79]
	v_mfma_f32_16x16x32_bf16 v[80:83], v[12:15], v[52:55], v[80:83]
	v_mfma_f32_16x16x32_bf16 v[84:87], v[20:23], v[52:55], v[84:87]
	v_mfma_f32_16x16x32_bf16 v[88:91], v[12:15], v[60:63], v[88:91]
	v_mfma_f32_16x16x32_bf16 v[92:95], v[20:23], v[60:63], v[92:95]
	v_mfma_f32_16x16x32_bf16 v[96:99], v[24:27], v[0:3], 0
	v_mfma_f32_16x16x32_bf16 v[0:3], v[32:35], v[0:3], 0
	v_mfma_f32_16x16x32_bf16 v[100:103], v[36:39], v[4:7], v[0:3]
	v_mfma_f32_16x16x32_bf16 v[0:3], v[24:27], v[40:43], 0
	v_mfma_f32_16x16x32_bf16 v[104:107], v[28:31], v[44:47], v[0:3]
	v_mfma_f32_16x16x32_bf16 v[0:3], v[32:35], v[40:43], 0
	v_mfma_f32_16x16x32_bf16 v[40:43], v[36:39], v[44:47], v[0:3]
	v_mfma_f32_16x16x32_bf16 v[0:3], v[24:27], v[48:51], 0
	v_mfma_f32_16x16x32_bf16 v[44:47], v[28:31], v[52:55], v[0:3]
	v_mfma_f32_16x16x32_bf16 v[0:3], v[32:35], v[48:51], 0
	v_mfma_f32_16x16x32_bf16 v[48:51], v[36:39], v[52:55], v[0:3]
	v_mfma_f32_16x16x32_bf16 v[0:3], v[24:27], v[56:59], 0
	v_mfma_f32_16x16x32_bf16 v[52:55], v[28:31], v[60:63], v[0:3]
	v_mfma_f32_16x16x32_bf16 v[0:3], v[32:35], v[56:59], 0
	v_mfma_f32_16x16x32_bf16 v[96:99], v[28:31], v[4:7], v[96:99]
	v_mfma_f32_16x16x32_bf16 v[56:59], v[36:39], v[60:63], v[0:3]
	s_barrier
	s_nop 3
	v_lshl_add_u64 v[0:1], s[38:39], 0, v[130:131]
	s_add_i32 s71, s60, s46
	v_lshl_add_u64 v[2:3], v[0:1], 0, s[18:19]
	s_mov_b32 m0, s71
	s_add_i32 s68, s71, 0x2000
	ds_read_b128 v[60:63], v140 offset:16384
	ds_read_b128 v[108:111], v140 offset:17408
	ds_read_b128 v[112:115], v140 offset:18432
	ds_read_b128 v[116:119], v140 offset:19456
	ds_read_b128 v[120:123], v140 offset:20480
	ds_read_b128 v[124:127], v140 offset:21504
	ds_read_b128 v[152:155], v140 offset:22528
	ds_read_b128 v[156:159], v140 offset:23552
	global_load_lds_dwordx4 v[2:3], off
	v_lshl_add_u64 v[2:3], s[38:39], 0, v[134:135]
	s_add_u32 s72, s38, 0x1900
	v_lshl_add_u64 v[4:5], v[2:3], 0, s[18:19]
	s_mov_b32 m0, s68
	s_addc_u32 s73, s39, 0
	s_add_i32 s69, s61, s46
	global_load_lds_dwordx4 v[4:5], off
	v_lshl_add_u64 v[4:5], s[72:73], 0, v[130:131]
	s_mov_b32 m0, s69
	s_add_i32 s70, s69, 0x2000
	global_load_lds_dwordx4 v[4:5], off
	v_lshl_add_u64 v[4:5], s[72:73], 0, v[134:135]
	s_mov_b32 m0, s70
	s_nop 0
	global_load_lds_dwordx4 v[4:5], off
	v_lshl_add_u64 v[4:5], s[36:37], 0, v[128:129]
	v_lshl_add_u64 v[6:7], v[4:5], 0, s[18:19]
	s_mov_b32 m0, s47
	s_nop 0
	global_load_lds_dwordx4 v[6:7], off
	v_lshl_add_u64 v[6:7], s[36:37], 0, v[132:133]
	v_lshl_add_u64 v[136:137], v[6:7], 0, s[18:19]
	s_mov_b32 m0, s48
	s_nop 0
	global_load_lds_dwordx4 v[136:137], off
	s_waitcnt vmcnt(8)
	s_waitcnt lgkmcnt(0)
	s_barrier
	s_waitcnt lgkmcnt(0)
	v_mfma_f32_16x16x32_bf16 v[160:163], v[8:11], v[60:63], 0
	v_mfma_f32_16x16x32_bf16 v[168:171], v[8:11], v[112:115], 0
	v_mfma_f32_16x16x32_bf16 v[176:179], v[8:11], v[120:123], 0
	v_mfma_f32_16x16x32_bf16 v[8:11], v[8:11], v[152:155], 0
	v_mfma_f32_16x16x32_bf16 v[160:163], v[12:15], v[108:111], v[160:163]
	v_mfma_f32_16x16x32_bf16 v[164:167], v[16:19], v[60:63], 0
	v_mfma_f32_16x16x32_bf16 v[168:171], v[12:15], v[116:119], v[168:171]
	v_mfma_f32_16x16x32_bf16 v[172:175], v[16:19], v[112:115], 0
	v_mfma_f32_16x16x32_bf16 v[176:179], v[12:15], v[124:127], v[176:179]
	v_mfma_f32_16x16x32_bf16 v[180:183], v[16:19], v[120:123], 0
	v_mfma_f32_16x16x32_bf16 v[10:13], v[12:15], v[156:159], v[8:11]
	v_mfma_f32_16x16x32_bf16 v[14:17], v[16:19], v[152:155], 0
	v_mfma_f32_16x16x32_bf16 v[14:17], v[20:23], v[156:159], v[14:17]
	v_mfma_f32_16x16x32_bf16 v[164:167], v[20:23], v[108:111], v[164:167]
	v_mfma_f32_16x16x32_bf16 v[172:175], v[20:23], v[116:119], v[172:175]
	v_mfma_f32_16x16x32_bf16 v[180:183], v[20:23], v[124:127], v[180:183]
	v_mfma_f32_16x16x32_bf16 v[18:21], v[24:27], v[60:63], 0
	v_mfma_f32_16x16x32_bf16 v[60:63], v[32:35], v[60:63], 0
	v_mfma_f32_16x16x32_bf16 v[18:21], v[28:31], v[108:111], v[18:21]
	v_mfma_f32_16x16x32_bf16 v[60:63], v[36:39], v[108:111], v[60:63]
	v_mfma_f32_16x16x32_bf16 v[108:111], v[24:27], v[112:115], 0
	v_mfma_f32_16x16x32_bf16 v[112:115], v[32:35], v[112:115], 0
	v_mfma_f32_16x16x32_bf16 v[108:111], v[28:31], v[116:119], v[108:111]
	v_mfma_f32_16x16x32_bf16 v[112:115], v[36:39], v[116:119], v[112:115]
	v_mfma_f32_16x16x32_bf16 v[116:119], v[24:27], v[120:123], 0
	v_mfma_f32_16x16x32_bf16 v[22:25], v[24:27], v[152:155], 0
	v_mfma_f32_16x16x32_bf16 v[116:119], v[28:31], v[124:127], v[116:119]
	v_mfma_f32_16x16x32_bf16 v[120:123], v[32:35], v[120:123], 0
	v_mfma_f32_16x16x32_bf16 v[22:25], v[28:31], v[156:159], v[22:25]
	v_mfma_f32_16x16x32_bf16 v[26:29], v[32:35], v[152:155], 0
	v_mfma_f32_16x16x32_bf16 v[120:123], v[36:39], v[124:127], v[120:123]
	v_mfma_f32_16x16x32_bf16 v[26:29], v[36:39], v[156:159], v[26:29]
	s_barrier
	s_add_i32 s75, 0, 0x18000
	s_add_i32 s74, 0, 0x1c000
	v_add_u32_e32 v8, s75, v139
	v_add_u32_e32 v9, s74, v139
	ds_read_b128 v[30:33], v8
	ds_read_b128 v[34:37], v8 offset:1024
	ds_read_b128 v[124:127], v8 offset:2048
	ds_read_b128 v[152:155], v8 offset:3072
	ds_read_b128 v[156:159], v9
	ds_read_b128 v[184:187], v9 offset:1024
	ds_read_b128 v[188:191], v9 offset:2048
	ds_read_b128 v[192:195], v9 offset:3072
	s_add_u32 s72, s36, 0x18100
	s_addc_u32 s73, s37, 0
	s_mov_b32 m0, s50
	v_lshl_add_u64 v[38:39], s[72:73], 0, v[128:129]
	ds_read_b128 v[196:199], v140 offset:32768
	ds_read_b128 v[200:203], v140 offset:33792
	ds_read_b128 v[204:207], v140 offset:34816
	ds_read_b128 v[208:211], v140 offset:35840
	ds_read_b128 v[212:215], v140 offset:36864
	ds_read_b128 v[216:219], v140 offset:37888
	ds_read_b128 v[220:223], v140 offset:38912
	ds_read_b128 v[224:227], v140 offset:39936
	global_load_lds_dwordx4 v[38:39], off
	v_lshl_add_u64 v[38:39], s[72:73], 0, v[132:133]
	s_mov_b32 m0, s51
	s_nop 0
	global_load_lds_dwordx4 v[38:39], off
	s_waitcnt vmcnt(8)
	s_waitcnt lgkmcnt(0)
	s_barrier
	s_waitcnt lgkmcnt(0)
	v_mfma_f32_16x16x32_bf16 v[64:67], v[30:33], v[196:199], v[64:67]
	v_mfma_f32_16x16x32_bf16 v[68:71], v[124:127], v[196:199], v[68:71]
	v_mfma_f32_16x16x32_bf16 v[72:75], v[30:33], v[204:207], v[72:75]
	v_mfma_f32_16x16x32_bf16 v[76:79], v[124:127], v[204:207], v[76:79]
	v_mfma_f32_16x16x32_bf16 v[80:83], v[30:33], v[212:215], v[80:83]
	v_mfma_f32_16x16x32_bf16 v[84:87], v[124:127], v[212:215], v[84:87]
	v_mfma_f32_16x16x32_bf16 v[88:91], v[30:33], v[220:223], v[88:91]
	v_mfma_f32_16x16x32_bf16 v[92:95], v[124:127], v[220:223], v[92:95]
	v_mfma_f32_16x16x32_bf16 v[64:67], v[34:37], v[200:203], v[64:67]
	v_mfma_f32_16x16x32_bf16 v[68:71], v[152:155], v[200:203], v[68:71]
	v_mfma_f32_16x16x32_bf16 v[72:75], v[34:37], v[208:211], v[72:75]
	v_mfma_f32_16x16x32_bf16 v[76:79], v[152:155], v[208:211], v[76:79]
	v_mfma_f32_16x16x32_bf16 v[80:83], v[34:37], v[216:219], v[80:83]
	v_mfma_f32_16x16x32_bf16 v[84:87], v[152:155], v[216:219], v[84:87]
	v_mfma_f32_16x16x32_bf16 v[88:91], v[34:37], v[224:227], v[88:91]
	v_mfma_f32_16x16x32_bf16 v[92:95], v[152:155], v[224:227], v[92:95]
	v_mfma_f32_16x16x32_bf16 v[96:99], v[156:159], v[196:199], v[96:99]
	v_mfma_f32_16x16x32_bf16 v[100:103], v[188:191], v[196:199], v[100:103]
	v_mfma_f32_16x16x32_bf16 v[104:107], v[156:159], v[204:207], v[104:107]
	v_mfma_f32_16x16x32_bf16 v[38:41], v[188:191], v[204:207], v[40:43]
	v_mfma_f32_16x16x32_bf16 v[42:45], v[156:159], v[212:215], v[44:47]
	v_mfma_f32_16x16x32_bf16 v[46:49], v[188:191], v[212:215], v[48:51]
	v_mfma_f32_16x16x32_bf16 v[50:53], v[156:159], v[220:223], v[52:55]
	v_mfma_f32_16x16x32_bf16 v[54:57], v[188:191], v[220:223], v[56:59]
	v_mfma_f32_16x16x32_bf16 v[96:99], v[184:187], v[200:203], v[96:99]
	v_mfma_f32_16x16x32_bf16 v[100:103], v[192:195], v[200:203], v[100:103]
	v_mfma_f32_16x16x32_bf16 v[104:107], v[184:187], v[208:211], v[104:107]
	v_mfma_f32_16x16x32_bf16 v[38:41], v[192:195], v[208:211], v[38:41]
	v_mfma_f32_16x16x32_bf16 v[42:45], v[184:187], v[216:219], v[42:45]
	v_mfma_f32_16x16x32_bf16 v[46:49], v[192:195], v[216:219], v[46:49]
	v_mfma_f32_16x16x32_bf16 v[50:53], v[184:187], v[224:227], v[50:53]
	v_mfma_f32_16x16x32_bf16 v[54:57], v[192:195], v[224:227], v[54:57]
	s_barrier
	s_add_i32 s75, s75, s46
	s_add_i32 s72, s75, 0x2000
	v_lshl_add_u64 v[58:59], v[0:1], 0, s[20:21]
	s_mov_b32 m0, s75
	s_add_u32 s76, s38, 0x1980
	ds_read_b128 v[196:199], v140 offset:49152
	ds_read_b128 v[200:203], v140 offset:50176
	ds_read_b128 v[204:207], v140 offset:51200
	ds_read_b128 v[208:211], v140 offset:52224
	ds_read_b128 v[212:215], v140 offset:53248
	ds_read_b128 v[216:219], v140 offset:54272
	ds_read_b128 v[220:223], v140 offset:55296
	ds_read_b128 v[224:227], v140 offset:56320
	global_load_lds_dwordx4 v[58:59], off
	v_lshl_add_u64 v[58:59], v[2:3], 0, s[20:21]
	s_mov_b32 m0, s72
	s_addc_u32 s77, s39, 0
	s_add_i32 s73, s74, s46
	global_load_lds_dwordx4 v[58:59], off
	v_lshl_add_u64 v[58:59], s[76:77], 0, v[130:131]
	s_mov_b32 m0, s73
	s_add_i32 s74, s73, 0x2000
	global_load_lds_dwordx4 v[58:59], off
	v_lshl_add_u64 v[58:59], s[76:77], 0, v[134:135]
	s_mov_b32 m0, s74
	s_nop 0
	global_load_lds_dwordx4 v[58:59], off
	v_lshl_add_u64 v[58:59], v[4:5], 0, s[20:21]
	s_mov_b32 m0, s53
	s_nop 0
	global_load_lds_dwordx4 v[58:59], off
	v_lshl_add_u64 v[58:59], v[6:7], 0, s[20:21]
	s_mov_b32 m0, s54
	s_nop 0
	global_load_lds_dwordx4 v[58:59], off
	s_waitcnt vmcnt(8)
	s_waitcnt lgkmcnt(0)
	s_barrier
	s_waitcnt lgkmcnt(0)
	v_mfma_f32_16x16x32_bf16 v[10:13], v[30:33], v[220:223], v[10:13]
	v_mfma_f32_16x16x32_bf16 v[14:17], v[124:127], v[220:223], v[14:17]
	v_mfma_f32_16x16x32_bf16 v[160:163], v[30:33], v[196:199], v[160:163]
	v_mfma_f32_16x16x32_bf16 v[164:167], v[124:127], v[196:199], v[164:167]
	v_mfma_f32_16x16x32_bf16 v[168:171], v[30:33], v[204:207], v[168:171]
	v_mfma_f32_16x16x32_bf16 v[172:175], v[124:127], v[204:207], v[172:175]
	v_mfma_f32_16x16x32_bf16 v[176:179], v[30:33], v[212:215], v[176:179]
	v_mfma_f32_16x16x32_bf16 v[180:183], v[124:127], v[212:215], v[180:183]
	v_mfma_f32_16x16x32_bf16 v[10:13], v[34:37], v[224:227], v[10:13]
	v_mfma_f32_16x16x32_bf16 v[14:17], v[152:155], v[224:227], v[14:17]
	v_mfma_f32_16x16x32_bf16 v[160:163], v[34:37], v[200:203], v[160:163]
	v_mfma_f32_16x16x32_bf16 v[164:167], v[152:155], v[200:203], v[164:167]
	v_mfma_f32_16x16x32_bf16 v[168:171], v[34:37], v[208:211], v[168:171]
	v_mfma_f32_16x16x32_bf16 v[172:175], v[152:155], v[208:211], v[172:175]
	v_mfma_f32_16x16x32_bf16 v[176:179], v[34:37], v[216:219], v[176:179]
	v_mfma_f32_16x16x32_bf16 v[180:183], v[152:155], v[216:219], v[180:183]
	v_mfma_f32_16x16x32_bf16 v[18:21], v[156:159], v[196:199], v[18:21]
	v_mfma_f32_16x16x32_bf16 v[30:33], v[188:191], v[196:199], v[60:63]
	v_mfma_f32_16x16x32_bf16 v[34:37], v[156:159], v[204:207], v[108:111]
	v_mfma_f32_16x16x32_bf16 v[58:61], v[188:191], v[204:207], v[112:115]
	v_mfma_f32_16x16x32_bf16 v[108:111], v[156:159], v[212:215], v[116:119]
	v_mfma_f32_16x16x32_bf16 v[112:115], v[188:191], v[212:215], v[120:123]
	v_mfma_f32_16x16x32_bf16 v[22:25], v[156:159], v[220:223], v[22:25]
	v_mfma_f32_16x16x32_bf16 v[26:29], v[188:191], v[220:223], v[26:29]
	v_mfma_f32_16x16x32_bf16 v[18:21], v[184:187], v[200:203], v[18:21]
	v_mfma_f32_16x16x32_bf16 v[30:33], v[192:195], v[200:203], v[30:33]
	v_mfma_f32_16x16x32_bf16 v[34:37], v[184:187], v[208:211], v[34:37]
	v_mfma_f32_16x16x32_bf16 v[58:61], v[192:195], v[208:211], v[58:61]
	v_mfma_f32_16x16x32_bf16 v[108:111], v[184:187], v[216:219], v[108:111]
	v_mfma_f32_16x16x32_bf16 v[112:115], v[192:195], v[216:219], v[112:115]
	v_mfma_f32_16x16x32_bf16 v[22:25], v[184:187], v[224:227], v[22:25]
	v_mfma_f32_16x16x32_bf16 v[26:29], v[192:195], v[224:227], v[26:29]
	s_barrier
	ds_read_b128 v[116:119], v149
	ds_read_b128 v[120:123], v149 offset:1024
	ds_read_b128 v[124:127], v149 offset:2048
	ds_read_b128 v[152:155], v149 offset:3072
	ds_read_b128 v[156:159], v150
	ds_read_b128 v[184:187], v150 offset:1024
	ds_read_b128 v[188:191], v150 offset:2048
	ds_read_b128 v[192:195], v150 offset:3072
	s_add_u32 s76, s36, 0x18180
	s_addc_u32 s77, s37, 0
	s_mov_b32 m0, s62
	v_lshl_add_u64 v[62:63], s[76:77], 0, v[128:129]
	ds_read_b128 v[196:199], v140
	ds_read_b128 v[200:203], v140 offset:1024
	ds_read_b128 v[204:207], v140 offset:2048
	ds_read_b128 v[208:211], v140 offset:3072
	ds_read_b128 v[212:215], v140 offset:4096
	ds_read_b128 v[216:219], v140 offset:5120
	ds_read_b128 v[220:223], v140 offset:6144
	ds_read_b128 v[224:227], v140 offset:7168
	global_load_lds_dwordx4 v[62:63], off
	v_lshl_add_u64 v[62:63], s[76:77], 0, v[132:133]
	s_mov_b32 m0, s63
	s_nop 0
	global_load_lds_dwordx4 v[62:63], off
	s_waitcnt vmcnt(8)
	s_waitcnt lgkmcnt(0)
	s_barrier
	s_waitcnt lgkmcnt(0)
	v_mfma_f32_16x16x32_bf16 v[62:65], v[116:119], v[196:199], v[64:67]
	v_mfma_f32_16x16x32_bf16 v[66:69], v[124:127], v[196:199], v[68:71]
	v_mfma_f32_16x16x32_bf16 v[70:73], v[116:119], v[204:207], v[72:75]
	v_mfma_f32_16x16x32_bf16 v[74:77], v[124:127], v[204:207], v[76:79]
	v_mfma_f32_16x16x32_bf16 v[78:81], v[116:119], v[212:215], v[80:83]
	v_mfma_f32_16x16x32_bf16 v[82:85], v[124:127], v[212:215], v[84:87]
	v_mfma_f32_16x16x32_bf16 v[86:89], v[116:119], v[220:223], v[88:91]
	v_mfma_f32_16x16x32_bf16 v[90:93], v[124:127], v[220:223], v[92:95]
	v_mfma_f32_16x16x32_bf16 v[62:65], v[120:123], v[200:203], v[62:65]
	v_mfma_f32_16x16x32_bf16 v[66:69], v[152:155], v[200:203], v[66:69]
	v_mfma_f32_16x16x32_bf16 v[70:73], v[120:123], v[208:211], v[70:73]
	v_mfma_f32_16x16x32_bf16 v[74:77], v[152:155], v[208:211], v[74:77]
	v_mfma_f32_16x16x32_bf16 v[78:81], v[120:123], v[216:219], v[78:81]
	v_mfma_f32_16x16x32_bf16 v[82:85], v[152:155], v[216:219], v[82:85]
	v_mfma_f32_16x16x32_bf16 v[86:89], v[120:123], v[224:227], v[86:89]
	v_mfma_f32_16x16x32_bf16 v[90:93], v[152:155], v[224:227], v[90:93]
	v_mfma_f32_16x16x32_bf16 v[94:97], v[156:159], v[196:199], v[96:99]
	v_mfma_f32_16x16x32_bf16 v[98:101], v[188:191], v[196:199], v[100:103]
	v_mfma_f32_16x16x32_bf16 v[102:105], v[156:159], v[204:207], v[104:107]
	v_mfma_f32_16x16x32_bf16 v[38:41], v[188:191], v[204:207], v[38:41]
	v_mfma_f32_16x16x32_bf16 v[42:45], v[156:159], v[212:215], v[42:45]
	v_mfma_f32_16x16x32_bf16 v[46:49], v[188:191], v[212:215], v[46:49]
	v_mfma_f32_16x16x32_bf16 v[50:53], v[156:159], v[220:223], v[50:53]
	v_mfma_f32_16x16x32_bf16 v[54:57], v[188:191], v[220:223], v[54:57]
	v_mfma_f32_16x16x32_bf16 v[94:97], v[184:187], v[200:203], v[94:97]
	v_mfma_f32_16x16x32_bf16 v[98:101], v[192:195], v[200:203], v[98:101]
	v_mfma_f32_16x16x32_bf16 v[102:105], v[184:187], v[208:211], v[102:105]
	v_mfma_f32_16x16x32_bf16 v[38:41], v[192:195], v[208:211], v[38:41]
	v_mfma_f32_16x16x32_bf16 v[42:45], v[184:187], v[216:219], v[42:45]
	v_mfma_f32_16x16x32_bf16 v[46:49], v[192:195], v[216:219], v[46:49]
	v_mfma_f32_16x16x32_bf16 v[50:53], v[184:187], v[224:227], v[50:53]
	v_mfma_f32_16x16x32_bf16 v[54:57], v[192:195], v[224:227], v[54:57]
	s_barrier
	s_mov_b32 m0, s71
	v_lshl_add_u64 v[106:107], v[0:1], 0, s[22:23]
	s_add_u32 s76, s38, 0x1a00
	ds_read_b128 v[196:199], v140 offset:16384
	ds_read_b128 v[200:203], v140 offset:17408
	ds_read_b128 v[204:207], v140 offset:18432
	ds_read_b128 v[208:211], v140 offset:19456
	ds_read_b128 v[212:215], v140 offset:20480
	ds_read_b128 v[216:219], v140 offset:21504
	ds_read_b128 v[220:223], v140 offset:22528
	ds_read_b128 v[224:227], v140 offset:23552
	global_load_lds_dwordx4 v[106:107], off
	v_lshl_add_u64 v[106:107], v[2:3], 0, s[22:23]
	s_mov_b32 m0, s68
	s_addc_u32 s77, s39, 0
	global_load_lds_dwordx4 v[106:107], off
	v_lshl_add_u64 v[106:107], s[76:77], 0, v[130:131]
	s_mov_b32 m0, s69
	s_nop 0
	global_load_lds_dwordx4 v[106:107], off
	v_lshl_add_u64 v[106:107], s[76:77], 0, v[134:135]
	s_mov_b32 m0, s70
	s_nop 0
	global_load_lds_dwordx4 v[106:107], off
	v_lshl_add_u64 v[106:107], v[4:5], 0, s[22:23]
	s_mov_b32 m0, s47
	s_nop 0
	global_load_lds_dwordx4 v[106:107], off
	v_lshl_add_u64 v[106:107], v[6:7], 0, s[22:23]
	s_mov_b32 m0, s48
	s_nop 0
	global_load_lds_dwordx4 v[106:107], off
	s_waitcnt vmcnt(8)
	s_waitcnt lgkmcnt(0)
	s_barrier
	s_waitcnt lgkmcnt(0)
	v_mfma_f32_16x16x32_bf16 v[10:13], v[116:119], v[220:223], v[10:13]
	v_mfma_f32_16x16x32_bf16 v[14:17], v[124:127], v[220:223], v[14:17]
	v_mfma_f32_16x16x32_bf16 v[160:163], v[116:119], v[196:199], v[160:163]
	v_mfma_f32_16x16x32_bf16 v[164:167], v[124:127], v[196:199], v[164:167]
	v_mfma_f32_16x16x32_bf16 v[168:171], v[116:119], v[204:207], v[168:171]
	v_mfma_f32_16x16x32_bf16 v[172:175], v[124:127], v[204:207], v[172:175]
	v_mfma_f32_16x16x32_bf16 v[176:179], v[116:119], v[212:215], v[176:179]
	v_mfma_f32_16x16x32_bf16 v[180:183], v[124:127], v[212:215], v[180:183]
	v_mfma_f32_16x16x32_bf16 v[10:13], v[120:123], v[224:227], v[10:13]
	v_mfma_f32_16x16x32_bf16 v[14:17], v[152:155], v[224:227], v[14:17]
	v_mfma_f32_16x16x32_bf16 v[160:163], v[120:123], v[200:203], v[160:163]
	v_mfma_f32_16x16x32_bf16 v[164:167], v[152:155], v[200:203], v[164:167]
	v_mfma_f32_16x16x32_bf16 v[168:171], v[120:123], v[208:211], v[168:171]
	v_mfma_f32_16x16x32_bf16 v[172:175], v[152:155], v[208:211], v[172:175]
	v_mfma_f32_16x16x32_bf16 v[176:179], v[120:123], v[216:219], v[176:179]
	v_mfma_f32_16x16x32_bf16 v[180:183], v[152:155], v[216:219], v[180:183]
	v_mfma_f32_16x16x32_bf16 v[18:21], v[156:159], v[196:199], v[18:21]
	v_mfma_f32_16x16x32_bf16 v[30:33], v[188:191], v[196:199], v[30:33]
	v_mfma_f32_16x16x32_bf16 v[34:37], v[156:159], v[204:207], v[34:37]
	v_mfma_f32_16x16x32_bf16 v[58:61], v[188:191], v[204:207], v[58:61]
	v_mfma_f32_16x16x32_bf16 v[106:109], v[156:159], v[212:215], v[108:111]
	v_mfma_f32_16x16x32_bf16 v[110:113], v[188:191], v[212:215], v[112:115]
	v_mfma_f32_16x16x32_bf16 v[22:25], v[156:159], v[220:223], v[22:25]
	v_mfma_f32_16x16x32_bf16 v[26:29], v[188:191], v[220:223], v[26:29]
	v_mfma_f32_16x16x32_bf16 v[18:21], v[184:187], v[200:203], v[18:21]
	v_mfma_f32_16x16x32_bf16 v[30:33], v[192:195], v[200:203], v[30:33]
	v_mfma_f32_16x16x32_bf16 v[34:37], v[184:187], v[208:211], v[34:37]
	v_mfma_f32_16x16x32_bf16 v[58:61], v[192:195], v[208:211], v[58:61]
	v_mfma_f32_16x16x32_bf16 v[106:109], v[184:187], v[216:219], v[106:109]
	v_mfma_f32_16x16x32_bf16 v[110:113], v[192:195], v[216:219], v[110:113]
	v_mfma_f32_16x16x32_bf16 v[22:25], v[184:187], v[224:227], v[22:25]
	v_mfma_f32_16x16x32_bf16 v[26:29], v[192:195], v[224:227], v[26:29]
	s_barrier
	ds_read_b128 v[114:117], v8
	ds_read_b128 v[118:121], v8 offset:1024
	ds_read_b128 v[122:125], v8 offset:2048
	ds_read_b128 v[152:155], v8 offset:3072
	ds_read_b128 v[156:159], v9
	ds_read_b128 v[184:187], v9 offset:1024
	ds_read_b128 v[188:191], v9 offset:2048
	ds_read_b128 v[192:195], v9 offset:3072
	s_add_u32 s76, s36, 0x18200
	s_addc_u32 s77, s37, 0
	s_mov_b32 m0, s50
	v_lshl_add_u64 v[126:127], s[76:77], 0, v[128:129]
	ds_read_b128 v[196:199], v140 offset:32768
	ds_read_b128 v[200:203], v140 offset:33792
	ds_read_b128 v[204:207], v140 offset:34816
	ds_read_b128 v[208:211], v140 offset:35840
	ds_read_b128 v[212:215], v140 offset:36864
	ds_read_b128 v[216:219], v140 offset:37888
	ds_read_b128 v[220:223], v140 offset:38912
	ds_read_b128 v[224:227], v140 offset:39936
	global_load_lds_dwordx4 v[126:127], off
	v_lshl_add_u64 v[126:127], s[76:77], 0, v[132:133]
	s_mov_b32 m0, s51
	s_nop 0
	global_load_lds_dwordx4 v[126:127], off
	s_waitcnt vmcnt(8)
	s_waitcnt lgkmcnt(0)
	s_barrier
	s_waitcnt lgkmcnt(0)
	v_mfma_f32_16x16x32_bf16 v[62:65], v[114:117], v[196:199], v[62:65]
	v_mfma_f32_16x16x32_bf16 v[66:69], v[122:125], v[196:199], v[66:69]
	v_mfma_f32_16x16x32_bf16 v[70:73], v[114:117], v[204:207], v[70:73]
	v_mfma_f32_16x16x32_bf16 v[74:77], v[122:125], v[204:207], v[74:77]
	v_mfma_f32_16x16x32_bf16 v[78:81], v[114:117], v[212:215], v[78:81]
	v_mfma_f32_16x16x32_bf16 v[82:85], v[122:125], v[212:215], v[82:85]
	v_mfma_f32_16x16x32_bf16 v[86:89], v[114:117], v[220:223], v[86:89]
	v_mfma_f32_16x16x32_bf16 v[90:93], v[122:125], v[220:223], v[90:93]
	v_mfma_f32_16x16x32_bf16 v[62:65], v[118:121], v[200:203], v[62:65]
	v_mfma_f32_16x16x32_bf16 v[66:69], v[152:155], v[200:203], v[66:69]
	v_mfma_f32_16x16x32_bf16 v[70:73], v[118:121], v[208:211], v[70:73]
	v_mfma_f32_16x16x32_bf16 v[74:77], v[152:155], v[208:211], v[74:77]
	v_mfma_f32_16x16x32_bf16 v[78:81], v[118:121], v[216:219], v[78:81]
	v_mfma_f32_16x16x32_bf16 v[82:85], v[152:155], v[216:219], v[82:85]
	v_mfma_f32_16x16x32_bf16 v[86:89], v[118:121], v[224:227], v[86:89]
	v_mfma_f32_16x16x32_bf16 v[90:93], v[152:155], v[224:227], v[90:93]
	v_mfma_f32_16x16x32_bf16 v[94:97], v[156:159], v[196:199], v[94:97]
	v_mfma_f32_16x16x32_bf16 v[98:101], v[188:191], v[196:199], v[98:101]
	v_mfma_f32_16x16x32_bf16 v[102:105], v[156:159], v[204:207], v[102:105]
	v_mfma_f32_16x16x32_bf16 v[38:41], v[188:191], v[204:207], v[38:41]
	v_mfma_f32_16x16x32_bf16 v[42:45], v[156:159], v[212:215], v[42:45]
	v_mfma_f32_16x16x32_bf16 v[46:49], v[188:191], v[212:215], v[46:49]
	v_mfma_f32_16x16x32_bf16 v[50:53], v[156:159], v[220:223], v[50:53]
	v_mfma_f32_16x16x32_bf16 v[54:57], v[188:191], v[220:223], v[54:57]
	v_mfma_f32_16x16x32_bf16 v[94:97], v[184:187], v[200:203], v[94:97]
	v_mfma_f32_16x16x32_bf16 v[98:101], v[192:195], v[200:203], v[98:101]
	v_mfma_f32_16x16x32_bf16 v[102:105], v[184:187], v[208:211], v[102:105]
	v_mfma_f32_16x16x32_bf16 v[38:41], v[192:195], v[208:211], v[38:41]
	v_mfma_f32_16x16x32_bf16 v[42:45], v[184:187], v[216:219], v[42:45]
	v_mfma_f32_16x16x32_bf16 v[46:49], v[192:195], v[216:219], v[46:49]
	v_mfma_f32_16x16x32_bf16 v[50:53], v[184:187], v[224:227], v[50:53]
	v_mfma_f32_16x16x32_bf16 v[54:57], v[192:195], v[224:227], v[54:57]
	s_barrier
	s_mov_b32 m0, s75
	v_lshl_add_u64 v[0:1], v[0:1], 0, s[24:25]
	s_add_u32 s38, s38, 0x1a80
	ds_read_b128 v[196:199], v140 offset:49152
	ds_read_b128 v[200:203], v140 offset:50176
	ds_read_b128 v[204:207], v140 offset:51200
	ds_read_b128 v[208:211], v140 offset:52224
	ds_read_b128 v[212:215], v140 offset:53248
	ds_read_b128 v[216:219], v140 offset:54272
	ds_read_b128 v[220:223], v140 offset:55296
	ds_read_b128 v[224:227], v140 offset:56320
	global_load_lds_dwordx4 v[0:1], off
	v_lshl_add_u64 v[0:1], v[2:3], 0, s[24:25]
	s_mov_b32 m0, s72
	s_addc_u32 s39, s39, 0
	global_load_lds_dwordx4 v[0:1], off
	v_lshl_add_u64 v[0:1], s[38:39], 0, v[130:131]
	s_mov_b32 m0, s73
	s_nop 0
	global_load_lds_dwordx4 v[0:1], off
	v_lshl_add_u64 v[0:1], s[38:39], 0, v[134:135]
	s_mov_b32 m0, s74
	s_nop 0
	global_load_lds_dwordx4 v[0:1], off
	v_lshl_add_u64 v[0:1], v[4:5], 0, s[24:25]
	s_mov_b32 m0, s53
	s_nop 0
	global_load_lds_dwordx4 v[0:1], off
	v_lshl_add_u64 v[0:1], v[6:7], 0, s[24:25]
	s_mov_b32 m0, s54
	s_nop 0
	global_load_lds_dwordx4 v[0:1], off
	s_waitcnt vmcnt(8)
	s_waitcnt lgkmcnt(0)
	s_barrier
	s_waitcnt lgkmcnt(0)
	v_mfma_f32_16x16x32_bf16 v[0:3], v[114:117], v[196:199], v[160:163]
	v_mfma_f32_16x16x32_bf16 v[4:7], v[122:125], v[196:199], v[164:167]
	v_mfma_f32_16x16x32_bf16 v[10:13], v[114:117], v[220:223], v[10:13]
	v_mfma_f32_16x16x32_bf16 v[14:17], v[122:125], v[220:223], v[14:17]
	v_mfma_f32_16x16x32_bf16 v[0:3], v[118:121], v[200:203], v[0:3]
	v_mfma_f32_16x16x32_bf16 v[4:7], v[152:155], v[200:203], v[4:7]
	v_mfma_f32_16x16x32_bf16 v[160:163], v[114:117], v[204:207], v[168:171]
	v_mfma_f32_16x16x32_bf16 v[164:167], v[122:125], v[204:207], v[172:175]
	v_mfma_f32_16x16x32_bf16 v[168:171], v[114:117], v[212:215], v[176:179]
	v_mfma_f32_16x16x32_bf16 v[172:175], v[122:125], v[212:215], v[180:183]
	v_mfma_f32_16x16x32_bf16 v[10:13], v[118:121], v[224:227], v[10:13]
	v_mfma_f32_16x16x32_bf16 v[14:17], v[152:155], v[224:227], v[14:17]
	v_mfma_f32_16x16x32_bf16 v[160:163], v[118:121], v[208:211], v[160:163]
	v_mfma_f32_16x16x32_bf16 v[164:167], v[152:155], v[208:211], v[164:167]
	v_mfma_f32_16x16x32_bf16 v[168:171], v[118:121], v[216:219], v[168:171]
	v_mfma_f32_16x16x32_bf16 v[172:175], v[152:155], v[216:219], v[172:175]
	v_mfma_f32_16x16x32_bf16 v[18:21], v[156:159], v[196:199], v[18:21]
	v_mfma_f32_16x16x32_bf16 v[30:33], v[188:191], v[196:199], v[30:33]
	v_mfma_f32_16x16x32_bf16 v[34:37], v[156:159], v[204:207], v[34:37]
	v_mfma_f32_16x16x32_bf16 v[58:61], v[188:191], v[204:207], v[58:61]
	v_mfma_f32_16x16x32_bf16 v[106:109], v[156:159], v[212:215], v[106:109]
	v_mfma_f32_16x16x32_bf16 v[110:113], v[188:191], v[212:215], v[110:113]
	v_mfma_f32_16x16x32_bf16 v[22:25], v[156:159], v[220:223], v[22:25]
	v_mfma_f32_16x16x32_bf16 v[26:29], v[188:191], v[220:223], v[26:29]
	v_mfma_f32_16x16x32_bf16 v[18:21], v[184:187], v[200:203], v[18:21]
	v_mfma_f32_16x16x32_bf16 v[30:33], v[192:195], v[200:203], v[30:33]
	v_mfma_f32_16x16x32_bf16 v[34:37], v[184:187], v[208:211], v[34:37]
	v_mfma_f32_16x16x32_bf16 v[58:61], v[192:195], v[208:211], v[58:61]
	v_mfma_f32_16x16x32_bf16 v[106:109], v[184:187], v[216:219], v[106:109]
	v_mfma_f32_16x16x32_bf16 v[110:113], v[192:195], v[216:219], v[110:113]
	v_mfma_f32_16x16x32_bf16 v[22:25], v[184:187], v[224:227], v[22:25]
	v_mfma_f32_16x16x32_bf16 v[26:29], v[192:195], v[224:227], v[26:29]
	s_barrier
	ds_read_b128 v[114:117], v149
	ds_read_b128 v[118:121], v149 offset:1024
	ds_read_b128 v[122:125], v149 offset:2048
	ds_read_b128 v[152:155], v149 offset:3072
	ds_read_b128 v[156:159], v150
	ds_read_b128 v[176:179], v150 offset:1024
	ds_read_b128 v[180:183], v150 offset:2048
	ds_read_b128 v[184:187], v150 offset:3072
	s_add_u32 s36, s36, 0x18280
	s_addc_u32 s37, s37, 0
	s_mov_b32 m0, s62
	v_lshl_add_u64 v[126:127], s[36:37], 0, v[128:129]
	ds_read_b128 v[188:191], v140
	ds_read_b128 v[192:195], v140 offset:1024
	ds_read_b128 v[196:199], v140 offset:2048
	ds_read_b128 v[200:203], v140 offset:3072
	ds_read_b128 v[204:207], v140 offset:4096
	ds_read_b128 v[208:211], v140 offset:5120
	ds_read_b128 v[212:215], v140 offset:6144
	ds_read_b128 v[216:219], v140 offset:7168
	global_load_lds_dwordx4 v[126:127], off
	v_lshl_add_u64 v[126:127], s[36:37], 0, v[132:133]
	s_mov_b32 m0, s63
	s_nop 0
	global_load_lds_dwordx4 v[126:127], off
	s_waitcnt vmcnt(8)
	s_waitcnt lgkmcnt(0)
	s_barrier
	s_waitcnt lgkmcnt(0)
	v_mfma_f32_16x16x32_bf16 v[82:85], v[122:125], v[204:207], v[82:85]
	v_mfma_f32_16x16x32_bf16 v[220:223], v[152:155], v[208:211], v[82:85]
	v_mfma_f32_16x16x32_bf16 v[82:85], v[114:117], v[212:215], v[86:89]
	v_mfma_f32_16x16x32_bf16 v[62:65], v[114:117], v[188:191], v[62:65]
	v_mfma_f32_16x16x32_bf16 v[66:69], v[122:125], v[188:191], v[66:69]
	v_mfma_f32_16x16x32_bf16 v[70:73], v[114:117], v[196:199], v[70:73]
	v_mfma_f32_16x16x32_bf16 v[74:77], v[122:125], v[196:199], v[74:77]
	v_mfma_f32_16x16x32_bf16 v[78:81], v[114:117], v[204:207], v[78:81]
	v_mfma_f32_16x16x32_bf16 v[224:227], v[118:121], v[216:219], v[82:85]
	v_mfma_f32_16x16x32_bf16 v[82:85], v[122:125], v[212:215], v[90:93]
	v_mfma_f32_16x16x32_bf16 v[62:65], v[118:121], v[192:195], v[62:65]
	v_mfma_f32_16x16x32_bf16 v[66:69], v[152:155], v[192:195], v[66:69]
	v_mfma_f32_16x16x32_bf16 v[70:73], v[118:121], v[200:203], v[70:73]
	v_mfma_f32_16x16x32_bf16 v[74:77], v[152:155], v[200:203], v[74:77]
	v_mfma_f32_16x16x32_bf16 v[78:81], v[118:121], v[208:211], v[78:81]
	v_mfma_f32_16x16x32_bf16 v[88:91], v[152:155], v[216:219], v[82:85]
	v_mfma_f32_16x16x32_bf16 v[82:85], v[156:159], v[188:191], v[94:97]
	v_mfma_f32_16x16x32_bf16 v[92:95], v[176:179], v[192:195], v[82:85]
	v_mfma_f32_16x16x32_bf16 v[82:85], v[180:183], v[188:191], v[98:101]
	v_mfma_f32_16x16x32_bf16 v[38:41], v[180:183], v[196:199], v[38:41]
	v_mfma_f32_16x16x32_bf16 v[42:45], v[156:159], v[204:207], v[42:45]
	v_mfma_f32_16x16x32_bf16 v[46:49], v[180:183], v[204:207], v[46:49]
	v_mfma_f32_16x16x32_bf16 v[50:53], v[156:159], v[212:215], v[50:53]
	v_mfma_f32_16x16x32_bf16 v[54:57], v[180:183], v[212:215], v[54:57]
	v_mfma_f32_16x16x32_bf16 v[188:191], v[184:187], v[192:195], v[82:85]
	v_mfma_f32_16x16x32_bf16 v[82:85], v[156:159], v[196:199], v[102:105]
	v_mfma_f32_16x16x32_bf16 v[38:41], v[184:187], v[200:203], v[38:41]
	v_mfma_f32_16x16x32_bf16 v[42:45], v[176:179], v[208:211], v[42:45]
	v_mfma_f32_16x16x32_bf16 v[46:49], v[184:187], v[208:211], v[46:49]
	v_mfma_f32_16x16x32_bf16 v[50:53], v[176:179], v[216:219], v[50:53]
	v_mfma_f32_16x16x32_bf16 v[54:57], v[184:187], v[216:219], v[54:57]
	v_mfma_f32_16x16x32_bf16 v[192:195], v[176:179], v[200:203], v[82:85]
	s_barrier
	s_mov_b32 m0, s71
	v_lshl_add_u64 v[136:137], s[28:29], 0, v[130:131]
	s_add_u32 s36, s28, 0x1800
	ds_read_b128 v[82:85], v140 offset:16384
	ds_read_b128 v[96:99], v140 offset:17408
	ds_read_b128 v[100:103], v140 offset:18432
	ds_read_b128 v[196:199], v140 offset:19456
	ds_read_b128 v[200:203], v140 offset:20480
	ds_read_b128 v[204:207], v140 offset:21504
	ds_read_b128 v[208:211], v140 offset:22528
	ds_read_b128 v[212:215], v140 offset:23552
	global_load_lds_dwordx4 v[136:137], off
	v_lshl_add_u64 v[142:143], s[28:29], 0, v[134:135]
	s_mov_b32 m0, s68
	s_addc_u32 s37, s29, 0
	global_load_lds_dwordx4 v[142:143], off
	v_lshl_add_u64 v[86:87], s[36:37], 0, v[130:131]
	s_mov_b32 m0, s69
	v_lshl_add_u64 v[144:145], s[26:27], 0, v[128:129]
	global_load_lds_dwordx4 v[86:87], off
	v_lshl_add_u64 v[86:87], s[36:37], 0, v[134:135]
	s_mov_b32 m0, s70
	v_lshl_add_u64 v[146:147], s[26:27], 0, v[132:133]
	global_load_lds_dwordx4 v[86:87], off
	s_mov_b32 m0, s47
	s_nop 0
	global_load_lds_dwordx4 v[144:145], off
	s_mov_b32 m0, s48
	s_nop 0
	global_load_lds_dwordx4 v[146:147], off
	s_waitcnt vmcnt(8)
	s_waitcnt lgkmcnt(0)
	s_barrier
	s_waitcnt lgkmcnt(0)
	v_mfma_f32_16x16x32_bf16 v[0:3], v[114:117], v[82:85], v[0:3]
	v_mfma_f32_16x16x32_bf16 v[4:7], v[122:125], v[82:85], v[4:7]
	v_mfma_f32_16x16x32_bf16 v[10:13], v[114:117], v[208:211], v[10:13]
	v_mfma_f32_16x16x32_bf16 v[0:3], v[118:121], v[96:99], v[0:3]
	v_mfma_f32_16x16x32_bf16 v[4:7], v[152:155], v[96:99], v[4:7]
	v_mfma_f32_16x16x32_bf16 v[160:163], v[114:117], v[100:103], v[160:163]
	v_mfma_f32_16x16x32_bf16 v[164:167], v[122:125], v[100:103], v[164:167]
	v_mfma_f32_16x16x32_bf16 v[168:171], v[114:117], v[200:203], v[168:171]
	v_mfma_f32_16x16x32_bf16 v[172:175], v[122:125], v[200:203], v[172:175]
	v_mfma_f32_16x16x32_bf16 v[10:13], v[118:121], v[212:215], v[10:13]
	v_mfma_f32_16x16x32_bf16 v[14:17], v[122:125], v[208:211], v[14:17]
	v_mfma_f32_16x16x32_bf16 v[160:163], v[118:121], v[196:199], v[160:163]
	v_mfma_f32_16x16x32_bf16 v[164:167], v[152:155], v[196:199], v[164:167]
	v_mfma_f32_16x16x32_bf16 v[168:171], v[118:121], v[204:207], v[168:171]
	v_mfma_f32_16x16x32_bf16 v[172:175], v[152:155], v[204:207], v[172:175]
	v_mfma_f32_16x16x32_bf16 v[152:155], v[152:155], v[212:215], v[14:17]
	v_mfma_f32_16x16x32_bf16 v[14:17], v[156:159], v[82:85], v[18:21]
	v_mfma_f32_16x16x32_bf16 v[216:219], v[176:179], v[96:99], v[14:17]
	v_mfma_f32_16x16x32_bf16 v[14:17], v[180:183], v[82:85], v[30:33]
	v_mfma_f32_16x16x32_bf16 v[228:231], v[184:187], v[96:99], v[14:17]
	v_mfma_f32_16x16x32_bf16 v[14:17], v[156:159], v[100:103], v[34:37]
	v_mfma_f32_16x16x32_bf16 v[232:235], v[176:179], v[196:199], v[14:17]
	v_mfma_f32_16x16x32_bf16 v[14:17], v[180:183], v[100:103], v[58:61]
	v_mfma_f32_16x16x32_bf16 v[196:199], v[184:187], v[196:199], v[14:17]
	v_mfma_f32_16x16x32_bf16 v[14:17], v[156:159], v[200:203], v[106:109]
	v_mfma_f32_16x16x32_bf16 v[236:239], v[176:179], v[204:207], v[14:17]
	v_mfma_f32_16x16x32_bf16 v[14:17], v[180:183], v[200:203], v[110:113]
	v_mfma_f32_16x16x32_bf16 v[200:203], v[184:187], v[204:207], v[14:17]
	v_mfma_f32_16x16x32_bf16 v[14:17], v[156:159], v[208:211], v[22:25]
	v_mfma_f32_16x16x32_bf16 v[156:159], v[176:179], v[212:215], v[14:17]
	v_mfma_f32_16x16x32_bf16 v[14:17], v[180:183], v[208:211], v[26:29]
	v_mfma_f32_16x16x32_bf16 v[176:179], v[184:187], v[212:215], v[14:17]
	s_barrier
	ds_read_b128 v[24:27], v8
	ds_read_b128 v[28:31], v8 offset:1024
	ds_read_b128 v[58:61], v8 offset:2048
	ds_read_b128 v[180:183], v8 offset:3072
	ds_read_b128 v[184:187], v9
	ds_read_b128 v[204:207], v9 offset:1024
	ds_read_b128 v[208:211], v9 offset:2048
	ds_read_b128 v[212:215], v9 offset:3072
	s_add_u32 s36, s26, 0x18000
	s_addc_u32 s37, s27, 0
	s_mov_b32 m0, s50
	v_lshl_add_u64 v[8:9], s[36:37], 0, v[128:129]
	ds_read_b128 v[14:17], v140 offset:32768
	ds_read_b128 v[18:21], v140 offset:33792
	ds_read_b128 v[32:35], v140 offset:34816
	ds_read_b128 v[108:111], v140 offset:35840
	ds_read_b128 v[240:243], v140 offset:36864
	ds_read_b128 v[244:247], v140 offset:37888
	ds_read_b128 v[248:251], v140 offset:38912
	ds_read_b128 v[252:255], v140 offset:39936
	global_load_lds_dwordx4 v[8:9], off
	v_lshl_add_u64 v[8:9], s[36:37], 0, v[132:133]
	s_mov_b32 m0, s51
	s_nop 0
	global_load_lds_dwordx4 v[8:9], off
	s_waitcnt vmcnt(8)
	s_waitcnt lgkmcnt(0)
	s_barrier
	s_waitcnt lgkmcnt(0)
	v_mfma_f32_16x16x32_bf16 v[62:65], v[24:27], v[14:17], v[62:65]
	v_mfma_f32_16x16x32_bf16 v[112:115], v[28:31], v[18:21], v[62:65]
	v_mfma_f32_16x16x32_bf16 v[62:65], v[58:61], v[14:17], v[66:69]
	v_mfma_f32_16x16x32_bf16 v[116:119], v[180:183], v[18:21], v[62:65]
	v_mfma_f32_16x16x32_bf16 v[62:65], v[24:27], v[32:35], v[70:73]
	v_mfma_f32_16x16x32_bf16 v[96:99], v[28:31], v[108:111], v[62:65]
	v_mfma_f32_16x16x32_bf16 v[62:65], v[58:61], v[32:35], v[74:77]
	v_mfma_f32_16x16x32_bf16 v[100:103], v[180:183], v[108:111], v[62:65]
	v_mfma_f32_16x16x32_bf16 v[62:65], v[24:27], v[240:243], v[78:81]
	v_mfma_f32_16x16x32_bf16 v[80:83], v[28:31], v[244:247], v[62:65]
	v_mfma_f32_16x16x32_bf16 v[62:65], v[58:61], v[240:243], v[220:223]
	v_mfma_f32_16x16x32_bf16 v[84:87], v[180:183], v[244:247], v[62:65]
	v_mfma_f32_16x16x32_bf16 v[62:65], v[24:27], v[248:251], v[224:227]
	v_mfma_f32_16x16x32_bf16 v[68:71], v[58:61], v[248:251], v[88:91]
	v_mfma_f32_16x16x32_bf16 v[64:67], v[28:31], v[252:255], v[62:65]
	v_mfma_f32_16x16x32_bf16 v[68:71], v[180:183], v[252:255], v[68:71]
	v_mfma_f32_16x16x32_bf16 v[72:75], v[184:187], v[14:17], v[92:95]
	v_mfma_f32_16x16x32_bf16 v[14:17], v[208:211], v[14:17], v[188:191]
	v_mfma_f32_16x16x32_bf16 v[124:127], v[212:215], v[18:21], v[14:17]
	v_mfma_f32_16x16x32_bf16 v[14:17], v[184:187], v[32:35], v[192:195]
	v_mfma_f32_16x16x32_bf16 v[104:107], v[204:207], v[108:111], v[14:17]
	v_mfma_f32_16x16x32_bf16 v[14:17], v[208:211], v[32:35], v[38:41]
	v_mfma_f32_16x16x32_bf16 v[108:111], v[212:215], v[108:111], v[14:17]
	v_mfma_f32_16x16x32_bf16 v[14:17], v[184:187], v[240:243], v[42:45]
	v_mfma_f32_16x16x32_bf16 v[88:91], v[204:207], v[244:247], v[14:17]
	v_mfma_f32_16x16x32_bf16 v[14:17], v[208:211], v[240:243], v[46:49]
	v_mfma_f32_16x16x32_bf16 v[92:95], v[212:215], v[244:247], v[14:17]
	v_mfma_f32_16x16x32_bf16 v[14:17], v[184:187], v[248:251], v[50:53]
	v_mfma_f32_16x16x32_bf16 v[120:123], v[204:207], v[18:21], v[72:75]
	v_mfma_f32_16x16x32_bf16 v[72:75], v[204:207], v[252:255], v[14:17]
	v_mfma_f32_16x16x32_bf16 v[14:17], v[208:211], v[248:251], v[54:57]
	v_mfma_f32_16x16x32_bf16 v[76:79], v[212:215], v[252:255], v[14:17]
	s_barrier
	s_mov_b32 m0, s75
	v_lshl_add_u64 v[8:9], v[136:137], 0, s[14:15]
	s_add_u32 s36, s28, 0x1880
	ds_read_b128 v[40:43], v140 offset:49152
	ds_read_b128 v[44:47], v140 offset:50176
	ds_read_b128 v[188:191], v140 offset:51200
	ds_read_b128 v[192:195], v140 offset:52224
	ds_read_b128 v[220:223], v140 offset:53248
	ds_read_b128 v[224:227], v140 offset:54272
	ds_read_b128 v[240:243], v140 offset:55296
	ds_read_b128 v[244:247], v140 offset:56320
	global_load_lds_dwordx4 v[8:9], off
	v_lshl_add_u64 v[8:9], v[142:143], 0, s[14:15]
	s_mov_b32 m0, s72
	s_addc_u32 s37, s29, 0
	global_load_lds_dwordx4 v[8:9], off
	v_lshl_add_u64 v[8:9], s[36:37], 0, v[130:131]
	s_mov_b32 m0, s73
	s_nop 0
	global_load_lds_dwordx4 v[8:9], off
	v_lshl_add_u64 v[8:9], s[36:37], 0, v[134:135]
	s_mov_b32 m0, s74
	s_nop 0
	global_load_lds_dwordx4 v[8:9], off
	v_lshl_add_u64 v[8:9], v[144:145], 0, s[14:15]
	s_mov_b32 m0, s53
	s_nop 0
	global_load_lds_dwordx4 v[8:9], off
	v_lshl_add_u64 v[8:9], v[146:147], 0, s[14:15]
	s_mov_b32 m0, s54
	s_nop 0
	global_load_lds_dwordx4 v[8:9], off
	s_waitcnt vmcnt(8)
	s_waitcnt lgkmcnt(0)
	s_barrier
	s_waitcnt lgkmcnt(0)
	v_mfma_f32_16x16x32_bf16 v[0:3], v[24:27], v[40:43], v[0:3]
	v_mfma_f32_16x16x32_bf16 v[48:51], v[28:31], v[44:47], v[0:3]
	v_mfma_f32_16x16x32_bf16 v[0:3], v[58:61], v[40:43], v[4:7]
	v_mfma_f32_16x16x32_bf16 v[52:55], v[180:183], v[44:47], v[0:3]
	v_mfma_f32_16x16x32_bf16 v[0:3], v[24:27], v[188:191], v[160:163]
	v_mfma_f32_16x16x32_bf16 v[32:35], v[28:31], v[192:195], v[0:3]
	v_mfma_f32_16x16x32_bf16 v[0:3], v[58:61], v[188:191], v[164:167]
	v_mfma_f32_16x16x32_bf16 v[36:39], v[180:183], v[192:195], v[0:3]
	v_mfma_f32_16x16x32_bf16 v[0:3], v[24:27], v[220:223], v[168:171]
	v_mfma_f32_16x16x32_bf16 v[16:19], v[28:31], v[224:227], v[0:3]
	v_mfma_f32_16x16x32_bf16 v[0:3], v[58:61], v[220:223], v[172:175]
	v_mfma_f32_16x16x32_bf16 v[20:23], v[180:183], v[224:227], v[0:3]
	v_mfma_f32_16x16x32_bf16 v[0:3], v[24:27], v[240:243], v[10:13]
	v_mfma_f32_16x16x32_bf16 v[4:7], v[58:61], v[240:243], v[152:155]
	v_mfma_f32_16x16x32_bf16 v[0:3], v[28:31], v[244:247], v[0:3]
	v_mfma_f32_16x16x32_bf16 v[4:7], v[180:183], v[244:247], v[4:7]
	v_mfma_f32_16x16x32_bf16 v[8:11], v[184:187], v[40:43], v[216:219]
	v_mfma_f32_16x16x32_bf16 v[56:59], v[204:207], v[44:47], v[8:11]
	v_mfma_f32_16x16x32_bf16 v[8:11], v[208:211], v[40:43], v[228:231]
	v_mfma_f32_16x16x32_bf16 v[60:63], v[212:215], v[44:47], v[8:11]
	v_mfma_f32_16x16x32_bf16 v[8:11], v[184:187], v[188:191], v[232:235]
	v_mfma_f32_16x16x32_bf16 v[40:43], v[204:207], v[192:195], v[8:11]
	v_mfma_f32_16x16x32_bf16 v[8:11], v[208:211], v[188:191], v[196:199]
	v_mfma_f32_16x16x32_bf16 v[44:47], v[212:215], v[192:195], v[8:11]
	v_mfma_f32_16x16x32_bf16 v[8:11], v[184:187], v[220:223], v[236:239]
	v_mfma_f32_16x16x32_bf16 v[24:27], v[204:207], v[224:227], v[8:11]
	v_mfma_f32_16x16x32_bf16 v[8:11], v[208:211], v[220:223], v[200:203]
	v_mfma_f32_16x16x32_bf16 v[28:31], v[212:215], v[224:227], v[8:11]
	v_mfma_f32_16x16x32_bf16 v[8:11], v[184:187], v[240:243], v[156:159]
	v_mfma_f32_16x16x32_bf16 v[12:15], v[208:211], v[240:243], v[176:179]
	v_mfma_f32_16x16x32_bf16 v[8:11], v[204:207], v[244:247], v[8:11]
	v_mfma_f32_16x16x32_bf16 v[12:15], v[212:215], v[244:247], v[12:15]
	s_barrier
	s_andn2_b64 vcc, exec, s[16:17]
	s_cbranch_vccnz .LBB0_1070
	s_barrier

.LBB0_1243:
	ds_read_b128 v[144:147], v155
	ds_read_b128 v[158:161], v155 offset:1024
	ds_read_b128 v[162:165], v155 offset:2048
	ds_read_b128 v[166:169], v155 offset:3072
	ds_read_b128 v[170:173], v156
	ds_read_b128 v[174:177], v156 offset:1024
	ds_read_b128 v[178:181], v156 offset:2048
	ds_read_b128 v[182:185], v156 offset:3072
	s_add_u32 s30, s28, 0x100
	s_addc_u32 s31, s29, 0
	s_cmp_eq_u32 s61, 12
	s_cselect_b32 s39, s23, s31
	s_cselect_b32 s38, s22, s30
	s_cselect_b32 s37, s25, s21
	s_cselect_b32 s36, s24, s19
	v_lshl_add_u64 v[150:151], s[28:29], 0, v[138:139]
	s_add_i32 m0, s27, 0xc000
	ds_read_b128 v[186:189], v157
	ds_read_b128 v[190:193], v157 offset:1024
	ds_read_b128 v[194:197], v157 offset:2048
	ds_read_b128 v[198:201], v157 offset:3072
	ds_read_b128 v[202:205], v157 offset:4096
	ds_read_b128 v[206:209], v157 offset:5120
	ds_read_b128 v[210:213], v157 offset:6144
	ds_read_b128 v[214:217], v157 offset:7168
	global_load_lds_dwordx4 v[150:151], off
	v_lshl_add_u64 v[150:151], s[28:29], 0, v[136:137]
	s_add_i32 m0, s27, 0xe000
	s_nop 0
	global_load_lds_dwordx4 v[150:151], off
	s_waitcnt vmcnt(8)
	s_waitcnt lgkmcnt(0)
	s_barrier
	s_waitcnt lgkmcnt(0)
	v_mfma_f32_16x16x32_bf16 v[124:127], v[144:147], v[186:189], v[124:127]
	v_mfma_f32_16x16x32_bf16 v[120:123], v[162:165], v[186:189], v[120:123]
	v_mfma_f32_16x16x32_bf16 v[116:119], v[144:147], v[194:197], v[116:119]
	v_mfma_f32_16x16x32_bf16 v[112:115], v[162:165], v[194:197], v[112:115]
	v_mfma_f32_16x16x32_bf16 v[108:111], v[144:147], v[202:205], v[108:111]
	v_mfma_f32_16x16x32_bf16 v[100:103], v[162:165], v[202:205], v[100:103]
	v_mfma_f32_16x16x32_bf16 v[92:95], v[144:147], v[210:213], v[92:95]
	v_mfma_f32_16x16x32_bf16 v[80:83], v[162:165], v[210:213], v[80:83]
	v_mfma_f32_16x16x32_bf16 v[124:127], v[158:161], v[190:193], v[124:127]
	v_mfma_f32_16x16x32_bf16 v[120:123], v[166:169], v[190:193], v[120:123]
	v_mfma_f32_16x16x32_bf16 v[116:119], v[158:161], v[198:201], v[116:119]
	v_mfma_f32_16x16x32_bf16 v[112:115], v[166:169], v[198:201], v[112:115]
	v_mfma_f32_16x16x32_bf16 v[108:111], v[158:161], v[206:209], v[108:111]
	v_mfma_f32_16x16x32_bf16 v[100:103], v[166:169], v[206:209], v[100:103]
	v_mfma_f32_16x16x32_bf16 v[92:95], v[158:161], v[214:217], v[92:95]
	v_mfma_f32_16x16x32_bf16 v[80:83], v[166:169], v[214:217], v[80:83]
	v_mfma_f32_16x16x32_bf16 v[104:107], v[170:173], v[186:189], v[104:107]
	v_mfma_f32_16x16x32_bf16 v[96:99], v[178:181], v[186:189], v[96:99]
	v_mfma_f32_16x16x32_bf16 v[88:91], v[170:173], v[194:197], v[88:91]
	v_mfma_f32_16x16x32_bf16 v[84:87], v[178:181], v[194:197], v[84:87]
	v_mfma_f32_16x16x32_bf16 v[76:79], v[170:173], v[202:205], v[76:79]
	v_mfma_f32_16x16x32_bf16 v[72:75], v[178:181], v[202:205], v[72:75]
	v_mfma_f32_16x16x32_bf16 v[68:71], v[170:173], v[210:213], v[68:71]
	v_mfma_f32_16x16x32_bf16 v[64:67], v[178:181], v[210:213], v[64:67]
	v_mfma_f32_16x16x32_bf16 v[104:107], v[174:177], v[190:193], v[104:107]
	v_mfma_f32_16x16x32_bf16 v[96:99], v[182:185], v[190:193], v[96:99]
	v_mfma_f32_16x16x32_bf16 v[88:91], v[174:177], v[198:201], v[88:91]
	v_mfma_f32_16x16x32_bf16 v[84:87], v[182:185], v[198:201], v[84:87]
	v_mfma_f32_16x16x32_bf16 v[76:79], v[174:177], v[206:209], v[76:79]
	v_mfma_f32_16x16x32_bf16 v[72:75], v[182:185], v[206:209], v[72:75]
	v_mfma_f32_16x16x32_bf16 v[68:71], v[174:177], v[214:217], v[68:71]
	v_mfma_f32_16x16x32_bf16 v[64:67], v[182:185], v[214:217], v[64:67]
	s_barrier
	s_add_i32 s28, s57, s48
	v_lshl_add_u64 v[150:151], s[36:37], 0, v[132:133]
	s_mov_b32 m0, s28
	ds_read_b128 v[186:189], v157 offset:16384
	ds_read_b128 v[190:193], v157 offset:17408
	ds_read_b128 v[194:197], v157 offset:18432
	ds_read_b128 v[198:201], v157 offset:19456
	ds_read_b128 v[202:205], v157 offset:20480
	ds_read_b128 v[206:209], v157 offset:21504
	ds_read_b128 v[210:213], v157 offset:22528
	ds_read_b128 v[214:217], v157 offset:23552
	global_load_lds_dwordx4 v[150:151], off
	s_add_i32 m0, s28, 0x2000
	s_add_u32 s28, s36, 0x40000
	v_lshl_add_u64 v[218:219], s[36:37], 0, v[128:129]
	s_addc_u32 s29, s37, 0
	s_add_i32 s62, s58, s48
	global_load_lds_dwordx4 v[218:219], off
	v_lshl_add_u64 v[220:221], s[28:29], 0, v[132:133]
	s_mov_b32 m0, s62
	v_lshl_add_u64 v[222:223], s[38:39], 0, v[130:131]
	global_load_lds_dwordx4 v[220:221], off
	v_lshl_add_u64 v[220:221], s[28:29], 0, v[128:129]
	s_add_i32 m0, s62, 0x2000
	s_nop 0
	global_load_lds_dwordx4 v[220:221], off
	v_lshl_add_u64 v[220:221], s[38:39], 0, v[134:135]
	s_mov_b32 m0, s27
	s_nop 0
	global_load_lds_dwordx4 v[220:221], off
	s_mov_b32 m0, s50
	s_nop 0
	global_load_lds_dwordx4 v[222:223], off
	s_waitcnt vmcnt(8)
	s_waitcnt lgkmcnt(0)
	s_barrier
	s_waitcnt lgkmcnt(0)
	v_mfma_f32_16x16x32_bf16 v[60:63], v[144:147], v[186:189], v[60:63]
	v_mfma_f32_16x16x32_bf16 v[56:59], v[162:165], v[186:189], v[56:59]
	v_mfma_f32_16x16x32_bf16 v[48:51], v[144:147], v[194:197], v[48:51]
	v_mfma_f32_16x16x32_bf16 v[40:43], v[162:165], v[194:197], v[40:43]
	v_mfma_f32_16x16x32_bf16 v[32:35], v[144:147], v[202:205], v[32:35]
	v_mfma_f32_16x16x32_bf16 v[24:27], v[162:165], v[202:205], v[24:27]
	v_mfma_f32_16x16x32_bf16 v[16:19], v[144:147], v[210:213], v[16:19]
	v_mfma_f32_16x16x32_bf16 v[8:11], v[162:165], v[210:213], v[8:11]
	v_mfma_f32_16x16x32_bf16 v[60:63], v[158:161], v[190:193], v[60:63]
	v_mfma_f32_16x16x32_bf16 v[56:59], v[166:169], v[190:193], v[56:59]
	v_mfma_f32_16x16x32_bf16 v[48:51], v[158:161], v[198:201], v[48:51]
	v_mfma_f32_16x16x32_bf16 v[40:43], v[166:169], v[198:201], v[40:43]
	v_mfma_f32_16x16x32_bf16 v[32:35], v[158:161], v[206:209], v[32:35]
	v_mfma_f32_16x16x32_bf16 v[24:27], v[166:169], v[206:209], v[24:27]
	v_mfma_f32_16x16x32_bf16 v[16:19], v[158:161], v[214:217], v[16:19]
	v_mfma_f32_16x16x32_bf16 v[8:11], v[166:169], v[214:217], v[8:11]
	v_mfma_f32_16x16x32_bf16 v[52:55], v[170:173], v[186:189], v[52:55]
	v_mfma_f32_16x16x32_bf16 v[44:47], v[178:181], v[186:189], v[44:47]
	v_mfma_f32_16x16x32_bf16 v[36:39], v[170:173], v[194:197], v[36:39]
	v_mfma_f32_16x16x32_bf16 v[28:31], v[178:181], v[194:197], v[28:31]
	v_mfma_f32_16x16x32_bf16 v[20:23], v[170:173], v[202:205], v[20:23]
	v_mfma_f32_16x16x32_bf16 v[12:15], v[178:181], v[202:205], v[12:15]
	v_mfma_f32_16x16x32_bf16 v[4:7], v[170:173], v[210:213], v[4:7]
	v_mfma_f32_16x16x32_bf16 v[0:3], v[178:181], v[210:213], v[0:3]
	v_mfma_f32_16x16x32_bf16 v[52:55], v[174:177], v[190:193], v[52:55]
	v_mfma_f32_16x16x32_bf16 v[44:47], v[182:185], v[190:193], v[44:47]
	v_mfma_f32_16x16x32_bf16 v[36:39], v[174:177], v[198:201], v[36:39]
	v_mfma_f32_16x16x32_bf16 v[28:31], v[182:185], v[198:201], v[28:31]
	v_mfma_f32_16x16x32_bf16 v[20:23], v[174:177], v[206:209], v[20:23]
	v_mfma_f32_16x16x32_bf16 v[12:15], v[182:185], v[206:209], v[12:15]
	v_mfma_f32_16x16x32_bf16 v[4:7], v[174:177], v[214:217], v[4:7]
	v_mfma_f32_16x16x32_bf16 v[0:3], v[182:185], v[214:217], v[0:3]
	s_barrier
	s_add_i32 s62, 0, 0x18000
	v_add_u32_e32 v148, s62, v153
	s_add_i32 s63, 0, 0x1c000
	ds_read_b128 v[144:147], v148
	ds_read_b128 v[158:161], v148 offset:1024
	ds_read_b128 v[162:165], v148 offset:2048
	ds_read_b128 v[166:169], v148 offset:3072
	v_add_u32_e32 v148, s63, v153
	ds_read_b128 v[170:173], v148
	ds_read_b128 v[174:177], v148 offset:1024
	ds_read_b128 v[178:181], v148 offset:2048
	ds_read_b128 v[182:185], v148 offset:3072
	s_add_u32 s28, s38, 0x40000
	s_addc_u32 s29, s39, 0
	s_mov_b32 m0, s51
	v_lshl_add_u64 v[224:225], s[28:29], 0, v[134:135]
	ds_read_b128 v[186:189], v157 offset:32768
	ds_read_b128 v[190:193], v157 offset:33792
	ds_read_b128 v[194:197], v157 offset:34816
	ds_read_b128 v[198:201], v157 offset:35840
	ds_read_b128 v[202:205], v157 offset:36864
	ds_read_b128 v[206:209], v157 offset:37888
	ds_read_b128 v[210:213], v157 offset:38912
	ds_read_b128 v[214:217], v157 offset:39936
	global_load_lds_dwordx4 v[224:225], off
	v_lshl_add_u64 v[224:225], s[28:29], 0, v[130:131]
	s_mov_b32 m0, s52
	s_nop 0
	global_load_lds_dwordx4 v[224:225], off
	s_waitcnt vmcnt(8)
	s_waitcnt lgkmcnt(0)
	s_barrier
	s_waitcnt lgkmcnt(0)
	v_mfma_f32_16x16x32_bf16 v[124:127], v[144:147], v[186:189], v[124:127]
	v_mfma_f32_16x16x32_bf16 v[120:123], v[162:165], v[186:189], v[120:123]
	v_mfma_f32_16x16x32_bf16 v[116:119], v[144:147], v[194:197], v[116:119]
	v_mfma_f32_16x16x32_bf16 v[112:115], v[162:165], v[194:197], v[112:115]
	v_mfma_f32_16x16x32_bf16 v[108:111], v[144:147], v[202:205], v[108:111]
	v_mfma_f32_16x16x32_bf16 v[100:103], v[162:165], v[202:205], v[100:103]
	v_mfma_f32_16x16x32_bf16 v[92:95], v[144:147], v[210:213], v[92:95]
	v_mfma_f32_16x16x32_bf16 v[80:83], v[162:165], v[210:213], v[80:83]
	v_mfma_f32_16x16x32_bf16 v[124:127], v[158:161], v[190:193], v[124:127]
	v_mfma_f32_16x16x32_bf16 v[120:123], v[166:169], v[190:193], v[120:123]
	v_mfma_f32_16x16x32_bf16 v[116:119], v[158:161], v[198:201], v[116:119]
	v_mfma_f32_16x16x32_bf16 v[112:115], v[166:169], v[198:201], v[112:115]
	v_mfma_f32_16x16x32_bf16 v[108:111], v[158:161], v[206:209], v[108:111]
	v_mfma_f32_16x16x32_bf16 v[100:103], v[166:169], v[206:209], v[100:103]
	v_mfma_f32_16x16x32_bf16 v[92:95], v[158:161], v[214:217], v[92:95]
	v_mfma_f32_16x16x32_bf16 v[80:83], v[166:169], v[214:217], v[80:83]
	v_mfma_f32_16x16x32_bf16 v[104:107], v[170:173], v[186:189], v[104:107]
	v_mfma_f32_16x16x32_bf16 v[96:99], v[178:181], v[186:189], v[96:99]
	v_mfma_f32_16x16x32_bf16 v[88:91], v[170:173], v[194:197], v[88:91]
	v_mfma_f32_16x16x32_bf16 v[84:87], v[178:181], v[194:197], v[84:87]
	v_mfma_f32_16x16x32_bf16 v[76:79], v[170:173], v[202:205], v[76:79]
	v_mfma_f32_16x16x32_bf16 v[72:75], v[178:181], v[202:205], v[72:75]
	v_mfma_f32_16x16x32_bf16 v[68:71], v[170:173], v[210:213], v[68:71]
	v_mfma_f32_16x16x32_bf16 v[64:67], v[178:181], v[210:213], v[64:67]
	v_mfma_f32_16x16x32_bf16 v[104:107], v[174:177], v[190:193], v[104:107]
	v_mfma_f32_16x16x32_bf16 v[96:99], v[182:185], v[190:193], v[96:99]
	v_mfma_f32_16x16x32_bf16 v[88:91], v[174:177], v[198:201], v[88:91]
	v_mfma_f32_16x16x32_bf16 v[84:87], v[182:185], v[198:201], v[84:87]
	v_mfma_f32_16x16x32_bf16 v[76:79], v[174:177], v[206:209], v[76:79]
	v_mfma_f32_16x16x32_bf16 v[72:75], v[182:185], v[206:209], v[72:75]
	v_mfma_f32_16x16x32_bf16 v[68:71], v[174:177], v[214:217], v[68:71]
	v_mfma_f32_16x16x32_bf16 v[64:67], v[182:185], v[214:217], v[64:67]
	s_barrier
	s_add_i32 s28, s62, s48
	v_lshl_add_u64 v[150:151], v[150:151], 0, s[14:15]
	s_mov_b32 m0, s28
	ds_read_b128 v[186:189], v157 offset:49152
	ds_read_b128 v[190:193], v157 offset:50176
	ds_read_b128 v[194:197], v157 offset:51200
	ds_read_b128 v[198:201], v157 offset:52224
	ds_read_b128 v[202:205], v157 offset:53248
	ds_read_b128 v[206:209], v157 offset:54272
	ds_read_b128 v[210:213], v157 offset:55296
	ds_read_b128 v[214:217], v157 offset:56320
	global_load_lds_dwordx4 v[150:151], off
	s_add_i32 m0, s28, 0x2000
	s_add_u32 s28, s36, 0x40080
	v_lshl_add_u64 v[150:151], v[218:219], 0, s[14:15]
	s_addc_u32 s29, s37, 0
	s_add_i32 s36, s63, s48
	global_load_lds_dwordx4 v[150:151], off
	v_lshl_add_u64 v[150:151], s[28:29], 0, v[132:133]
	s_mov_b32 m0, s36
	s_nop 0
	global_load_lds_dwordx4 v[150:151], off
	v_lshl_add_u64 v[150:151], s[28:29], 0, v[128:129]
	s_add_i32 m0, s36, 0x2000
	s_nop 0
	global_load_lds_dwordx4 v[150:151], off
	v_lshl_add_u64 v[150:151], v[220:221], 0, s[14:15]
	s_mov_b32 m0, s53
	s_nop 0
	global_load_lds_dwordx4 v[150:151], off
	v_lshl_add_u64 v[150:151], v[222:223], 0, s[14:15]
	s_mov_b32 m0, s54
	s_nop 0
	global_load_lds_dwordx4 v[150:151], off
	s_waitcnt vmcnt(8)
	s_waitcnt lgkmcnt(0)
	s_barrier
	s_waitcnt lgkmcnt(0)
	v_mfma_f32_16x16x32_bf16 v[60:63], v[144:147], v[186:189], v[60:63]
	v_mfma_f32_16x16x32_bf16 v[56:59], v[162:165], v[186:189], v[56:59]
	v_mfma_f32_16x16x32_bf16 v[48:51], v[144:147], v[194:197], v[48:51]
	v_mfma_f32_16x16x32_bf16 v[40:43], v[162:165], v[194:197], v[40:43]
	v_mfma_f32_16x16x32_bf16 v[32:35], v[144:147], v[202:205], v[32:35]
	v_mfma_f32_16x16x32_bf16 v[24:27], v[162:165], v[202:205], v[24:27]
	v_mfma_f32_16x16x32_bf16 v[16:19], v[144:147], v[210:213], v[16:19]
	v_mfma_f32_16x16x32_bf16 v[8:11], v[162:165], v[210:213], v[8:11]
	v_mfma_f32_16x16x32_bf16 v[60:63], v[158:161], v[190:193], v[60:63]
	v_mfma_f32_16x16x32_bf16 v[56:59], v[166:169], v[190:193], v[56:59]
	v_mfma_f32_16x16x32_bf16 v[48:51], v[158:161], v[198:201], v[48:51]
	v_mfma_f32_16x16x32_bf16 v[40:43], v[166:169], v[198:201], v[40:43]
	v_mfma_f32_16x16x32_bf16 v[32:35], v[158:161], v[206:209], v[32:35]
	v_mfma_f32_16x16x32_bf16 v[24:27], v[166:169], v[206:209], v[24:27]
	v_mfma_f32_16x16x32_bf16 v[16:19], v[158:161], v[214:217], v[16:19]
	v_mfma_f32_16x16x32_bf16 v[8:11], v[166:169], v[214:217], v[8:11]
	v_mfma_f32_16x16x32_bf16 v[52:55], v[170:173], v[186:189], v[52:55]
	v_mfma_f32_16x16x32_bf16 v[44:47], v[178:181], v[186:189], v[44:47]
	v_mfma_f32_16x16x32_bf16 v[36:39], v[170:173], v[194:197], v[36:39]
	v_mfma_f32_16x16x32_bf16 v[28:31], v[178:181], v[194:197], v[28:31]
	v_mfma_f32_16x16x32_bf16 v[20:23], v[170:173], v[202:205], v[20:23]
	v_mfma_f32_16x16x32_bf16 v[12:15], v[178:181], v[202:205], v[12:15]
	v_mfma_f32_16x16x32_bf16 v[4:7], v[170:173], v[210:213], v[4:7]
	v_mfma_f32_16x16x32_bf16 v[0:3], v[178:181], v[210:213], v[0:3]
	v_mfma_f32_16x16x32_bf16 v[52:55], v[174:177], v[190:193], v[52:55]
	v_mfma_f32_16x16x32_bf16 v[44:47], v[182:185], v[190:193], v[44:47]
	v_mfma_f32_16x16x32_bf16 v[36:39], v[174:177], v[198:201], v[36:39]
	v_mfma_f32_16x16x32_bf16 v[28:31], v[182:185], v[198:201], v[28:31]
	v_mfma_f32_16x16x32_bf16 v[20:23], v[174:177], v[206:209], v[20:23]
	v_mfma_f32_16x16x32_bf16 v[12:15], v[182:185], v[206:209], v[12:15]
	v_mfma_f32_16x16x32_bf16 v[4:7], v[174:177], v[214:217], v[4:7]
	v_mfma_f32_16x16x32_bf16 v[0:3], v[182:185], v[214:217], v[0:3]
	s_barrier
	s_add_i32 s61, s61, 2
	s_add_u32 s19, s19, 0x100
	s_addc_u32 s21, s21, 0
	s_cmp_gt_u32 s61, 13
	s_mov_b64 s[28:29], s[30:31]
	s_cbranch_scc0 .LBB0_1243
	s_and_b64 vcc, exec, s[16:17]
	s_cbranch_vccz .LBB0_1246
	s_barrier

.LBB0_1405:
	ds_read_b128 v[150:153], v147
	ds_read_b128 v[154:157], v147 offset:1024
	ds_read_b128 v[158:161], v147 offset:2048
	ds_read_b128 v[162:165], v147 offset:3072
	ds_read_b128 v[166:169], v148
	ds_read_b128 v[170:173], v148 offset:1024
	ds_read_b128 v[174:177], v148 offset:2048
	ds_read_b128 v[178:181], v148 offset:3072
	s_add_u32 s22, s20, 0x100
	s_addc_u32 s23, s21, 0
	s_cmp_eq_u32 s61, 2
	s_cselect_b32 s27, s17, s23
	s_cselect_b32 s26, s16, s22
	s_cselect_b32 s25, s19, s60
	s_cselect_b32 s24, s18, s59
	v_lshl_add_u64 v[214:215], s[20:21], 0, v[138:139]
	s_add_i32 m0, s42, 0xc000
	ds_read_b128 v[182:185], v149
	ds_read_b128 v[186:189], v149 offset:1024
	ds_read_b128 v[190:193], v149 offset:2048
	ds_read_b128 v[194:197], v149 offset:3072
	ds_read_b128 v[198:201], v149 offset:4096
	ds_read_b128 v[202:205], v149 offset:5120
	ds_read_b128 v[206:209], v149 offset:6144
	ds_read_b128 v[210:213], v149 offset:7168
	global_load_lds_dwordx4 v[214:215], off
	v_lshl_add_u64 v[214:215], s[20:21], 0, v[136:137]
	s_add_i32 m0, s42, 0xe000
	s_nop 0
	global_load_lds_dwordx4 v[214:215], off
	s_waitcnt vmcnt(8)
	s_waitcnt lgkmcnt(0)
	s_barrier
	s_waitcnt lgkmcnt(0)
	v_mfma_f32_16x16x32_bf16 v[124:127], v[150:153], v[182:185], v[124:127]
	v_mfma_f32_16x16x32_bf16 v[120:123], v[158:161], v[182:185], v[120:123]
	v_mfma_f32_16x16x32_bf16 v[112:115], v[150:153], v[190:193], v[112:115]
	v_mfma_f32_16x16x32_bf16 v[104:107], v[158:161], v[190:193], v[104:107]
	v_mfma_f32_16x16x32_bf16 v[96:99], v[150:153], v[198:201], v[96:99]
	v_mfma_f32_16x16x32_bf16 v[88:91], v[158:161], v[198:201], v[88:91]
	v_mfma_f32_16x16x32_bf16 v[80:83], v[150:153], v[206:209], v[80:83]
	v_mfma_f32_16x16x32_bf16 v[72:75], v[158:161], v[206:209], v[72:75]
	v_mfma_f32_16x16x32_bf16 v[124:127], v[154:157], v[186:189], v[124:127]
	v_mfma_f32_16x16x32_bf16 v[120:123], v[162:165], v[186:189], v[120:123]
	v_mfma_f32_16x16x32_bf16 v[112:115], v[154:157], v[194:197], v[112:115]
	v_mfma_f32_16x16x32_bf16 v[104:107], v[162:165], v[194:197], v[104:107]
	v_mfma_f32_16x16x32_bf16 v[96:99], v[154:157], v[202:205], v[96:99]
	v_mfma_f32_16x16x32_bf16 v[88:91], v[162:165], v[202:205], v[88:91]
	v_mfma_f32_16x16x32_bf16 v[80:83], v[154:157], v[210:213], v[80:83]
	v_mfma_f32_16x16x32_bf16 v[72:75], v[162:165], v[210:213], v[72:75]
	v_mfma_f32_16x16x32_bf16 v[116:119], v[166:169], v[182:185], v[116:119]
	v_mfma_f32_16x16x32_bf16 v[108:111], v[174:177], v[182:185], v[108:111]
	v_mfma_f32_16x16x32_bf16 v[100:103], v[166:169], v[190:193], v[100:103]
	v_mfma_f32_16x16x32_bf16 v[92:95], v[174:177], v[190:193], v[92:95]
	v_mfma_f32_16x16x32_bf16 v[84:87], v[166:169], v[198:201], v[84:87]
	v_mfma_f32_16x16x32_bf16 v[76:79], v[174:177], v[198:201], v[76:79]
	v_mfma_f32_16x16x32_bf16 v[68:71], v[166:169], v[206:209], v[68:71]
	v_mfma_f32_16x16x32_bf16 v[64:67], v[174:177], v[206:209], v[64:67]
	v_mfma_f32_16x16x32_bf16 v[116:119], v[170:173], v[186:189], v[116:119]
	v_mfma_f32_16x16x32_bf16 v[108:111], v[178:181], v[186:189], v[108:111]
	v_mfma_f32_16x16x32_bf16 v[100:103], v[170:173], v[194:197], v[100:103]
	v_mfma_f32_16x16x32_bf16 v[92:95], v[178:181], v[194:197], v[92:95]
	v_mfma_f32_16x16x32_bf16 v[84:87], v[170:173], v[202:205], v[84:87]
	v_mfma_f32_16x16x32_bf16 v[76:79], v[178:181], v[202:205], v[76:79]
	v_mfma_f32_16x16x32_bf16 v[68:71], v[170:173], v[210:213], v[68:71]
	v_mfma_f32_16x16x32_bf16 v[64:67], v[178:181], v[210:213], v[64:67]
	s_barrier
	s_add_i32 s20, s52, s39
	v_lshl_add_u64 v[214:215], s[24:25], 0, v[132:133]
	s_mov_b32 m0, s20
	ds_read_b128 v[182:185], v149 offset:16384
	ds_read_b128 v[186:189], v149 offset:17408
	ds_read_b128 v[190:193], v149 offset:18432
	ds_read_b128 v[194:197], v149 offset:19456
	ds_read_b128 v[198:201], v149 offset:20480
	ds_read_b128 v[202:205], v149 offset:21504
	ds_read_b128 v[206:209], v149 offset:22528
	ds_read_b128 v[210:213], v149 offset:23552
	global_load_lds_dwordx4 v[214:215], off
	s_add_i32 m0, s20, 0x2000
	s_add_u32 s20, s24, 0x1800
	v_lshl_add_u64 v[216:217], s[24:25], 0, v[128:129]
	s_addc_u32 s21, s25, 0
	s_add_i32 s62, s53, s39
	global_load_lds_dwordx4 v[216:217], off
	v_lshl_add_u64 v[218:219], s[20:21], 0, v[132:133]
	s_mov_b32 m0, s62
	v_lshl_add_u64 v[220:221], s[26:27], 0, v[130:131]
	global_load_lds_dwordx4 v[218:219], off
	v_lshl_add_u64 v[218:219], s[20:21], 0, v[128:129]
	s_add_i32 m0, s62, 0x2000
	s_nop 0
	global_load_lds_dwordx4 v[218:219], off
	v_lshl_add_u64 v[218:219], s[26:27], 0, v[134:135]
	s_mov_b32 m0, s42
	s_nop 0
	global_load_lds_dwordx4 v[218:219], off
	s_mov_b32 m0, s43
	s_nop 0
	global_load_lds_dwordx4 v[220:221], off
	s_waitcnt vmcnt(8)
	s_waitcnt lgkmcnt(0)
	s_barrier
	s_waitcnt lgkmcnt(0)
	v_mfma_f32_16x16x32_bf16 v[60:63], v[150:153], v[182:185], v[60:63]
	v_mfma_f32_16x16x32_bf16 v[56:59], v[158:161], v[182:185], v[56:59]
	v_mfma_f32_16x16x32_bf16 v[48:51], v[150:153], v[190:193], v[48:51]
	v_mfma_f32_16x16x32_bf16 v[40:43], v[158:161], v[190:193], v[40:43]
	v_mfma_f32_16x16x32_bf16 v[32:35], v[150:153], v[198:201], v[32:35]
	v_mfma_f32_16x16x32_bf16 v[24:27], v[158:161], v[198:201], v[24:27]
	v_mfma_f32_16x16x32_bf16 v[16:19], v[150:153], v[206:209], v[16:19]
	v_mfma_f32_16x16x32_bf16 v[8:11], v[158:161], v[206:209], v[8:11]
	v_mfma_f32_16x16x32_bf16 v[60:63], v[154:157], v[186:189], v[60:63]
	v_mfma_f32_16x16x32_bf16 v[56:59], v[162:165], v[186:189], v[56:59]
	v_mfma_f32_16x16x32_bf16 v[48:51], v[154:157], v[194:197], v[48:51]
	v_mfma_f32_16x16x32_bf16 v[40:43], v[162:165], v[194:197], v[40:43]
	v_mfma_f32_16x16x32_bf16 v[32:35], v[154:157], v[202:205], v[32:35]
	v_mfma_f32_16x16x32_bf16 v[24:27], v[162:165], v[202:205], v[24:27]
	v_mfma_f32_16x16x32_bf16 v[16:19], v[154:157], v[210:213], v[16:19]
	v_mfma_f32_16x16x32_bf16 v[8:11], v[162:165], v[210:213], v[8:11]
	v_mfma_f32_16x16x32_bf16 v[52:55], v[166:169], v[182:185], v[52:55]
	v_mfma_f32_16x16x32_bf16 v[44:47], v[174:177], v[182:185], v[44:47]
	v_mfma_f32_16x16x32_bf16 v[36:39], v[166:169], v[190:193], v[36:39]
	v_mfma_f32_16x16x32_bf16 v[28:31], v[174:177], v[190:193], v[28:31]
	v_mfma_f32_16x16x32_bf16 v[20:23], v[166:169], v[198:201], v[20:23]
	v_mfma_f32_16x16x32_bf16 v[12:15], v[174:177], v[198:201], v[12:15]
	v_mfma_f32_16x16x32_bf16 v[4:7], v[166:169], v[206:209], v[4:7]
	v_mfma_f32_16x16x32_bf16 v[0:3], v[174:177], v[206:209], v[0:3]
	v_mfma_f32_16x16x32_bf16 v[52:55], v[170:173], v[186:189], v[52:55]
	v_mfma_f32_16x16x32_bf16 v[44:47], v[178:181], v[186:189], v[44:47]
	v_mfma_f32_16x16x32_bf16 v[36:39], v[170:173], v[194:197], v[36:39]
	v_mfma_f32_16x16x32_bf16 v[28:31], v[178:181], v[194:197], v[28:31]
	v_mfma_f32_16x16x32_bf16 v[20:23], v[170:173], v[202:205], v[20:23]
	v_mfma_f32_16x16x32_bf16 v[12:15], v[178:181], v[202:205], v[12:15]
	v_mfma_f32_16x16x32_bf16 v[4:7], v[170:173], v[210:213], v[4:7]
	v_mfma_f32_16x16x32_bf16 v[0:3], v[178:181], v[210:213], v[0:3]
	s_barrier
	s_add_i32 s62, 0, 0x18000
	s_add_i32 s63, 0, 0x1c000
	v_add_u32_e32 v162, s62, v145
	v_add_u32_e32 v178, s63, v145
	ds_read_b128 v[150:153], v162
	ds_read_b128 v[154:157], v162 offset:1024
	ds_read_b128 v[158:161], v162 offset:2048
	ds_read_b128 v[162:165], v162 offset:3072
	ds_read_b128 v[166:169], v178
	ds_read_b128 v[170:173], v178 offset:1024
	ds_read_b128 v[174:177], v178 offset:2048
	ds_read_b128 v[178:181], v178 offset:3072
	s_add_u32 s20, s26, 0x30000
	s_addc_u32 s21, s27, 0
	s_mov_b32 m0, s46
	v_lshl_add_u64 v[222:223], s[20:21], 0, v[134:135]
	ds_read_b128 v[182:185], v149 offset:32768
	ds_read_b128 v[186:189], v149 offset:33792
	ds_read_b128 v[190:193], v149 offset:34816
	ds_read_b128 v[194:197], v149 offset:35840
	ds_read_b128 v[198:201], v149 offset:36864
	ds_read_b128 v[202:205], v149 offset:37888
	ds_read_b128 v[206:209], v149 offset:38912
	ds_read_b128 v[210:213], v149 offset:39936
	global_load_lds_dwordx4 v[222:223], off
	v_lshl_add_u64 v[222:223], s[20:21], 0, v[130:131]
	s_mov_b32 m0, s47
	s_nop 0
	global_load_lds_dwordx4 v[222:223], off
	s_waitcnt vmcnt(8)
	s_waitcnt lgkmcnt(0)
	s_barrier
	s_waitcnt lgkmcnt(0)
	v_mfma_f32_16x16x32_bf16 v[124:127], v[150:153], v[182:185], v[124:127]
	v_mfma_f32_16x16x32_bf16 v[120:123], v[158:161], v[182:185], v[120:123]
	v_mfma_f32_16x16x32_bf16 v[112:115], v[150:153], v[190:193], v[112:115]
	v_mfma_f32_16x16x32_bf16 v[104:107], v[158:161], v[190:193], v[104:107]
	v_mfma_f32_16x16x32_bf16 v[96:99], v[150:153], v[198:201], v[96:99]
	v_mfma_f32_16x16x32_bf16 v[88:91], v[158:161], v[198:201], v[88:91]
	v_mfma_f32_16x16x32_bf16 v[80:83], v[150:153], v[206:209], v[80:83]
	v_mfma_f32_16x16x32_bf16 v[72:75], v[158:161], v[206:209], v[72:75]
	v_mfma_f32_16x16x32_bf16 v[124:127], v[154:157], v[186:189], v[124:127]
	v_mfma_f32_16x16x32_bf16 v[120:123], v[162:165], v[186:189], v[120:123]
	v_mfma_f32_16x16x32_bf16 v[112:115], v[154:157], v[194:197], v[112:115]
	v_mfma_f32_16x16x32_bf16 v[104:107], v[162:165], v[194:197], v[104:107]
	v_mfma_f32_16x16x32_bf16 v[96:99], v[154:157], v[202:205], v[96:99]
	v_mfma_f32_16x16x32_bf16 v[88:91], v[162:165], v[202:205], v[88:91]
	v_mfma_f32_16x16x32_bf16 v[80:83], v[154:157], v[210:213], v[80:83]
	v_mfma_f32_16x16x32_bf16 v[72:75], v[162:165], v[210:213], v[72:75]
	v_mfma_f32_16x16x32_bf16 v[116:119], v[166:169], v[182:185], v[116:119]
	v_mfma_f32_16x16x32_bf16 v[108:111], v[174:177], v[182:185], v[108:111]
	v_mfma_f32_16x16x32_bf16 v[100:103], v[166:169], v[190:193], v[100:103]
	v_mfma_f32_16x16x32_bf16 v[92:95], v[174:177], v[190:193], v[92:95]
	v_mfma_f32_16x16x32_bf16 v[84:87], v[166:169], v[198:201], v[84:87]
	v_mfma_f32_16x16x32_bf16 v[76:79], v[174:177], v[198:201], v[76:79]
	v_mfma_f32_16x16x32_bf16 v[68:71], v[166:169], v[206:209], v[68:71]
	v_mfma_f32_16x16x32_bf16 v[64:67], v[174:177], v[206:209], v[64:67]
	v_mfma_f32_16x16x32_bf16 v[116:119], v[170:173], v[186:189], v[116:119]
	v_mfma_f32_16x16x32_bf16 v[108:111], v[178:181], v[186:189], v[108:111]
	v_mfma_f32_16x16x32_bf16 v[100:103], v[170:173], v[194:197], v[100:103]
	v_mfma_f32_16x16x32_bf16 v[92:95], v[178:181], v[194:197], v[92:95]
	v_mfma_f32_16x16x32_bf16 v[84:87], v[170:173], v[202:205], v[84:87]
	v_mfma_f32_16x16x32_bf16 v[76:79], v[178:181], v[202:205], v[76:79]
	v_mfma_f32_16x16x32_bf16 v[68:71], v[170:173], v[210:213], v[68:71]
	v_mfma_f32_16x16x32_bf16 v[64:67], v[178:181], v[210:213], v[64:67]
	s_barrier
	s_add_i32 s20, s62, s39
	v_lshl_add_u64 v[214:215], v[214:215], 0, s[12:13]
	s_mov_b32 m0, s20
	ds_read_b128 v[182:185], v149 offset:49152
	ds_read_b128 v[186:189], v149 offset:50176
	ds_read_b128 v[190:193], v149 offset:51200
	ds_read_b128 v[194:197], v149 offset:52224
	ds_read_b128 v[198:201], v149 offset:53248
	ds_read_b128 v[202:205], v149 offset:54272
	ds_read_b128 v[206:209], v149 offset:55296
	ds_read_b128 v[210:213], v149 offset:56320
	global_load_lds_dwordx4 v[214:215], off
	s_add_i32 m0, s20, 0x2000
	s_add_u32 s20, s24, 0x1880
	v_lshl_add_u64 v[214:215], v[216:217], 0, s[12:13]
	s_addc_u32 s21, s25, 0
	s_add_i32 s24, s63, s39
	global_load_lds_dwordx4 v[214:215], off
	v_lshl_add_u64 v[214:215], s[20:21], 0, v[132:133]
	s_mov_b32 m0, s24
	s_nop 0
	global_load_lds_dwordx4 v[214:215], off
	v_lshl_add_u64 v[214:215], s[20:21], 0, v[128:129]
	s_add_i32 m0, s24, 0x2000
	s_nop 0
	global_load_lds_dwordx4 v[214:215], off
	v_lshl_add_u64 v[214:215], v[218:219], 0, s[12:13]
	s_mov_b32 m0, s48
	s_nop 0
	global_load_lds_dwordx4 v[214:215], off
	v_lshl_add_u64 v[214:215], v[220:221], 0, s[12:13]
	s_mov_b32 m0, s49
	s_nop 0
	global_load_lds_dwordx4 v[214:215], off
	s_waitcnt vmcnt(8)
	s_waitcnt lgkmcnt(0)
	s_barrier
	s_waitcnt lgkmcnt(0)
	v_mfma_f32_16x16x32_bf16 v[60:63], v[150:153], v[182:185], v[60:63]
	v_mfma_f32_16x16x32_bf16 v[56:59], v[158:161], v[182:185], v[56:59]
	v_mfma_f32_16x16x32_bf16 v[48:51], v[150:153], v[190:193], v[48:51]
	v_mfma_f32_16x16x32_bf16 v[40:43], v[158:161], v[190:193], v[40:43]
	v_mfma_f32_16x16x32_bf16 v[32:35], v[150:153], v[198:201], v[32:35]
	v_mfma_f32_16x16x32_bf16 v[24:27], v[158:161], v[198:201], v[24:27]
	v_mfma_f32_16x16x32_bf16 v[16:19], v[150:153], v[206:209], v[16:19]
	v_mfma_f32_16x16x32_bf16 v[8:11], v[158:161], v[206:209], v[8:11]
	v_mfma_f32_16x16x32_bf16 v[60:63], v[154:157], v[186:189], v[60:63]
	v_mfma_f32_16x16x32_bf16 v[56:59], v[162:165], v[186:189], v[56:59]
	v_mfma_f32_16x16x32_bf16 v[48:51], v[154:157], v[194:197], v[48:51]
	v_mfma_f32_16x16x32_bf16 v[40:43], v[162:165], v[194:197], v[40:43]
	v_mfma_f32_16x16x32_bf16 v[32:35], v[154:157], v[202:205], v[32:35]
	v_mfma_f32_16x16x32_bf16 v[24:27], v[162:165], v[202:205], v[24:27]
	v_mfma_f32_16x16x32_bf16 v[16:19], v[154:157], v[210:213], v[16:19]
	v_mfma_f32_16x16x32_bf16 v[8:11], v[162:165], v[210:213], v[8:11]
	v_mfma_f32_16x16x32_bf16 v[52:55], v[166:169], v[182:185], v[52:55]
	v_mfma_f32_16x16x32_bf16 v[44:47], v[174:177], v[182:185], v[44:47]
	v_mfma_f32_16x16x32_bf16 v[36:39], v[166:169], v[190:193], v[36:39]
	v_mfma_f32_16x16x32_bf16 v[28:31], v[174:177], v[190:193], v[28:31]
	v_mfma_f32_16x16x32_bf16 v[20:23], v[166:169], v[198:201], v[20:23]
	v_mfma_f32_16x16x32_bf16 v[12:15], v[174:177], v[198:201], v[12:15]
	v_mfma_f32_16x16x32_bf16 v[4:7], v[166:169], v[206:209], v[4:7]
	v_mfma_f32_16x16x32_bf16 v[0:3], v[174:177], v[206:209], v[0:3]
	v_mfma_f32_16x16x32_bf16 v[52:55], v[170:173], v[186:189], v[52:55]
	v_mfma_f32_16x16x32_bf16 v[44:47], v[178:181], v[186:189], v[44:47]
	v_mfma_f32_16x16x32_bf16 v[36:39], v[170:173], v[194:197], v[36:39]
	v_mfma_f32_16x16x32_bf16 v[28:31], v[178:181], v[194:197], v[28:31]
	v_mfma_f32_16x16x32_bf16 v[20:23], v[170:173], v[202:205], v[20:23]
	v_mfma_f32_16x16x32_bf16 v[12:15], v[178:181], v[202:205], v[12:15]
	v_mfma_f32_16x16x32_bf16 v[4:7], v[170:173], v[210:213], v[4:7]
	v_mfma_f32_16x16x32_bf16 v[0:3], v[178:181], v[210:213], v[0:3]
	s_barrier
	s_add_i32 s61, s61, 2
	s_add_u32 s59, s59, 0x100
	s_addc_u32 s60, s60, 0
	s_cmp_gt_u32 s61, 3
	s_mov_b64 s[20:21], s[22:23]
	s_cbranch_scc0 .LBB0_1405
	s_and_b64 vcc, exec, s[14:15]
	s_cbranch_vccz .LBB0_1408
	s_barrier

.LBB0_1429:
	s_add_u32 s40, s22, s17
	s_addc_u32 s41, s23, 0
	s_add_u32 s36, s40, 0x100
	s_addc_u32 s37, s41, 0
	s_and_b64 s[30:31], s[28:29], exec
	s_cselect_b32 s37, s19, s37
	s_cselect_b32 s36, s18, s36
	s_add_u32 s17, s24, s17
	s_addc_u32 s30, s25, 0
	s_add_u32 s17, s17, 0x100
	s_addc_u32 s30, s30, 0
	s_and_b64 s[28:29], s[28:29], exec
	s_cselect_b32 s39, s21, s30
	s_cselect_b32 s38, s20, s17
	s_add_u32 s42, s40, 0x30080
	ds_read_b128 v[146:149], v143
	ds_read_b128 v[150:153], v143 offset:1024
	ds_read_b128 v[154:157], v143 offset:2048
	ds_read_b128 v[158:161], v143 offset:3072
	ds_read_b128 v[162:165], v144
	ds_read_b128 v[166:169], v144 offset:1024
	ds_read_b128 v[170:173], v144 offset:2048
	ds_read_b128 v[174:177], v144 offset:3072
	s_addc_u32 s43, s41, 0
	s_add_i32 s76, s62, s53
	s_add_i32 m0, s54, 0xc000
	s_add_i32 s79, s54, 0xe000
	s_add_i32 s73, s76, 0x2000
	s_add_u32 s40, s38, 0x1000
	s_addc_u32 s41, s39, 0
	s_add_i32 s75, s63, s53
	s_add_i32 s74, s75, 0x2000
	s_add_i32 s72, 0, 0x18000
	s_add_i32 s71, 0, 0x1c000
	s_add_u32 s30, s36, 0x30000
	s_addc_u32 s31, s37, 0
	s_add_i32 s70, s72, s53
	s_add_i32 s17, s70, 0x2000
	s_add_u32 s28, s38, 0x1080
	s_addc_u32 s29, s39, 0
	s_add_i32 s78, s71, s53
	s_add_i32 s77, s78, 0x2000
	v_lshl_add_u64 v[210:211], s[42:43], 0, v[128:129]
	ds_read_b128 v[178:181], v145
	ds_read_b128 v[182:185], v145 offset:1024
	ds_read_b128 v[186:189], v145 offset:2048
	ds_read_b128 v[190:193], v145 offset:3072
	ds_read_b128 v[194:197], v145 offset:4096
	ds_read_b128 v[198:201], v145 offset:5120
	ds_read_b128 v[202:205], v145 offset:6144
	ds_read_b128 v[206:209], v145 offset:7168
	global_load_lds_dwordx4 v[210:211], off
	v_lshl_add_u64 v[210:211], s[42:43], 0, v[132:133]
	s_mov_b32 m0, s79
	s_nop 0
	global_load_lds_dwordx4 v[210:211], off
	s_waitcnt vmcnt(8)
	s_waitcnt lgkmcnt(0)
	s_barrier
	s_waitcnt lgkmcnt(0)
	v_mfma_f32_16x16x32_bf16 v[124:127], v[146:149], v[178:181], v[124:127]
	v_mfma_f32_16x16x32_bf16 v[120:123], v[154:157], v[178:181], v[120:123]
	v_mfma_f32_16x16x32_bf16 v[108:111], v[146:149], v[186:189], v[108:111]
	v_mfma_f32_16x16x32_bf16 v[104:107], v[154:157], v[186:189], v[104:107]
	v_mfma_f32_16x16x32_bf16 v[92:95], v[146:149], v[194:197], v[92:95]
	v_mfma_f32_16x16x32_bf16 v[88:91], v[154:157], v[194:197], v[88:91]
	v_mfma_f32_16x16x32_bf16 v[76:79], v[146:149], v[202:205], v[76:79]
	v_mfma_f32_16x16x32_bf16 v[72:75], v[154:157], v[202:205], v[72:75]
	v_mfma_f32_16x16x32_bf16 v[124:127], v[150:153], v[182:185], v[124:127]
	v_mfma_f32_16x16x32_bf16 v[120:123], v[158:161], v[182:185], v[120:123]
	v_mfma_f32_16x16x32_bf16 v[108:111], v[150:153], v[190:193], v[108:111]
	v_mfma_f32_16x16x32_bf16 v[104:107], v[158:161], v[190:193], v[104:107]
	v_mfma_f32_16x16x32_bf16 v[92:95], v[150:153], v[198:201], v[92:95]
	v_mfma_f32_16x16x32_bf16 v[88:91], v[158:161], v[198:201], v[88:91]
	v_mfma_f32_16x16x32_bf16 v[76:79], v[150:153], v[206:209], v[76:79]
	v_mfma_f32_16x16x32_bf16 v[72:75], v[158:161], v[206:209], v[72:75]
	v_mfma_f32_16x16x32_bf16 v[116:119], v[162:165], v[178:181], v[116:119]
	v_mfma_f32_16x16x32_bf16 v[112:115], v[170:173], v[178:181], v[112:115]
	v_mfma_f32_16x16x32_bf16 v[100:103], v[162:165], v[186:189], v[100:103]
	v_mfma_f32_16x16x32_bf16 v[96:99], v[170:173], v[186:189], v[96:99]
	v_mfma_f32_16x16x32_bf16 v[84:87], v[162:165], v[194:197], v[84:87]
	v_mfma_f32_16x16x32_bf16 v[80:83], v[170:173], v[194:197], v[80:83]
	v_mfma_f32_16x16x32_bf16 v[68:71], v[162:165], v[202:205], v[68:71]
	v_mfma_f32_16x16x32_bf16 v[64:67], v[170:173], v[202:205], v[64:67]
	v_mfma_f32_16x16x32_bf16 v[116:119], v[166:169], v[182:185], v[116:119]
	v_mfma_f32_16x16x32_bf16 v[112:115], v[174:177], v[182:185], v[112:115]
	v_mfma_f32_16x16x32_bf16 v[100:103], v[166:169], v[190:193], v[100:103]
	v_mfma_f32_16x16x32_bf16 v[96:99], v[174:177], v[190:193], v[96:99]
	v_mfma_f32_16x16x32_bf16 v[84:87], v[166:169], v[198:201], v[84:87]
	v_mfma_f32_16x16x32_bf16 v[80:83], v[174:177], v[198:201], v[80:83]
	v_mfma_f32_16x16x32_bf16 v[68:71], v[166:169], v[206:209], v[68:71]
	v_mfma_f32_16x16x32_bf16 v[64:67], v[174:177], v[206:209], v[64:67]
	s_barrier
	s_mov_b32 m0, s76
	v_lshl_add_u64 v[210:211], s[38:39], 0, v[130:131]
	ds_read_b128 v[178:181], v145 offset:16384
	ds_read_b128 v[182:185], v145 offset:17408
	ds_read_b128 v[186:189], v145 offset:18432
	ds_read_b128 v[190:193], v145 offset:19456
	ds_read_b128 v[194:197], v145 offset:20480
	ds_read_b128 v[198:201], v145 offset:21504
	ds_read_b128 v[202:205], v145 offset:22528
	ds_read_b128 v[206:209], v145 offset:23552
	global_load_lds_dwordx4 v[210:211], off
	v_lshl_add_u64 v[212:213], s[38:39], 0, v[134:135]
	s_mov_b32 m0, s73
	v_lshl_add_u64 v[214:215], s[40:41], 0, v[130:131]
	global_load_lds_dwordx4 v[212:213], off
	s_mov_b32 m0, s75
	v_lshl_add_u64 v[216:217], s[36:37], 0, v[132:133]
	global_load_lds_dwordx4 v[214:215], off
	v_lshl_add_u64 v[214:215], s[40:41], 0, v[134:135]
	s_mov_b32 m0, s74
	s_nop 0
	global_load_lds_dwordx4 v[214:215], off
	v_lshl_add_u64 v[214:215], s[36:37], 0, v[128:129]
	s_mov_b32 m0, s54
	s_nop 0
	global_load_lds_dwordx4 v[214:215], off
	s_mov_b32 m0, s55
	s_nop 0
	global_load_lds_dwordx4 v[216:217], off
	s_waitcnt vmcnt(8)
	s_waitcnt lgkmcnt(0)
	s_barrier
	s_waitcnt lgkmcnt(0)
	v_mfma_f32_16x16x32_bf16 v[60:63], v[146:149], v[178:181], v[60:63]
	v_mfma_f32_16x16x32_bf16 v[56:59], v[154:157], v[178:181], v[56:59]
	v_mfma_f32_16x16x32_bf16 v[48:51], v[146:149], v[186:189], v[48:51]
	v_mfma_f32_16x16x32_bf16 v[40:43], v[154:157], v[186:189], v[40:43]
	v_mfma_f32_16x16x32_bf16 v[32:35], v[146:149], v[194:197], v[32:35]
	v_mfma_f32_16x16x32_bf16 v[24:27], v[154:157], v[194:197], v[24:27]
	v_mfma_f32_16x16x32_bf16 v[16:19], v[146:149], v[202:205], v[16:19]
	v_mfma_f32_16x16x32_bf16 v[8:11], v[154:157], v[202:205], v[8:11]
	v_mfma_f32_16x16x32_bf16 v[60:63], v[150:153], v[182:185], v[60:63]
	v_mfma_f32_16x16x32_bf16 v[56:59], v[158:161], v[182:185], v[56:59]
	v_mfma_f32_16x16x32_bf16 v[48:51], v[150:153], v[190:193], v[48:51]
	v_mfma_f32_16x16x32_bf16 v[40:43], v[158:161], v[190:193], v[40:43]
	v_mfma_f32_16x16x32_bf16 v[32:35], v[150:153], v[198:201], v[32:35]
	v_mfma_f32_16x16x32_bf16 v[24:27], v[158:161], v[198:201], v[24:27]
	v_mfma_f32_16x16x32_bf16 v[16:19], v[150:153], v[206:209], v[16:19]
	v_mfma_f32_16x16x32_bf16 v[8:11], v[158:161], v[206:209], v[8:11]
	v_mfma_f32_16x16x32_bf16 v[52:55], v[162:165], v[178:181], v[52:55]
	v_mfma_f32_16x16x32_bf16 v[44:47], v[170:173], v[178:181], v[44:47]
	v_mfma_f32_16x16x32_bf16 v[36:39], v[162:165], v[186:189], v[36:39]
	v_mfma_f32_16x16x32_bf16 v[28:31], v[170:173], v[186:189], v[28:31]
	v_mfma_f32_16x16x32_bf16 v[20:23], v[162:165], v[194:197], v[20:23]
	v_mfma_f32_16x16x32_bf16 v[12:15], v[170:173], v[194:197], v[12:15]
	v_mfma_f32_16x16x32_bf16 v[4:7], v[162:165], v[202:205], v[4:7]
	v_mfma_f32_16x16x32_bf16 v[0:3], v[170:173], v[202:205], v[0:3]
	v_mfma_f32_16x16x32_bf16 v[52:55], v[166:169], v[182:185], v[52:55]
	v_mfma_f32_16x16x32_bf16 v[44:47], v[174:177], v[182:185], v[44:47]
	v_mfma_f32_16x16x32_bf16 v[36:39], v[166:169], v[190:193], v[36:39]
	v_mfma_f32_16x16x32_bf16 v[28:31], v[174:177], v[190:193], v[28:31]
	v_mfma_f32_16x16x32_bf16 v[20:23], v[166:169], v[198:201], v[20:23]
	v_mfma_f32_16x16x32_bf16 v[12:15], v[174:177], v[198:201], v[12:15]
	v_mfma_f32_16x16x32_bf16 v[4:7], v[166:169], v[206:209], v[4:7]
	v_mfma_f32_16x16x32_bf16 v[0:3], v[174:177], v[206:209], v[0:3]
	s_barrier
	v_add_u32_e32 v158, s72, v141
	v_add_u32_e32 v174, s71, v141
	ds_read_b128 v[146:149], v158
	ds_read_b128 v[150:153], v158 offset:1024
	ds_read_b128 v[154:157], v158 offset:2048
	ds_read_b128 v[158:161], v158 offset:3072
	ds_read_b128 v[162:165], v174
	ds_read_b128 v[166:169], v174 offset:1024
	ds_read_b128 v[170:173], v174 offset:2048
	ds_read_b128 v[174:177], v174 offset:3072
	s_mov_b32 m0, s56
	v_lshl_add_u64 v[218:219], s[30:31], 0, v[128:129]
	ds_read_b128 v[178:181], v145 offset:32768
	ds_read_b128 v[182:185], v145 offset:33792
	ds_read_b128 v[186:189], v145 offset:34816
	ds_read_b128 v[190:193], v145 offset:35840
	ds_read_b128 v[194:197], v145 offset:36864
	ds_read_b128 v[198:201], v145 offset:37888
	ds_read_b128 v[202:205], v145 offset:38912
	ds_read_b128 v[206:209], v145 offset:39936
	global_load_lds_dwordx4 v[218:219], off
	v_lshl_add_u64 v[218:219], s[30:31], 0, v[132:133]
	s_mov_b32 m0, s57
	s_nop 0
	global_load_lds_dwordx4 v[218:219], off
	s_waitcnt vmcnt(8)
	s_waitcnt lgkmcnt(0)
	s_barrier
	s_waitcnt lgkmcnt(0)
	v_mfma_f32_16x16x32_bf16 v[124:127], v[146:149], v[178:181], v[124:127]
	v_mfma_f32_16x16x32_bf16 v[120:123], v[154:157], v[178:181], v[120:123]
	v_mfma_f32_16x16x32_bf16 v[108:111], v[146:149], v[186:189], v[108:111]
	v_mfma_f32_16x16x32_bf16 v[104:107], v[154:157], v[186:189], v[104:107]
	v_mfma_f32_16x16x32_bf16 v[92:95], v[146:149], v[194:197], v[92:95]
	v_mfma_f32_16x16x32_bf16 v[88:91], v[154:157], v[194:197], v[88:91]
	v_mfma_f32_16x16x32_bf16 v[76:79], v[146:149], v[202:205], v[76:79]
	v_mfma_f32_16x16x32_bf16 v[72:75], v[154:157], v[202:205], v[72:75]
	v_mfma_f32_16x16x32_bf16 v[124:127], v[150:153], v[182:185], v[124:127]
	v_mfma_f32_16x16x32_bf16 v[120:123], v[158:161], v[182:185], v[120:123]
	v_mfma_f32_16x16x32_bf16 v[108:111], v[150:153], v[190:193], v[108:111]
	v_mfma_f32_16x16x32_bf16 v[104:107], v[158:161], v[190:193], v[104:107]
	v_mfma_f32_16x16x32_bf16 v[92:95], v[150:153], v[198:201], v[92:95]
	v_mfma_f32_16x16x32_bf16 v[88:91], v[158:161], v[198:201], v[88:91]
	v_mfma_f32_16x16x32_bf16 v[76:79], v[150:153], v[206:209], v[76:79]
	v_mfma_f32_16x16x32_bf16 v[72:75], v[158:161], v[206:209], v[72:75]
	v_mfma_f32_16x16x32_bf16 v[116:119], v[162:165], v[178:181], v[116:119]
	v_mfma_f32_16x16x32_bf16 v[112:115], v[170:173], v[178:181], v[112:115]
	v_mfma_f32_16x16x32_bf16 v[100:103], v[162:165], v[186:189], v[100:103]
	v_mfma_f32_16x16x32_bf16 v[96:99], v[170:173], v[186:189], v[96:99]
	v_mfma_f32_16x16x32_bf16 v[84:87], v[162:165], v[194:197], v[84:87]
	v_mfma_f32_16x16x32_bf16 v[80:83], v[170:173], v[194:197], v[80:83]
	v_mfma_f32_16x16x32_bf16 v[68:71], v[162:165], v[202:205], v[68:71]
	v_mfma_f32_16x16x32_bf16 v[64:67], v[170:173], v[202:205], v[64:67]
	v_mfma_f32_16x16x32_bf16 v[116:119], v[166:169], v[182:185], v[116:119]
	v_mfma_f32_16x16x32_bf16 v[112:115], v[174:177], v[182:185], v[112:115]
	v_mfma_f32_16x16x32_bf16 v[100:103], v[166:169], v[190:193], v[100:103]
	v_mfma_f32_16x16x32_bf16 v[96:99], v[174:177], v[190:193], v[96:99]
	v_mfma_f32_16x16x32_bf16 v[84:87], v[166:169], v[198:201], v[84:87]
	v_mfma_f32_16x16x32_bf16 v[80:83], v[174:177], v[198:201], v[80:83]
	v_mfma_f32_16x16x32_bf16 v[68:71], v[166:169], v[206:209], v[68:71]
	v_mfma_f32_16x16x32_bf16 v[64:67], v[174:177], v[206:209], v[64:67]
	s_barrier
	s_mov_b32 m0, s70
	v_lshl_add_u64 v[210:211], v[210:211], 0, s[12:13]
	ds_read_b128 v[178:181], v145 offset:49152
	ds_read_b128 v[182:185], v145 offset:50176
	ds_read_b128 v[186:189], v145 offset:51200
	ds_read_b128 v[190:193], v145 offset:52224
	ds_read_b128 v[194:197], v145 offset:53248
	ds_read_b128 v[198:201], v145 offset:54272
	ds_read_b128 v[202:205], v145 offset:55296
	ds_read_b128 v[206:209], v145 offset:56320
	global_load_lds_dwordx4 v[210:211], off
	v_lshl_add_u64 v[210:211], v[212:213], 0, s[12:13]
	s_mov_b32 m0, s17
	s_nop 0
	global_load_lds_dwordx4 v[210:211], off
	v_lshl_add_u64 v[210:211], s[28:29], 0, v[130:131]
	s_mov_b32 m0, s78
	s_nop 0
	global_load_lds_dwordx4 v[210:211], off
	v_lshl_add_u64 v[210:211], s[28:29], 0, v[134:135]
	s_mov_b32 m0, s77
	s_nop 0
	global_load_lds_dwordx4 v[210:211], off
	v_lshl_add_u64 v[210:211], v[214:215], 0, s[12:13]
	s_mov_b32 m0, s59
	s_nop 0
	global_load_lds_dwordx4 v[210:211], off
	v_lshl_add_u64 v[210:211], v[216:217], 0, s[12:13]
	s_mov_b32 m0, s60
	s_nop 0
	global_load_lds_dwordx4 v[210:211], off
	s_waitcnt vmcnt(8)
	s_waitcnt lgkmcnt(0)
	s_barrier
	s_waitcnt lgkmcnt(0)
	v_mfma_f32_16x16x32_bf16 v[60:63], v[146:149], v[178:181], v[60:63]
	v_mfma_f32_16x16x32_bf16 v[56:59], v[154:157], v[178:181], v[56:59]
	v_mfma_f32_16x16x32_bf16 v[48:51], v[146:149], v[186:189], v[48:51]
	v_mfma_f32_16x16x32_bf16 v[40:43], v[154:157], v[186:189], v[40:43]
	v_mfma_f32_16x16x32_bf16 v[32:35], v[146:149], v[194:197], v[32:35]
	v_mfma_f32_16x16x32_bf16 v[24:27], v[154:157], v[194:197], v[24:27]
	v_mfma_f32_16x16x32_bf16 v[16:19], v[146:149], v[202:205], v[16:19]
	v_mfma_f32_16x16x32_bf16 v[8:11], v[154:157], v[202:205], v[8:11]
	v_mfma_f32_16x16x32_bf16 v[60:63], v[150:153], v[182:185], v[60:63]
	v_mfma_f32_16x16x32_bf16 v[56:59], v[158:161], v[182:185], v[56:59]
	v_mfma_f32_16x16x32_bf16 v[48:51], v[150:153], v[190:193], v[48:51]
	v_mfma_f32_16x16x32_bf16 v[40:43], v[158:161], v[190:193], v[40:43]
	v_mfma_f32_16x16x32_bf16 v[32:35], v[150:153], v[198:201], v[32:35]
	v_mfma_f32_16x16x32_bf16 v[24:27], v[158:161], v[198:201], v[24:27]
	v_mfma_f32_16x16x32_bf16 v[16:19], v[150:153], v[206:209], v[16:19]
	v_mfma_f32_16x16x32_bf16 v[8:11], v[158:161], v[206:209], v[8:11]
	v_mfma_f32_16x16x32_bf16 v[52:55], v[162:165], v[178:181], v[52:55]
	v_mfma_f32_16x16x32_bf16 v[44:47], v[170:173], v[178:181], v[44:47]
	v_mfma_f32_16x16x32_bf16 v[36:39], v[162:165], v[186:189], v[36:39]
	v_mfma_f32_16x16x32_bf16 v[28:31], v[170:173], v[186:189], v[28:31]
	v_mfma_f32_16x16x32_bf16 v[20:23], v[162:165], v[194:197], v[20:23]
	v_mfma_f32_16x16x32_bf16 v[12:15], v[170:173], v[194:197], v[12:15]
	v_mfma_f32_16x16x32_bf16 v[4:7], v[162:165], v[202:205], v[4:7]
	v_mfma_f32_16x16x32_bf16 v[0:3], v[170:173], v[202:205], v[0:3]
	v_mfma_f32_16x16x32_bf16 v[52:55], v[166:169], v[182:185], v[52:55]
	v_mfma_f32_16x16x32_bf16 v[44:47], v[174:177], v[182:185], v[44:47]
	v_mfma_f32_16x16x32_bf16 v[36:39], v[166:169], v[190:193], v[36:39]
	v_mfma_f32_16x16x32_bf16 v[28:31], v[174:177], v[190:193], v[28:31]
	v_mfma_f32_16x16x32_bf16 v[20:23], v[166:169], v[198:201], v[20:23]
	v_mfma_f32_16x16x32_bf16 v[12:15], v[174:177], v[198:201], v[12:15]
	v_mfma_f32_16x16x32_bf16 v[4:7], v[166:169], v[206:209], v[4:7]
	v_mfma_f32_16x16x32_bf16 v[0:3], v[174:177], v[206:209], v[0:3]
	s_barrier
	s_movk_i32 s17, 0x100
	s_andn2_b64 vcc, exec, s[26:27]
	s_mov_b64 s[28:29], -1
	s_mov_b64 s[26:27], 0
	s_cbranch_vccz .LBB0_1429
	s_and_b64 vcc, exec, s[14:15]
	s_cbranch_vccz .LBB0_1432
	s_barrier

.LBB0_1605:
	s_mov_b64 s[4:5], -1
	s_and_b64 vcc, exec, s[2:3]
	s_cbranch_vccz .LBB0_1593
	s_mov_b32 s2, 24
	s_lshl_b32 s2, s2, 3
	s_add_i32 s2, s2, 0
	s_add_i32 s2, s2, 0x201c0
	v_mov_b32_e32 v0, s2
	s_waitcnt vmcnt(0)
	ds_read_b32 v1, v0
	s_ashr_i32 s45, s44, 31
	ds_read_b32 v0, v0 offset:4
	s_lshl_b64 s[2:3], s[44:45], 14
	s_lshl_b32 s63, s6, 8
	s_add_u32 s2, s2, s63
	s_addc_u32 s3, s3, 0
	s_mulk_i32 s3, 0xc0
	s_mul_hi_u32 s4, s2, 0xc0
	s_waitcnt lgkmcnt(1)
	v_readfirstlane_b32 s61, v1
	s_add_i32 s4, s4, s3
	s_mulk_i32 s2, 0xc0
	s_waitcnt lgkmcnt(0)
	v_readfirstlane_b32 s62, v0
	s_add_u32 s2, s61, s2
	s_addc_u32 s3, s62, s4
	s_add_u32 s2, s2, 0x3b000000
	s_addc_u32 s3, s3, 0
	s_mul_i32 s5, s44, 0x300000
	s_mul_hi_i32 s4, s44, 0x300000
	s_add_u32 s5, s61, s5
	s_addc_u32 s4, s62, s4
	s_add_u32 s28, s5, 0x41000000
	s_addc_u32 s13, s4, 0
	s_lshl_b64 s[4:5], s[44:45], 21
	s_add_u32 s4, s61, s4
	s_addc_u32 s5, s62, s5
	v_mbcnt_lo_u32_b32 v192, -1, 0
	v_mbcnt_hi_u32_b32 v192, -1, v192
	s_add_u32 s36, s4, 0x47000000
	v_add_u32_e32 v32, s49, v192
	s_addc_u32 s5, s5, 0
	v_readfirstlane_b32 s4, v32
	s_ashr_i32 s43, s4, 6
	s_cmp_lt_i32 s43, 4
	s_cselect_b64 s[6:7], -1, 0
	s_cmp_gt_i32 s43, 3
	v_lshlrev_b32_e32 v12, 3, v32
	v_mov_b32_e32 v64, 0x42700000
	s_cselect_b64 s[46:47], -1, 0
	v_add_u32_e32 v202, 0x2000, v12
	v_lshlrev_b32_e32 v203, 4, v32
	s_and_b32 s29, s13, 0xffff
	buffer_load_dwordx4 v[0:3], v203, s[28:31], 0 offen
	buffer_load_dwordx2 v[8:9], v202, s[28:31], 0 offen
	buffer_load_dwordx4 v[4:7], v203, s[28:31], s54 offen
	buffer_load_dwordx2 v[10:11], v202, s[28:31], s54 offen
	v_mul_hi_i32 v13, v32, s51
	v_lshrrev_b32_e32 v14, 31, v13
	v_lshrrev_b32_e32 v13, 1, v13
	v_add_u32_e32 v13, v13, v14
	v_mul_hi_i32 v14, v202, s51
	v_add_lshl_u32 v199, v13, v32, 4
	v_lshrrev_b32_e32 v13, 31, v14
	v_ashrrev_i32_e32 v14, 5, v14
	v_and_b32_e32 v194, 31, v192
	v_add_u32_e32 v13, v14, v13
	s_lshl_b32 s42, s43, 5
	v_lshl_add_u32 v200, v13, 4, v12
	v_mov_b64_e32 v[12:13], s[2:3]
	v_or_b32_e32 v14, s42, v194
	v_and_b32_e32 v184, 32, v192
	v_mad_i64_i32 v[12:13], s[2:3], v14, s50, v[12:13]
	s_mov_b32 s39, s31
	v_add_u32_e32 v50, 0, v199
	v_add_u32_e32 v51, 0, v200
	s_and_b32 s37, s5, 0xffff
	v_lshl_add_u64 v[12:13], v[12:13], 0, v[184:185]
	global_load_dwordx4 v[140:143], v[12:13], off offset:16
	global_load_dwordx4 v[136:139], v[12:13], off
	global_load_dwordx4 v[132:135], v[12:13], off offset:80
	global_load_dwordx4 v[128:131], v[12:13], off offset:64
	global_load_dwordx4 v[124:127], v[12:13], off offset:144
	global_load_dwordx4 v[120:123], v[12:13], off offset:128
	v_mad_u32_u24 v201, v194, s56, 0
	v_add_u32_e32 v204, v201, v184
	v_lshrrev_b32_e32 v32, 2, v32
	v_mul_lo_u32 v52, v32, s53
	v_and_b32_e32 v53, 48, v203
	v_mov_b32_e32 v65, v64
	v_mov_b32_e32 v66, v64
	v_mov_b32_e32 v67, v64
	v_mov_b32_e32 v68, v64
	v_mov_b32_e32 v69, v64
	v_mov_b32_e32 v70, v64
	v_mov_b32_e32 v71, v64
	v_mov_b32_e32 v72, v64
	v_mov_b32_e32 v73, v64
	v_mov_b32_e32 v74, v64
	v_mov_b32_e32 v75, v64
	v_mov_b32_e32 v76, v64
	v_mov_b32_e32 v77, v64
	v_mov_b32_e32 v78, v64
	v_mov_b32_e32 v79, v64
	s_waitcnt vmcnt(9)
	ds_write_b128 v50, v[0:3] offset:20480
	s_waitcnt vmcnt(8)
	ds_write_b64 v51, v[8:9] offset:28672
	s_waitcnt vmcnt(7)
	ds_write_b128 v50, v[4:7] offset:33792
	s_waitcnt vmcnt(6)
	ds_write_b64 v51, v[10:11] offset:41984
	s_waitcnt lgkmcnt(0)
	s_barrier
	buffer_load_dwordx4 v[40:43], v203, s[28:31], s55 offen
	buffer_load_dwordx2 v[48:49], v202, s[28:31], s55 offen
	buffer_load_dwordx4 v[44:47], v203, s[36:39], 0 offen
	ds_read_b128 v[0:3], v204 offset:20480
	ds_read_b128 v[4:7], v204 offset:20496
	ds_read_b128 v[8:11], v204 offset:27136
	ds_read_b128 v[12:15], v204 offset:27152
	ds_read_b128 v[16:19], v204 offset:20544
	ds_read_b128 v[20:23], v204 offset:20560
	ds_read_b128 v[24:27], v204 offset:27200
	ds_read_b128 v[28:31], v204 offset:27216
	v_mov_b64_e32 v[110:111], v[78:79]
	v_mov_b64_e32 v[108:109], v[76:77]
	v_mov_b64_e32 v[106:107], v[74:75]
	v_mov_b64_e32 v[104:105], v[72:73]
	v_mov_b64_e32 v[102:103], v[70:71]
	v_mov_b64_e32 v[100:101], v[68:69]
	v_mov_b64_e32 v[98:99], v[66:67]
	v_mov_b64_e32 v[96:97], v[64:65]
	v_add3_u32 v205, 0, v52, v53
	s_waitcnt vmcnt(7) lgkmcnt(6)
	v_mfma_scale_f32_32x32x64_f8f6f4 v[80:95], v[0:7], v[136:143], v[64:79], v191, v190 op_sel_hi:[0,0,0]
	ds_read_b128 v[0:3], v204 offset:20608
	ds_read_b128 v[4:7], v204 offset:20624
	ds_read_b128 v[32:35], v204 offset:27264
	ds_read_b128 v[36:39], v204 offset:27280
	s_waitcnt lgkmcnt(8)
	v_mfma_scale_f32_32x32x64_f8f6f4 v[96:111], v[8:15], v[136:143], v[96:111], v191, v190 op_sel_hi:[0,0,0]
	s_waitcnt vmcnt(2)
	ds_write_b128 v50, v[40:43] offset:47104
	s_waitcnt vmcnt(1)
	ds_write_b64 v51, v[48:49] offset:55296
	s_waitcnt vmcnt(0)
	ds_write_b128 v205, v[44:47]
	buffer_load_dwordx4 v[180:183], v203, s[28:31], s57 offen
	buffer_load_dwordx2 v[188:189], v202, s[28:31], s57 offen
	buffer_load_dwordx4 v[176:179], v203, s[36:39], s52 offen
	s_waitcnt lgkmcnt(9)
	v_mfma_scale_f32_32x32x64_f8f6f4 v[80:95], v[16:23], v[128:135], v[80:95], v191, v190 op_sel_hi:[0,0,0]
	s_waitcnt lgkmcnt(7)
	v_mfma_scale_f32_32x32x64_f8f6f4 v[96:111], v[24:31], v[128:135], v[96:111], v191, v190 op_sel_hi:[0,0,0]
	s_waitcnt lgkmcnt(5)
	v_mfma_scale_f32_32x32x64_f8f6f4 v[80:95], v[0:7], v[120:127], v[80:95], v191, v190 op_sel_hi:[0,0,0]
	s_waitcnt lgkmcnt(3)
	v_mfma_scale_f32_32x32x64_f8f6f4 v[96:111], v[32:39], v[120:127], v[96:111], v191, v190 op_sel_hi:[0,0,0]
	s_mov_b32 s13, s12
	s_mov_b32 s14, s12
	s_mov_b32 s15, s12
	s_mov_b32 s16, s12
	s_mov_b32 s17, s12
	s_mov_b32 s18, s12
	s_mov_b32 s19, s12
	s_mov_b32 s20, s12
	s_mov_b32 s21, s12
	s_mov_b32 s22, s12
	s_mov_b32 s23, s12
	s_mov_b32 s24, s12
	s_mov_b32 s25, s12
	s_mov_b32 s26, s12
	s_mov_b32 s27, s12
	v_mov_b64_e32 v[0:1], s[12:13]
	v_mov_b64_e32 v[14:15], s[26:27]
	v_mov_b64_e32 v[2:3], s[14:15]
	v_mov_b64_e32 v[4:5], s[16:17]
	v_mov_b64_e32 v[6:7], s[18:19]
	v_mov_b64_e32 v[8:9], s[20:21]
	v_mov_b64_e32 v[10:11], s[22:23]
	v_mov_b64_e32 v[12:13], s[24:25]
	v_mov_b64_e32 v[30:31], v[14:15]
	v_mov_b64_e32 v[46:47], v[14:15]
	v_mov_b64_e32 v[62:63], v[14:15]
	v_mov_b64_e32 v[28:29], v[12:13]
	v_mov_b64_e32 v[26:27], v[10:11]
	v_mov_b64_e32 v[24:25], v[8:9]
	v_mov_b64_e32 v[22:23], v[6:7]
	v_mov_b64_e32 v[20:21], v[4:5]
	v_mov_b64_e32 v[18:19], v[2:3]
	v_mov_b64_e32 v[16:17], v[0:1]
	v_mov_b64_e32 v[44:45], v[12:13]
	v_mov_b64_e32 v[42:43], v[10:11]
	v_mov_b64_e32 v[40:41], v[8:9]
	v_mov_b64_e32 v[38:39], v[6:7]
	v_mov_b64_e32 v[36:37], v[4:5]
	v_mov_b64_e32 v[34:35], v[2:3]
	v_mov_b64_e32 v[32:33], v[0:1]
	v_mov_b64_e32 v[60:61], v[12:13]
	v_mov_b64_e32 v[58:59], v[10:11]
	v_mov_b64_e32 v[56:57], v[8:9]
	v_mov_b64_e32 v[54:55], v[6:7]
	v_mov_b64_e32 v[52:53], v[4:5]
	v_mov_b64_e32 v[50:51], v[2:3]
	v_mov_b64_e32 v[48:49], v[0:1]
	v_mov_b32_e32 v112, v185
	v_mov_b32_e32 v113, v185
	v_mov_b32_e32 v114, v185
	v_mov_b32_e32 v115, v185
	v_mov_b32_e32 v116, v185
	v_mov_b32_e32 v117, v185
	v_mov_b32_e32 v118, v185
	v_mov_b32_e32 v119, v185
	s_and_b64 vcc, exec, s[6:7]
	s_cbranch_vccnz .LBB0_1608
	s_waitcnt lgkmcnt(0)
	s_barrier

.LBB0_1614:
	s_mul_i32 s14, s13, 0x3400
	s_and_b32 s7, 1, s18
	s_add_i32 s14, s14, 0
	s_andn2_b32 s15, 1, s18
	s_mul_i32 s6, s17, 0x3400
	s_cmpk_lt_u32 s18, 0xfc
	s_cselect_b32 s21, s20, 0x2fd000
	s_cmp_eq_u32 s7, 1
	v_add_u32_e32 v96, s14, v199
	s_waitcnt lgkmcnt(6)
	v_mfma_scale_f32_32x32x64_f8f6f4 v[80:95], v[168:175], v[136:143], v[64:79], v191, v190 op_sel_hi:[0,0,0]
	s_waitcnt vmcnt(2)
	ds_write_b128 v96, v[180:183] offset:20480
	v_add_u32_e32 v96, s14, v200
	s_mulk_i32 s15, 0x2800
	s_waitcnt vmcnt(1)
	ds_write_b64 v96, v[188:189] offset:28672
	v_add_u32_e32 v96, s15, v205
	s_mov_b32 s39, s31
	s_waitcnt vmcnt(0)
	ds_write_b128 v96, v[176:179]
	buffer_load_dwordx4 v[180:183], v203, s[28:31], s21 offen
	buffer_load_dwordx2 v[188:189], v202, s[28:31], s21 offen
	buffer_load_dwordx4 v[176:179], v203, s[36:39], s19 offen
	v_add_u32_e32 v172, s6, v204
	s_cselect_b32 s6, 0x2800, 0
	v_add_u32_e32 v186, s6, v198
	s_waitcnt lgkmcnt(7)
	v_mfma_scale_f32_32x32x64_f8f6f4 v[96:111], v[160:167], v[136:143], v[64:79], v191, v190 op_sel_hi:[0,0,0]
	ds_read_b128 v[160:163], v172 offset:20608
	ds_read_b128 v[164:167], v172 offset:20624
	ds_read_b128 v[168:171], v172 offset:27264
	ds_read_b128 v[172:175], v172 offset:27280
	s_waitcnt lgkmcnt(9)
	v_mfma_scale_f32_32x32x64_f8f6f4 v[80:95], v[152:159], v[128:135], v[80:95], v191, v190 op_sel_hi:[0,0,0]
	ds_read_b128 v[152:155], v186
	ds_read_b128 v[156:159], v186 offset:16
	ds_read_b128 v[206:209], v186 offset:2560
	ds_read_b128 v[210:213], v186 offset:2576
	s_waitcnt lgkmcnt(11)
	v_mfma_scale_f32_32x32x64_f8f6f4 v[96:111], v[144:151], v[128:135], v[96:111], v191, v190 op_sel_hi:[0,0,0]
	ds_read_b128 v[144:147], v186 offset:5120
	ds_read_b128 v[148:151], v186 offset:5136
	ds_read_b128 v[214:217], v186 offset:7680
	ds_read_b128 v[218:221], v186 offset:7696
	s_waitcnt lgkmcnt(10)
	v_mfma_scale_f32_32x32x64_f8f6f4 v[80:95], v[160:167], v[120:127], v[80:95], v191, v190 op_sel_hi:[0,0,0]
	s_waitcnt lgkmcnt(8)
	v_mfma_scale_f32_32x32x64_f8f6f4 v[96:111], v[168:175], v[120:127], v[96:111], v191, v190 op_sel_hi:[0,0,0]
	s_waitcnt lgkmcnt(6)
	v_mfma_f32_32x32x64_f8f6f4 v[0:15], v[112:119], v[152:159], v[0:15]
	s_waitcnt lgkmcnt(4)
	v_mfma_f32_32x32x64_f8f6f4 v[16:31], v[112:119], v[206:213], v[16:31]
	s_waitcnt lgkmcnt(2)
	v_mfma_f32_32x32x64_f8f6f4 v[32:47], v[112:119], v[144:151], v[32:47]
	s_waitcnt lgkmcnt(0)
	v_mfma_f32_32x32x64_f8f6f4 v[48:63], v[112:119], v[214:221], v[48:63]
	v_cndmask_b32_e64 v144, 0, 1, s[46:47]
	v_cmp_ne_u32_e64 s[6:7], 1, v144
	s_andn2_b64 vcc, exec, s[46:47]
	s_cbranch_vccnz .LBB0_1616
	s_barrier

.LBB0_1622:
	s_mul_i32 s14, s17, 0x3400
	s_mulk_i32 s13, 0x3400
	s_add_i32 s13, s13, 0
	v_add_u32_e32 v96, s13, v199
	s_waitcnt lgkmcnt(6)
	v_mfma_scale_f32_32x32x64_f8f6f4 v[80:95], v[168:175], v[136:143], v[64:79], v191, v190 op_sel_hi:[0,0,0]
	s_waitcnt vmcnt(2)
	ds_write_b128 v96, v[180:183] offset:20480
	v_add_u32_e32 v96, s13, v200
	s_waitcnt vmcnt(1)
	ds_write_b64 v96, v[188:189] offset:28672
	s_waitcnt vmcnt(0)
	ds_write_b128 v205, v[176:179] offset:10240
	v_add3_u32 v108, v201, s14, v184
	s_waitcnt lgkmcnt(7)
	v_mfma_scale_f32_32x32x64_f8f6f4 v[64:79], v[160:167], v[136:143], v[64:79], v191, v190 op_sel_hi:[0,0,0]
	ds_read_b128 v[96:99], v108 offset:20608
	ds_read_b128 v[100:103], v108 offset:20624
	ds_read_b128 v[104:107], v108 offset:27264
	ds_read_b128 v[108:111], v108 offset:27280
	s_waitcnt lgkmcnt(9)
	v_mfma_scale_f32_32x32x64_f8f6f4 v[80:95], v[152:159], v[128:135], v[80:95], v191, v190 op_sel_hi:[0,0,0]
	ds_read_b128 v[136:139], v198
	ds_read_b128 v[140:143], v198 offset:16
	ds_read_b128 v[152:155], v198 offset:2560
	ds_read_b128 v[156:159], v198 offset:2576
	s_waitcnt lgkmcnt(11)
	v_mfma_scale_f32_32x32x64_f8f6f4 v[64:79], v[144:151], v[128:135], v[64:79], v191, v190 op_sel_hi:[0,0,0]
	ds_read_b128 v[128:131], v198 offset:5120
	ds_read_b128 v[132:135], v198 offset:5136
	ds_read_b128 v[144:147], v198 offset:7680
	ds_read_b128 v[148:151], v198 offset:7696
	s_waitcnt lgkmcnt(10)
	v_mfma_scale_f32_32x32x64_f8f6f4 v[80:95], v[96:103], v[120:127], v[80:95], v191, v190 op_sel_hi:[0,0,0]
	s_waitcnt lgkmcnt(8)
	v_mfma_scale_f32_32x32x64_f8f6f4 v[64:79], v[104:111], v[120:127], v[64:79], v191, v190 op_sel_hi:[0,0,0]
	s_waitcnt lgkmcnt(6)
	v_mfma_f32_32x32x64_f8f6f4 v[0:15], v[112:119], v[136:143], v[0:15]
	s_waitcnt lgkmcnt(4)
	v_mfma_f32_32x32x64_f8f6f4 v[16:31], v[112:119], v[152:159], v[16:31]
	s_waitcnt lgkmcnt(2)
	v_mfma_f32_32x32x64_f8f6f4 v[32:47], v[112:119], v[128:135], v[32:47]
	s_waitcnt lgkmcnt(0)
	v_mfma_f32_32x32x64_f8f6f4 v[48:63], v[112:119], v[144:151], v[48:63]
	s_and_b64 vcc, exec, s[6:7]
	s_cbranch_vccnz .LBB0_1624
	s_barrier

.LBB0_1627:
	ds_read_b128 v[88:91], v198 offset:10240
	ds_read_b128 v[92:95], v198 offset:10256
	ds_read_b128 v[80:83], v198 offset:12800
	ds_read_b128 v[84:87], v198 offset:12816
	ds_read_b128 v[72:75], v198 offset:15360
	ds_read_b128 v[76:79], v198 offset:15376
	ds_read_b128 v[64:67], v198 offset:17920
	ds_read_b128 v[68:71], v198 offset:17936
	v_mov_b32_e32 v96, v187
	s_nop 1
	v_permlane32_swap_b32_e32 v187, v96
	s_and_saveexec_b64 s[4:5], s[2:3]
	s_cbranch_execz .LBB0_1592
	v_add_f32_e32 v96, v187, v96
	ds_write_b32 v196, v96 offset:60416
	s_branch .LBB0_1592

.LBB0_4355:
	ds_read_b128 v[160:163], v152
	ds_read_b128 v[164:167], v152 offset:1024
	ds_read_b128 v[168:171], v152 offset:2048
	ds_read_b128 v[172:175], v152 offset:3072
	ds_read_b128 v[176:179], v153
	ds_read_b128 v[180:183], v153 offset:1024
	ds_read_b128 v[184:187], v153 offset:2048
	ds_read_b128 v[188:191], v153 offset:3072
	s_add_u32 s38, s30, s36
	s_addc_u32 s39, s31, s37
	s_add_u32 s40, s38, 0x100
	s_addc_u32 s41, s39, 0
	s_add_u32 s67, s23, s36
	s_addc_u32 s68, s65, s37
	s_cmpk_eq_i32 s36, 0x700
	s_cselect_b64 vcc, -1, 0
	s_and_b64 s[38:39], vcc, exec
	v_cndmask_b32_e32 v132, v138, v157, vcc
	s_cselect_b32 s41, s27, s41
	s_cselect_b32 s40, s26, s40
	v_cndmask_b32_e32 v224, v136, v156, vcc
	v_cndmask_b32_e32 v135, v134, v155, vcc
	v_cndmask_b32_e32 v141, v140, v158, vcc
	s_cselect_b32 s39, s25, s68
	s_cselect_b32 s38, s24, s67
	s_mov_b32 m0, s59
	v_lshl_add_u64 v[226:227], v[144:145], 0, s[36:37]
	ds_read_b128 v[192:195], v154
	ds_read_b128 v[196:199], v154 offset:1024
	ds_read_b128 v[200:203], v154 offset:2048
	ds_read_b128 v[204:207], v154 offset:3072
	ds_read_b128 v[208:211], v154 offset:4096
	ds_read_b128 v[212:215], v154 offset:5120
	ds_read_b128 v[216:219], v154 offset:6144
	ds_read_b128 v[220:223], v154 offset:7168
	global_load_lds_dwordx4 v[226:227], off
	v_lshl_add_u64 v[226:227], v[142:143], 0, s[36:37]
	s_add_i32 m0, s49, 0xe000
	s_nop 0
	global_load_lds_dwordx4 v[226:227], off
	s_waitcnt vmcnt(8)
	s_waitcnt lgkmcnt(0)
	s_barrier
	s_waitcnt lgkmcnt(0)
	v_mfma_f32_16x16x32_bf16 v[116:119], v[160:163], v[192:195], v[116:119]
	v_mfma_f32_16x16x32_bf16 v[112:115], v[168:171], v[192:195], v[112:115]
	v_mfma_f32_16x16x32_bf16 v[108:111], v[160:163], v[200:203], v[108:111]
	v_mfma_f32_16x16x32_bf16 v[104:107], v[168:171], v[200:203], v[104:107]
	v_mfma_f32_16x16x32_bf16 v[92:95], v[160:163], v[208:211], v[92:95]
	v_mfma_f32_16x16x32_bf16 v[88:91], v[168:171], v[208:211], v[88:91]
	v_mfma_f32_16x16x32_bf16 v[76:79], v[160:163], v[216:219], v[76:79]
	v_mfma_f32_16x16x32_bf16 v[72:75], v[168:171], v[216:219], v[72:75]
	v_mfma_f32_16x16x32_bf16 v[116:119], v[164:167], v[196:199], v[116:119]
	v_mfma_f32_16x16x32_bf16 v[112:115], v[172:175], v[196:199], v[112:115]
	v_mfma_f32_16x16x32_bf16 v[108:111], v[164:167], v[204:207], v[108:111]
	v_mfma_f32_16x16x32_bf16 v[104:107], v[172:175], v[204:207], v[104:107]
	v_mfma_f32_16x16x32_bf16 v[92:95], v[164:167], v[212:215], v[92:95]
	v_mfma_f32_16x16x32_bf16 v[88:91], v[172:175], v[212:215], v[88:91]
	v_mfma_f32_16x16x32_bf16 v[76:79], v[164:167], v[220:223], v[76:79]
	v_mfma_f32_16x16x32_bf16 v[72:75], v[172:175], v[220:223], v[72:75]
	v_mfma_f32_16x16x32_bf16 v[124:127], v[176:179], v[192:195], v[124:127]
	v_mfma_f32_16x16x32_bf16 v[120:123], v[184:187], v[192:195], v[120:123]
	v_mfma_f32_16x16x32_bf16 v[100:103], v[176:179], v[200:203], v[100:103]
	v_mfma_f32_16x16x32_bf16 v[96:99], v[184:187], v[200:203], v[96:99]
	v_mfma_f32_16x16x32_bf16 v[84:87], v[176:179], v[208:211], v[84:87]
	v_mfma_f32_16x16x32_bf16 v[80:83], v[184:187], v[208:211], v[80:83]
	v_mfma_f32_16x16x32_bf16 v[68:71], v[176:179], v[216:219], v[68:71]
	v_mfma_f32_16x16x32_bf16 v[64:67], v[184:187], v[216:219], v[64:67]
	v_mfma_f32_16x16x32_bf16 v[124:127], v[180:183], v[196:199], v[124:127]
	v_mfma_f32_16x16x32_bf16 v[120:123], v[188:191], v[196:199], v[120:123]
	v_mfma_f32_16x16x32_bf16 v[100:103], v[180:183], v[204:207], v[100:103]
	v_mfma_f32_16x16x32_bf16 v[96:99], v[188:191], v[204:207], v[96:99]
	v_mfma_f32_16x16x32_bf16 v[84:87], v[180:183], v[212:215], v[84:87]
	v_mfma_f32_16x16x32_bf16 v[80:83], v[188:191], v[212:215], v[80:83]
	v_mfma_f32_16x16x32_bf16 v[68:71], v[180:183], v[220:223], v[68:71]
	v_mfma_f32_16x16x32_bf16 v[64:67], v[188:191], v[220:223], v[64:67]
	s_barrier
	s_add_i32 s67, s56, s29
	v_lshl_add_u64 v[226:227], s[38:39], 0, v[128:129]
	s_mov_b32 m0, s67
	ds_read_b128 v[192:195], v154 offset:16384
	ds_read_b128 v[196:199], v154 offset:17408
	ds_read_b128 v[200:203], v154 offset:18432
	ds_read_b128 v[204:207], v154 offset:19456
	ds_read_b128 v[208:211], v154 offset:20480
	ds_read_b128 v[212:215], v154 offset:21504
	ds_read_b128 v[216:219], v154 offset:22528
	ds_read_b128 v[220:223], v154 offset:23552
	global_load_lds_dwordx4 v[226:227], off
	s_add_i32 m0, s67, 0x2000
	s_add_u32 s68, s38, 0x40000
	v_lshl_add_u64 v[228:229], s[38:39], 0, v[130:131]
	s_addc_u32 s69, s39, 0
	s_add_i32 s67, s57, s29
	global_load_lds_dwordx4 v[228:229], off
	v_lshl_add_u64 v[230:231], s[68:69], 0, v[128:129]
	s_mov_b32 m0, s67
	v_mov_b32_e32 v225, v133
	global_load_lds_dwordx4 v[230:231], off
	v_lshl_add_u64 v[230:231], s[68:69], 0, v[130:131]
	s_add_i32 m0, s67, 0x2000
	s_nop 0
	global_load_lds_dwordx4 v[230:231], off
	s_mov_b32 m0, s49
	v_lshl_add_u64 v[230:231], s[40:41], 0, v[132:133]
	global_load_lds_dwordx4 v132, s[40:41]
	s_mov_b32 m0, s50
	s_nop 0
	global_load_lds_dwordx4 v224, s[40:41]
	s_waitcnt vmcnt(8)
	s_waitcnt lgkmcnt(0)
	v_lshl_add_u64 v[224:225], s[40:41], 0, v[224:225]
	s_barrier
	s_waitcnt lgkmcnt(0)
	v_mfma_f32_16x16x32_bf16 v[60:63], v[160:163], v[192:195], v[60:63]
	v_mfma_f32_16x16x32_bf16 v[56:59], v[168:171], v[192:195], v[56:59]
	v_mfma_f32_16x16x32_bf16 v[44:47], v[160:163], v[200:203], v[44:47]
	v_mfma_f32_16x16x32_bf16 v[40:43], v[168:171], v[200:203], v[40:43]
	v_mfma_f32_16x16x32_bf16 v[28:31], v[160:163], v[208:211], v[28:31]
	v_mfma_f32_16x16x32_bf16 v[24:27], v[168:171], v[208:211], v[24:27]
	v_mfma_f32_16x16x32_bf16 v[12:15], v[160:163], v[216:219], v[12:15]
	v_mfma_f32_16x16x32_bf16 v[8:11], v[168:171], v[216:219], v[8:11]
	v_mfma_f32_16x16x32_bf16 v[60:63], v[164:167], v[196:199], v[60:63]
	v_mfma_f32_16x16x32_bf16 v[56:59], v[172:175], v[196:199], v[56:59]
	v_mfma_f32_16x16x32_bf16 v[44:47], v[164:167], v[204:207], v[44:47]
	v_mfma_f32_16x16x32_bf16 v[40:43], v[172:175], v[204:207], v[40:43]
	v_mfma_f32_16x16x32_bf16 v[28:31], v[164:167], v[212:215], v[28:31]
	v_mfma_f32_16x16x32_bf16 v[24:27], v[172:175], v[212:215], v[24:27]
	v_mfma_f32_16x16x32_bf16 v[12:15], v[164:167], v[220:223], v[12:15]
	v_mfma_f32_16x16x32_bf16 v[8:11], v[172:175], v[220:223], v[8:11]
	v_mfma_f32_16x16x32_bf16 v[52:55], v[176:179], v[192:195], v[52:55]
	v_mfma_f32_16x16x32_bf16 v[48:51], v[184:187], v[192:195], v[48:51]
	v_mfma_f32_16x16x32_bf16 v[36:39], v[176:179], v[200:203], v[36:39]
	v_mfma_f32_16x16x32_bf16 v[32:35], v[184:187], v[200:203], v[32:35]
	v_mfma_f32_16x16x32_bf16 v[20:23], v[176:179], v[208:211], v[20:23]
	v_mfma_f32_16x16x32_bf16 v[16:19], v[184:187], v[208:211], v[16:19]
	v_mfma_f32_16x16x32_bf16 v[4:7], v[176:179], v[216:219], v[4:7]
	v_mfma_f32_16x16x32_bf16 v[0:3], v[184:187], v[216:219], v[0:3]
	v_mfma_f32_16x16x32_bf16 v[52:55], v[180:183], v[196:199], v[52:55]
	v_mfma_f32_16x16x32_bf16 v[48:51], v[188:191], v[196:199], v[48:51]
	v_mfma_f32_16x16x32_bf16 v[36:39], v[180:183], v[204:207], v[36:39]
	v_mfma_f32_16x16x32_bf16 v[32:35], v[188:191], v[204:207], v[32:35]
	v_mfma_f32_16x16x32_bf16 v[20:23], v[180:183], v[212:215], v[20:23]
	v_mfma_f32_16x16x32_bf16 v[16:19], v[188:191], v[212:215], v[16:19]
	v_mfma_f32_16x16x32_bf16 v[4:7], v[180:183], v[220:223], v[4:7]
	v_mfma_f32_16x16x32_bf16 v[0:3], v[188:191], v[220:223], v[0:3]
	s_barrier
	s_add_i32 s67, 0, 0x18000
	v_add_u32_e32 v132, s67, v139
	s_add_i32 s68, 0, 0x1c000
	ds_read_b128 v[160:163], v132
	ds_read_b128 v[164:167], v132 offset:1024
	ds_read_b128 v[168:171], v132 offset:2048
	ds_read_b128 v[172:175], v132 offset:3072
	v_add_u32_e32 v132, s68, v139
	ds_read_b128 v[176:179], v132
	ds_read_b128 v[180:183], v132 offset:1024
	ds_read_b128 v[184:187], v132 offset:2048
	ds_read_b128 v[188:191], v132 offset:3072
	s_mov_b32 m0, s51
	ds_read_b128 v[192:195], v154 offset:32768
	ds_read_b128 v[196:199], v154 offset:33792
	ds_read_b128 v[200:203], v154 offset:34816
	ds_read_b128 v[204:207], v154 offset:35840
	ds_read_b128 v[208:211], v154 offset:36864
	ds_read_b128 v[212:215], v154 offset:37888
	ds_read_b128 v[216:219], v154 offset:38912
	ds_read_b128 v[220:223], v154 offset:39936
	global_load_lds_dwordx4 v135, s[40:41]
	s_mov_b32 m0, s52
	s_nop 0
	global_load_lds_dwordx4 v141, s[40:41]
	s_waitcnt vmcnt(8)
	s_waitcnt lgkmcnt(0)
	s_barrier
	s_waitcnt lgkmcnt(0)
	v_mfma_f32_16x16x32_bf16 v[116:119], v[160:163], v[192:195], v[116:119]
	v_mfma_f32_16x16x32_bf16 v[112:115], v[168:171], v[192:195], v[112:115]
	v_mfma_f32_16x16x32_bf16 v[108:111], v[160:163], v[200:203], v[108:111]
	v_mfma_f32_16x16x32_bf16 v[104:107], v[168:171], v[200:203], v[104:107]
	v_mfma_f32_16x16x32_bf16 v[92:95], v[160:163], v[208:211], v[92:95]
	v_mfma_f32_16x16x32_bf16 v[88:91], v[168:171], v[208:211], v[88:91]
	v_mfma_f32_16x16x32_bf16 v[76:79], v[160:163], v[216:219], v[76:79]
	v_mfma_f32_16x16x32_bf16 v[72:75], v[168:171], v[216:219], v[72:75]
	v_mfma_f32_16x16x32_bf16 v[116:119], v[164:167], v[196:199], v[116:119]
	v_mfma_f32_16x16x32_bf16 v[112:115], v[172:175], v[196:199], v[112:115]
	v_mfma_f32_16x16x32_bf16 v[108:111], v[164:167], v[204:207], v[108:111]
	v_mfma_f32_16x16x32_bf16 v[104:107], v[172:175], v[204:207], v[104:107]
	v_mfma_f32_16x16x32_bf16 v[92:95], v[164:167], v[212:215], v[92:95]
	v_mfma_f32_16x16x32_bf16 v[88:91], v[172:175], v[212:215], v[88:91]
	v_mfma_f32_16x16x32_bf16 v[76:79], v[164:167], v[220:223], v[76:79]
	v_mfma_f32_16x16x32_bf16 v[72:75], v[172:175], v[220:223], v[72:75]
	v_mfma_f32_16x16x32_bf16 v[124:127], v[176:179], v[192:195], v[124:127]
	v_mfma_f32_16x16x32_bf16 v[120:123], v[184:187], v[192:195], v[120:123]
	v_mfma_f32_16x16x32_bf16 v[100:103], v[176:179], v[200:203], v[100:103]
	v_mfma_f32_16x16x32_bf16 v[96:99], v[184:187], v[200:203], v[96:99]
	v_mfma_f32_16x16x32_bf16 v[84:87], v[176:179], v[208:211], v[84:87]
	v_mfma_f32_16x16x32_bf16 v[80:83], v[184:187], v[208:211], v[80:83]
	v_mfma_f32_16x16x32_bf16 v[68:71], v[176:179], v[216:219], v[68:71]
	v_mfma_f32_16x16x32_bf16 v[64:67], v[184:187], v[216:219], v[64:67]
	v_mfma_f32_16x16x32_bf16 v[124:127], v[180:183], v[196:199], v[124:127]
	v_mfma_f32_16x16x32_bf16 v[120:123], v[188:191], v[196:199], v[120:123]
	v_mfma_f32_16x16x32_bf16 v[100:103], v[180:183], v[204:207], v[100:103]
	v_mfma_f32_16x16x32_bf16 v[96:99], v[188:191], v[204:207], v[96:99]
	v_mfma_f32_16x16x32_bf16 v[84:87], v[180:183], v[212:215], v[84:87]
	v_mfma_f32_16x16x32_bf16 v[80:83], v[188:191], v[212:215], v[80:83]
	v_mfma_f32_16x16x32_bf16 v[68:71], v[180:183], v[220:223], v[68:71]
	v_mfma_f32_16x16x32_bf16 v[64:67], v[188:191], v[220:223], v[64:67]
	s_barrier
	s_add_i32 s40, s67, s29
	v_lshl_add_u64 v[226:227], v[226:227], 0, s[18:19]
	s_mov_b32 m0, s40
	ds_read_b128 v[192:195], v154 offset:49152
	ds_read_b128 v[196:199], v154 offset:50176
	ds_read_b128 v[200:203], v154 offset:51200
	ds_read_b128 v[204:207], v154 offset:52224
	ds_read_b128 v[208:211], v154 offset:53248
	ds_read_b128 v[212:215], v154 offset:54272
	ds_read_b128 v[216:219], v154 offset:55296
	ds_read_b128 v[220:223], v154 offset:56320
	global_load_lds_dwordx4 v[226:227], off
	s_add_i32 m0, s40, 0x2000
	s_add_u32 s38, s38, 0x40080
	v_lshl_add_u64 v[226:227], v[228:229], 0, s[18:19]
	s_addc_u32 s39, s39, 0
	s_add_i32 s40, s68, s29
	global_load_lds_dwordx4 v[226:227], off
	v_lshl_add_u64 v[226:227], s[38:39], 0, v[128:129]
	s_mov_b32 m0, s40
	v_lshl_add_u64 v[224:225], v[224:225], 0, s[18:19]
	global_load_lds_dwordx4 v[226:227], off
	v_lshl_add_u64 v[226:227], s[38:39], 0, v[130:131]
	s_add_i32 m0, s40, 0x2000
	s_nop 0
	global_load_lds_dwordx4 v[226:227], off
	v_lshl_add_u64 v[226:227], v[230:231], 0, s[18:19]
	s_mov_b32 m0, s54
	s_nop 0
	global_load_lds_dwordx4 v[226:227], off
	s_mov_b32 m0, s55
	s_nop 0
	global_load_lds_dwordx4 v[224:225], off
	s_waitcnt vmcnt(8)
	s_waitcnt lgkmcnt(0)
	s_barrier
	s_waitcnt lgkmcnt(0)
	v_mfma_f32_16x16x32_bf16 v[60:63], v[160:163], v[192:195], v[60:63]
	v_mfma_f32_16x16x32_bf16 v[56:59], v[168:171], v[192:195], v[56:59]
	v_mfma_f32_16x16x32_bf16 v[44:47], v[160:163], v[200:203], v[44:47]
	v_mfma_f32_16x16x32_bf16 v[40:43], v[168:171], v[200:203], v[40:43]
	v_mfma_f32_16x16x32_bf16 v[28:31], v[160:163], v[208:211], v[28:31]
	v_mfma_f32_16x16x32_bf16 v[24:27], v[168:171], v[208:211], v[24:27]
	v_mfma_f32_16x16x32_bf16 v[12:15], v[160:163], v[216:219], v[12:15]
	v_mfma_f32_16x16x32_bf16 v[8:11], v[168:171], v[216:219], v[8:11]
	v_mfma_f32_16x16x32_bf16 v[60:63], v[164:167], v[196:199], v[60:63]
	v_mfma_f32_16x16x32_bf16 v[56:59], v[172:175], v[196:199], v[56:59]
	v_mfma_f32_16x16x32_bf16 v[44:47], v[164:167], v[204:207], v[44:47]
	v_mfma_f32_16x16x32_bf16 v[40:43], v[172:175], v[204:207], v[40:43]
	v_mfma_f32_16x16x32_bf16 v[28:31], v[164:167], v[212:215], v[28:31]
	v_mfma_f32_16x16x32_bf16 v[24:27], v[172:175], v[212:215], v[24:27]
	v_mfma_f32_16x16x32_bf16 v[12:15], v[164:167], v[220:223], v[12:15]
	v_mfma_f32_16x16x32_bf16 v[8:11], v[172:175], v[220:223], v[8:11]
	v_mfma_f32_16x16x32_bf16 v[52:55], v[176:179], v[192:195], v[52:55]
	v_mfma_f32_16x16x32_bf16 v[48:51], v[184:187], v[192:195], v[48:51]
	v_mfma_f32_16x16x32_bf16 v[36:39], v[176:179], v[200:203], v[36:39]
	v_mfma_f32_16x16x32_bf16 v[32:35], v[184:187], v[200:203], v[32:35]
	v_mfma_f32_16x16x32_bf16 v[20:23], v[176:179], v[208:211], v[20:23]
	v_mfma_f32_16x16x32_bf16 v[16:19], v[184:187], v[208:211], v[16:19]
	v_mfma_f32_16x16x32_bf16 v[4:7], v[176:179], v[216:219], v[4:7]
	v_mfma_f32_16x16x32_bf16 v[0:3], v[184:187], v[216:219], v[0:3]
	v_mfma_f32_16x16x32_bf16 v[52:55], v[180:183], v[196:199], v[52:55]
	v_mfma_f32_16x16x32_bf16 v[48:51], v[188:191], v[196:199], v[48:51]
	v_mfma_f32_16x16x32_bf16 v[36:39], v[180:183], v[204:207], v[36:39]
	v_mfma_f32_16x16x32_bf16 v[32:35], v[188:191], v[204:207], v[32:35]
	v_mfma_f32_16x16x32_bf16 v[20:23], v[180:183], v[212:215], v[20:23]
	v_mfma_f32_16x16x32_bf16 v[16:19], v[188:191], v[212:215], v[16:19]
	v_mfma_f32_16x16x32_bf16 v[4:7], v[180:183], v[220:223], v[4:7]
	v_mfma_f32_16x16x32_bf16 v[0:3], v[188:191], v[220:223], v[0:3]
	s_barrier
	s_add_i32 s66, s66, 2
	s_add_u32 s36, s36, 0x100
	s_addc_u32 s37, s37, 0
	s_cmp_gt_u32 s66, 13
	s_cbranch_scc0 .LBB0_4355
	s_and_b64 vcc, exec, s[20:21]
	s_cbranch_vccz .LBB0_4358
	s_barrier

.LBB0_4459:
	ds_read_b128 v[8:11], v149
	ds_read_b128 v[12:15], v149 offset:1024
	ds_read_b128 v[16:19], v149 offset:2048
	ds_read_b128 v[20:23], v149 offset:3072
	ds_read_b128 v[24:27], v150
	ds_read_b128 v[28:31], v150 offset:1024
	ds_read_b128 v[32:35], v150 offset:2048
	ds_read_b128 v[36:39], v150 offset:3072
	s_add_u32 s68, s36, 0x18080
	s_addc_u32 s69, s37, 0
	s_mov_b32 m0, s61
	v_lshl_add_u64 v[64:65], s[68:69], 0, v[128:129]
	ds_read_b128 v[0:3], v140
	ds_read_b128 v[4:7], v140 offset:1024
	ds_read_b128 v[40:43], v140 offset:2048
	ds_read_b128 v[44:47], v140 offset:3072
	ds_read_b128 v[48:51], v140 offset:4096
	ds_read_b128 v[52:55], v140 offset:5120
	ds_read_b128 v[56:59], v140 offset:6144
	ds_read_b128 v[60:63], v140 offset:7168
	global_load_lds_dwordx4 v[64:65], off
	v_lshl_add_u64 v[64:65], s[68:69], 0, v[132:133]
	s_mov_b32 m0, s62
	s_nop 0
	global_load_lds_dwordx4 v[64:65], off
	s_waitcnt vmcnt(8)
	s_waitcnt lgkmcnt(0)
	s_barrier
	s_waitcnt lgkmcnt(0)
	v_mfma_f32_16x16x32_bf16 v[64:67], v[8:11], v[0:3], 0
	v_mfma_f32_16x16x32_bf16 v[68:71], v[16:19], v[0:3], 0
	v_mfma_f32_16x16x32_bf16 v[72:75], v[8:11], v[40:43], 0
	v_mfma_f32_16x16x32_bf16 v[76:79], v[16:19], v[40:43], 0
	v_mfma_f32_16x16x32_bf16 v[80:83], v[8:11], v[48:51], 0
	v_mfma_f32_16x16x32_bf16 v[84:87], v[16:19], v[48:51], 0
	v_mfma_f32_16x16x32_bf16 v[88:91], v[8:11], v[56:59], 0
	v_mfma_f32_16x16x32_bf16 v[92:95], v[16:19], v[56:59], 0
	v_mfma_f32_16x16x32_bf16 v[64:67], v[12:15], v[4:7], v[64:67]
	v_mfma_f32_16x16x32_bf16 v[68:71], v[20:23], v[4:7], v[68:71]
	v_mfma_f32_16x16x32_bf16 v[72:75], v[12:15], v[44:47], v[72:75]
	v_mfma_f32_16x16x32_bf16 v[76:79], v[20:23], v[44:47], v[76:79]
	v_mfma_f32_16x16x32_bf16 v[80:83], v[12:15], v[52:55], v[80:83]
	v_mfma_f32_16x16x32_bf16 v[84:87], v[20:23], v[52:55], v[84:87]
	v_mfma_f32_16x16x32_bf16 v[88:91], v[12:15], v[60:63], v[88:91]
	v_mfma_f32_16x16x32_bf16 v[92:95], v[20:23], v[60:63], v[92:95]
	v_mfma_f32_16x16x32_bf16 v[96:99], v[24:27], v[0:3], 0
	v_mfma_f32_16x16x32_bf16 v[0:3], v[32:35], v[0:3], 0
	v_mfma_f32_16x16x32_bf16 v[100:103], v[36:39], v[4:7], v[0:3]
	v_mfma_f32_16x16x32_bf16 v[0:3], v[24:27], v[40:43], 0
	v_mfma_f32_16x16x32_bf16 v[104:107], v[28:31], v[44:47], v[0:3]
	v_mfma_f32_16x16x32_bf16 v[0:3], v[32:35], v[40:43], 0
	v_mfma_f32_16x16x32_bf16 v[40:43], v[36:39], v[44:47], v[0:3]
	v_mfma_f32_16x16x32_bf16 v[0:3], v[24:27], v[48:51], 0
	v_mfma_f32_16x16x32_bf16 v[44:47], v[28:31], v[52:55], v[0:3]
	v_mfma_f32_16x16x32_bf16 v[0:3], v[32:35], v[48:51], 0
	v_mfma_f32_16x16x32_bf16 v[48:51], v[36:39], v[52:55], v[0:3]
	v_mfma_f32_16x16x32_bf16 v[0:3], v[24:27], v[56:59], 0
	v_mfma_f32_16x16x32_bf16 v[52:55], v[28:31], v[60:63], v[0:3]
	v_mfma_f32_16x16x32_bf16 v[0:3], v[32:35], v[56:59], 0
	v_mfma_f32_16x16x32_bf16 v[96:99], v[28:31], v[4:7], v[96:99]
	v_mfma_f32_16x16x32_bf16 v[56:59], v[36:39], v[60:63], v[0:3]
	s_barrier
	s_nop 3
	v_lshl_add_u64 v[0:1], s[38:39], 0, v[130:131]
	s_add_i32 s70, s59, s45
	v_lshl_add_u64 v[2:3], v[0:1], 0, s[18:19]
	s_mov_b32 m0, s70
	s_add_i32 s67, s70, 0x2000
	ds_read_b128 v[60:63], v140 offset:16384
	ds_read_b128 v[108:111], v140 offset:17408
	ds_read_b128 v[112:115], v140 offset:18432
	ds_read_b128 v[116:119], v140 offset:19456
	ds_read_b128 v[120:123], v140 offset:20480
	ds_read_b128 v[124:127], v140 offset:21504
	ds_read_b128 v[152:155], v140 offset:22528
	ds_read_b128 v[156:159], v140 offset:23552
	global_load_lds_dwordx4 v[2:3], off
	v_lshl_add_u64 v[2:3], s[38:39], 0, v[134:135]
	s_add_u32 s72, s38, 0x1900
	v_lshl_add_u64 v[4:5], v[2:3], 0, s[18:19]
	s_mov_b32 m0, s67
	s_addc_u32 s73, s39, 0
	s_add_i32 s68, s60, s45
	global_load_lds_dwordx4 v[4:5], off
	v_lshl_add_u64 v[4:5], s[72:73], 0, v[130:131]
	s_mov_b32 m0, s68
	s_add_i32 s69, s68, 0x2000
	global_load_lds_dwordx4 v[4:5], off
	v_lshl_add_u64 v[4:5], s[72:73], 0, v[134:135]
	s_mov_b32 m0, s69
	s_nop 0
	global_load_lds_dwordx4 v[4:5], off
	v_lshl_add_u64 v[4:5], s[36:37], 0, v[128:129]
	v_lshl_add_u64 v[6:7], v[4:5], 0, s[18:19]
	s_mov_b32 m0, s46
	s_nop 0
	global_load_lds_dwordx4 v[6:7], off
	v_lshl_add_u64 v[6:7], s[36:37], 0, v[132:133]
	v_lshl_add_u64 v[136:137], v[6:7], 0, s[18:19]
	s_mov_b32 m0, s47
	s_nop 0
	global_load_lds_dwordx4 v[136:137], off
	s_waitcnt vmcnt(8)
	s_waitcnt lgkmcnt(0)
	s_barrier
	s_waitcnt lgkmcnt(0)
	v_mfma_f32_16x16x32_bf16 v[160:163], v[8:11], v[60:63], 0
	v_mfma_f32_16x16x32_bf16 v[168:171], v[8:11], v[112:115], 0
	v_mfma_f32_16x16x32_bf16 v[176:179], v[8:11], v[120:123], 0
	v_mfma_f32_16x16x32_bf16 v[8:11], v[8:11], v[152:155], 0
	v_mfma_f32_16x16x32_bf16 v[160:163], v[12:15], v[108:111], v[160:163]
	v_mfma_f32_16x16x32_bf16 v[164:167], v[16:19], v[60:63], 0
	v_mfma_f32_16x16x32_bf16 v[168:171], v[12:15], v[116:119], v[168:171]
	v_mfma_f32_16x16x32_bf16 v[172:175], v[16:19], v[112:115], 0
	v_mfma_f32_16x16x32_bf16 v[176:179], v[12:15], v[124:127], v[176:179]
	v_mfma_f32_16x16x32_bf16 v[180:183], v[16:19], v[120:123], 0
	v_mfma_f32_16x16x32_bf16 v[10:13], v[12:15], v[156:159], v[8:11]
	v_mfma_f32_16x16x32_bf16 v[14:17], v[16:19], v[152:155], 0
	v_mfma_f32_16x16x32_bf16 v[14:17], v[20:23], v[156:159], v[14:17]
	v_mfma_f32_16x16x32_bf16 v[164:167], v[20:23], v[108:111], v[164:167]
	v_mfma_f32_16x16x32_bf16 v[172:175], v[20:23], v[116:119], v[172:175]
	v_mfma_f32_16x16x32_bf16 v[180:183], v[20:23], v[124:127], v[180:183]
	v_mfma_f32_16x16x32_bf16 v[18:21], v[24:27], v[60:63], 0
	v_mfma_f32_16x16x32_bf16 v[60:63], v[32:35], v[60:63], 0
	v_mfma_f32_16x16x32_bf16 v[18:21], v[28:31], v[108:111], v[18:21]
	v_mfma_f32_16x16x32_bf16 v[60:63], v[36:39], v[108:111], v[60:63]
	v_mfma_f32_16x16x32_bf16 v[108:111], v[24:27], v[112:115], 0
	v_mfma_f32_16x16x32_bf16 v[112:115], v[32:35], v[112:115], 0
	v_mfma_f32_16x16x32_bf16 v[108:111], v[28:31], v[116:119], v[108:111]
	v_mfma_f32_16x16x32_bf16 v[112:115], v[36:39], v[116:119], v[112:115]
	v_mfma_f32_16x16x32_bf16 v[116:119], v[24:27], v[120:123], 0
	v_mfma_f32_16x16x32_bf16 v[22:25], v[24:27], v[152:155], 0
	v_mfma_f32_16x16x32_bf16 v[116:119], v[28:31], v[124:127], v[116:119]
	v_mfma_f32_16x16x32_bf16 v[120:123], v[32:35], v[120:123], 0
	v_mfma_f32_16x16x32_bf16 v[22:25], v[28:31], v[156:159], v[22:25]
	v_mfma_f32_16x16x32_bf16 v[26:29], v[32:35], v[152:155], 0
	v_mfma_f32_16x16x32_bf16 v[120:123], v[36:39], v[124:127], v[120:123]
	v_mfma_f32_16x16x32_bf16 v[26:29], v[36:39], v[156:159], v[26:29]
	s_barrier
	s_add_i32 s74, 0, 0x18000
	s_add_i32 s75, 0, 0x1c000
	v_add_u32_e32 v8, s74, v139
	v_add_u32_e32 v9, s75, v139
	ds_read_b128 v[30:33], v8
	ds_read_b128 v[34:37], v8 offset:1024
	ds_read_b128 v[124:127], v8 offset:2048
	ds_read_b128 v[152:155], v8 offset:3072
	ds_read_b128 v[156:159], v9
	ds_read_b128 v[184:187], v9 offset:1024
	ds_read_b128 v[188:191], v9 offset:2048
	ds_read_b128 v[192:195], v9 offset:3072
	s_add_u32 s72, s36, 0x18100
	s_addc_u32 s73, s37, 0
	s_mov_b32 m0, s49
	v_lshl_add_u64 v[38:39], s[72:73], 0, v[128:129]
	ds_read_b128 v[196:199], v140 offset:32768
	ds_read_b128 v[200:203], v140 offset:33792
	ds_read_b128 v[204:207], v140 offset:34816
	ds_read_b128 v[208:211], v140 offset:35840
	ds_read_b128 v[212:215], v140 offset:36864
	ds_read_b128 v[216:219], v140 offset:37888
	ds_read_b128 v[220:223], v140 offset:38912
	ds_read_b128 v[224:227], v140 offset:39936
	global_load_lds_dwordx4 v[38:39], off
	v_lshl_add_u64 v[38:39], s[72:73], 0, v[132:133]
	s_mov_b32 m0, s50
	s_nop 0
	global_load_lds_dwordx4 v[38:39], off
	s_waitcnt vmcnt(8)
	s_waitcnt lgkmcnt(0)
	s_barrier
	s_waitcnt lgkmcnt(0)
	v_mfma_f32_16x16x32_bf16 v[64:67], v[30:33], v[196:199], v[64:67]
	v_mfma_f32_16x16x32_bf16 v[68:71], v[124:127], v[196:199], v[68:71]
	v_mfma_f32_16x16x32_bf16 v[72:75], v[30:33], v[204:207], v[72:75]
	v_mfma_f32_16x16x32_bf16 v[76:79], v[124:127], v[204:207], v[76:79]
	v_mfma_f32_16x16x32_bf16 v[80:83], v[30:33], v[212:215], v[80:83]
	v_mfma_f32_16x16x32_bf16 v[84:87], v[124:127], v[212:215], v[84:87]
	v_mfma_f32_16x16x32_bf16 v[88:91], v[30:33], v[220:223], v[88:91]
	v_mfma_f32_16x16x32_bf16 v[92:95], v[124:127], v[220:223], v[92:95]
	v_mfma_f32_16x16x32_bf16 v[64:67], v[34:37], v[200:203], v[64:67]
	v_mfma_f32_16x16x32_bf16 v[68:71], v[152:155], v[200:203], v[68:71]
	v_mfma_f32_16x16x32_bf16 v[72:75], v[34:37], v[208:211], v[72:75]
	v_mfma_f32_16x16x32_bf16 v[76:79], v[152:155], v[208:211], v[76:79]
	v_mfma_f32_16x16x32_bf16 v[80:83], v[34:37], v[216:219], v[80:83]
	v_mfma_f32_16x16x32_bf16 v[84:87], v[152:155], v[216:219], v[84:87]
	v_mfma_f32_16x16x32_bf16 v[88:91], v[34:37], v[224:227], v[88:91]
	v_mfma_f32_16x16x32_bf16 v[92:95], v[152:155], v[224:227], v[92:95]
	v_mfma_f32_16x16x32_bf16 v[96:99], v[156:159], v[196:199], v[96:99]
	v_mfma_f32_16x16x32_bf16 v[100:103], v[188:191], v[196:199], v[100:103]
	v_mfma_f32_16x16x32_bf16 v[104:107], v[156:159], v[204:207], v[104:107]
	v_mfma_f32_16x16x32_bf16 v[38:41], v[188:191], v[204:207], v[40:43]
	v_mfma_f32_16x16x32_bf16 v[42:45], v[156:159], v[212:215], v[44:47]
	v_mfma_f32_16x16x32_bf16 v[46:49], v[188:191], v[212:215], v[48:51]
	v_mfma_f32_16x16x32_bf16 v[50:53], v[156:159], v[220:223], v[52:55]
	v_mfma_f32_16x16x32_bf16 v[54:57], v[188:191], v[220:223], v[56:59]
	v_mfma_f32_16x16x32_bf16 v[96:99], v[184:187], v[200:203], v[96:99]
	v_mfma_f32_16x16x32_bf16 v[100:103], v[192:195], v[200:203], v[100:103]
	v_mfma_f32_16x16x32_bf16 v[104:107], v[184:187], v[208:211], v[104:107]
	v_mfma_f32_16x16x32_bf16 v[38:41], v[192:195], v[208:211], v[38:41]
	v_mfma_f32_16x16x32_bf16 v[42:45], v[184:187], v[216:219], v[42:45]
	v_mfma_f32_16x16x32_bf16 v[46:49], v[192:195], v[216:219], v[46:49]
	v_mfma_f32_16x16x32_bf16 v[50:53], v[184:187], v[224:227], v[50:53]
	v_mfma_f32_16x16x32_bf16 v[54:57], v[192:195], v[224:227], v[54:57]
	s_barrier
	s_add_i32 s74, s74, s45
	s_add_i32 s71, s74, 0x2000
	v_lshl_add_u64 v[58:59], v[0:1], 0, s[20:21]
	s_mov_b32 m0, s74
	s_add_u32 s76, s38, 0x1980
	ds_read_b128 v[196:199], v140 offset:49152
	ds_read_b128 v[200:203], v140 offset:50176
	ds_read_b128 v[204:207], v140 offset:51200
	ds_read_b128 v[208:211], v140 offset:52224
	ds_read_b128 v[212:215], v140 offset:53248
	ds_read_b128 v[216:219], v140 offset:54272
	ds_read_b128 v[220:223], v140 offset:55296
	ds_read_b128 v[224:227], v140 offset:56320
	global_load_lds_dwordx4 v[58:59], off
	v_lshl_add_u64 v[58:59], v[2:3], 0, s[20:21]
	s_mov_b32 m0, s71
	s_addc_u32 s77, s39, 0
	s_add_i32 s72, s75, s45
	global_load_lds_dwordx4 v[58:59], off
	v_lshl_add_u64 v[58:59], s[76:77], 0, v[130:131]
	s_mov_b32 m0, s72
	s_add_i32 s73, s72, 0x2000
	global_load_lds_dwordx4 v[58:59], off
	v_lshl_add_u64 v[58:59], s[76:77], 0, v[134:135]
	s_mov_b32 m0, s73
	s_nop 0
	global_load_lds_dwordx4 v[58:59], off
	v_lshl_add_u64 v[58:59], v[4:5], 0, s[20:21]
	s_mov_b32 m0, s52
	s_nop 0
	global_load_lds_dwordx4 v[58:59], off
	v_lshl_add_u64 v[58:59], v[6:7], 0, s[20:21]
	s_mov_b32 m0, s53
	s_nop 0
	global_load_lds_dwordx4 v[58:59], off
	s_waitcnt vmcnt(8)
	s_waitcnt lgkmcnt(0)
	s_barrier
	s_waitcnt lgkmcnt(0)
	v_mfma_f32_16x16x32_bf16 v[10:13], v[30:33], v[220:223], v[10:13]
	v_mfma_f32_16x16x32_bf16 v[14:17], v[124:127], v[220:223], v[14:17]
	v_mfma_f32_16x16x32_bf16 v[160:163], v[30:33], v[196:199], v[160:163]
	v_mfma_f32_16x16x32_bf16 v[164:167], v[124:127], v[196:199], v[164:167]
	v_mfma_f32_16x16x32_bf16 v[168:171], v[30:33], v[204:207], v[168:171]
	v_mfma_f32_16x16x32_bf16 v[172:175], v[124:127], v[204:207], v[172:175]
	v_mfma_f32_16x16x32_bf16 v[176:179], v[30:33], v[212:215], v[176:179]
	v_mfma_f32_16x16x32_bf16 v[180:183], v[124:127], v[212:215], v[180:183]
	v_mfma_f32_16x16x32_bf16 v[10:13], v[34:37], v[224:227], v[10:13]
	v_mfma_f32_16x16x32_bf16 v[14:17], v[152:155], v[224:227], v[14:17]
	v_mfma_f32_16x16x32_bf16 v[160:163], v[34:37], v[200:203], v[160:163]
	v_mfma_f32_16x16x32_bf16 v[164:167], v[152:155], v[200:203], v[164:167]
	v_mfma_f32_16x16x32_bf16 v[168:171], v[34:37], v[208:211], v[168:171]
	v_mfma_f32_16x16x32_bf16 v[172:175], v[152:155], v[208:211], v[172:175]
	v_mfma_f32_16x16x32_bf16 v[176:179], v[34:37], v[216:219], v[176:179]
	v_mfma_f32_16x16x32_bf16 v[180:183], v[152:155], v[216:219], v[180:183]
	v_mfma_f32_16x16x32_bf16 v[18:21], v[156:159], v[196:199], v[18:21]
	v_mfma_f32_16x16x32_bf16 v[30:33], v[188:191], v[196:199], v[60:63]
	v_mfma_f32_16x16x32_bf16 v[34:37], v[156:159], v[204:207], v[108:111]
	v_mfma_f32_16x16x32_bf16 v[58:61], v[188:191], v[204:207], v[112:115]
	v_mfma_f32_16x16x32_bf16 v[108:111], v[156:159], v[212:215], v[116:119]
	v_mfma_f32_16x16x32_bf16 v[112:115], v[188:191], v[212:215], v[120:123]
	v_mfma_f32_16x16x32_bf16 v[22:25], v[156:159], v[220:223], v[22:25]
	v_mfma_f32_16x16x32_bf16 v[26:29], v[188:191], v[220:223], v[26:29]
	v_mfma_f32_16x16x32_bf16 v[18:21], v[184:187], v[200:203], v[18:21]
	v_mfma_f32_16x16x32_bf16 v[30:33], v[192:195], v[200:203], v[30:33]
	v_mfma_f32_16x16x32_bf16 v[34:37], v[184:187], v[208:211], v[34:37]
	v_mfma_f32_16x16x32_bf16 v[58:61], v[192:195], v[208:211], v[58:61]
	v_mfma_f32_16x16x32_bf16 v[108:111], v[184:187], v[216:219], v[108:111]
	v_mfma_f32_16x16x32_bf16 v[112:115], v[192:195], v[216:219], v[112:115]
	v_mfma_f32_16x16x32_bf16 v[22:25], v[184:187], v[224:227], v[22:25]
	v_mfma_f32_16x16x32_bf16 v[26:29], v[192:195], v[224:227], v[26:29]
	s_barrier
	ds_read_b128 v[116:119], v149
	ds_read_b128 v[120:123], v149 offset:1024
	ds_read_b128 v[124:127], v149 offset:2048
	ds_read_b128 v[152:155], v149 offset:3072
	ds_read_b128 v[156:159], v150
	ds_read_b128 v[184:187], v150 offset:1024
	ds_read_b128 v[188:191], v150 offset:2048
	ds_read_b128 v[192:195], v150 offset:3072
	s_add_u32 s76, s36, 0x18180
	s_addc_u32 s77, s37, 0
	s_mov_b32 m0, s61
	v_lshl_add_u64 v[62:63], s[76:77], 0, v[128:129]
	ds_read_b128 v[196:199], v140
	ds_read_b128 v[200:203], v140 offset:1024
	ds_read_b128 v[204:207], v140 offset:2048
	ds_read_b128 v[208:211], v140 offset:3072
	ds_read_b128 v[212:215], v140 offset:4096
	ds_read_b128 v[216:219], v140 offset:5120
	ds_read_b128 v[220:223], v140 offset:6144
	ds_read_b128 v[224:227], v140 offset:7168
	global_load_lds_dwordx4 v[62:63], off
	v_lshl_add_u64 v[62:63], s[76:77], 0, v[132:133]
	s_mov_b32 m0, s62
	s_nop 0
	global_load_lds_dwordx4 v[62:63], off
	s_waitcnt vmcnt(8)
	s_waitcnt lgkmcnt(0)
	s_barrier
	s_waitcnt lgkmcnt(0)
	v_mfma_f32_16x16x32_bf16 v[62:65], v[116:119], v[196:199], v[64:67]
	v_mfma_f32_16x16x32_bf16 v[66:69], v[124:127], v[196:199], v[68:71]
	v_mfma_f32_16x16x32_bf16 v[70:73], v[116:119], v[204:207], v[72:75]
	v_mfma_f32_16x16x32_bf16 v[74:77], v[124:127], v[204:207], v[76:79]
	v_mfma_f32_16x16x32_bf16 v[78:81], v[116:119], v[212:215], v[80:83]
	v_mfma_f32_16x16x32_bf16 v[82:85], v[124:127], v[212:215], v[84:87]
	v_mfma_f32_16x16x32_bf16 v[86:89], v[116:119], v[220:223], v[88:91]
	v_mfma_f32_16x16x32_bf16 v[90:93], v[124:127], v[220:223], v[92:95]
	v_mfma_f32_16x16x32_bf16 v[62:65], v[120:123], v[200:203], v[62:65]
	v_mfma_f32_16x16x32_bf16 v[66:69], v[152:155], v[200:203], v[66:69]
	v_mfma_f32_16x16x32_bf16 v[70:73], v[120:123], v[208:211], v[70:73]
	v_mfma_f32_16x16x32_bf16 v[74:77], v[152:155], v[208:211], v[74:77]
	v_mfma_f32_16x16x32_bf16 v[78:81], v[120:123], v[216:219], v[78:81]
	v_mfma_f32_16x16x32_bf16 v[82:85], v[152:155], v[216:219], v[82:85]
	v_mfma_f32_16x16x32_bf16 v[86:89], v[120:123], v[224:227], v[86:89]
	v_mfma_f32_16x16x32_bf16 v[90:93], v[152:155], v[224:227], v[90:93]
	v_mfma_f32_16x16x32_bf16 v[94:97], v[156:159], v[196:199], v[96:99]
	v_mfma_f32_16x16x32_bf16 v[98:101], v[188:191], v[196:199], v[100:103]
	v_mfma_f32_16x16x32_bf16 v[102:105], v[156:159], v[204:207], v[104:107]
	v_mfma_f32_16x16x32_bf16 v[38:41], v[188:191], v[204:207], v[38:41]
	v_mfma_f32_16x16x32_bf16 v[42:45], v[156:159], v[212:215], v[42:45]
	v_mfma_f32_16x16x32_bf16 v[46:49], v[188:191], v[212:215], v[46:49]
	v_mfma_f32_16x16x32_bf16 v[50:53], v[156:159], v[220:223], v[50:53]
	v_mfma_f32_16x16x32_bf16 v[54:57], v[188:191], v[220:223], v[54:57]
	v_mfma_f32_16x16x32_bf16 v[94:97], v[184:187], v[200:203], v[94:97]
	v_mfma_f32_16x16x32_bf16 v[98:101], v[192:195], v[200:203], v[98:101]
	v_mfma_f32_16x16x32_bf16 v[102:105], v[184:187], v[208:211], v[102:105]
	v_mfma_f32_16x16x32_bf16 v[38:41], v[192:195], v[208:211], v[38:41]
	v_mfma_f32_16x16x32_bf16 v[42:45], v[184:187], v[216:219], v[42:45]
	v_mfma_f32_16x16x32_bf16 v[46:49], v[192:195], v[216:219], v[46:49]
	v_mfma_f32_16x16x32_bf16 v[50:53], v[184:187], v[224:227], v[50:53]
	v_mfma_f32_16x16x32_bf16 v[54:57], v[192:195], v[224:227], v[54:57]
	s_barrier
	s_mov_b32 m0, s70
	v_lshl_add_u64 v[106:107], v[0:1], 0, s[22:23]
	s_add_u32 s76, s38, 0x1a00
	ds_read_b128 v[196:199], v140 offset:16384
	ds_read_b128 v[200:203], v140 offset:17408
	ds_read_b128 v[204:207], v140 offset:18432
	ds_read_b128 v[208:211], v140 offset:19456
	ds_read_b128 v[212:215], v140 offset:20480
	ds_read_b128 v[216:219], v140 offset:21504
	ds_read_b128 v[220:223], v140 offset:22528
	ds_read_b128 v[224:227], v140 offset:23552
	global_load_lds_dwordx4 v[106:107], off
	v_lshl_add_u64 v[106:107], v[2:3], 0, s[22:23]
	s_mov_b32 m0, s67
	s_addc_u32 s77, s39, 0
	global_load_lds_dwordx4 v[106:107], off
	v_lshl_add_u64 v[106:107], s[76:77], 0, v[130:131]
	s_mov_b32 m0, s68
	s_nop 0
	global_load_lds_dwordx4 v[106:107], off
	v_lshl_add_u64 v[106:107], s[76:77], 0, v[134:135]
	s_mov_b32 m0, s69
	s_nop 0
	global_load_lds_dwordx4 v[106:107], off
	v_lshl_add_u64 v[106:107], v[4:5], 0, s[22:23]
	s_mov_b32 m0, s46
	s_nop 0
	global_load_lds_dwordx4 v[106:107], off
	v_lshl_add_u64 v[106:107], v[6:7], 0, s[22:23]
	s_mov_b32 m0, s47
	s_nop 0
	global_load_lds_dwordx4 v[106:107], off
	s_waitcnt vmcnt(8)
	s_waitcnt lgkmcnt(0)
	s_barrier
	s_waitcnt lgkmcnt(0)
	v_mfma_f32_16x16x32_bf16 v[10:13], v[116:119], v[220:223], v[10:13]
	v_mfma_f32_16x16x32_bf16 v[14:17], v[124:127], v[220:223], v[14:17]
	v_mfma_f32_16x16x32_bf16 v[160:163], v[116:119], v[196:199], v[160:163]
	v_mfma_f32_16x16x32_bf16 v[164:167], v[124:127], v[196:199], v[164:167]
	v_mfma_f32_16x16x32_bf16 v[168:171], v[116:119], v[204:207], v[168:171]
	v_mfma_f32_16x16x32_bf16 v[172:175], v[124:127], v[204:207], v[172:175]
	v_mfma_f32_16x16x32_bf16 v[176:179], v[116:119], v[212:215], v[176:179]
	v_mfma_f32_16x16x32_bf16 v[180:183], v[124:127], v[212:215], v[180:183]
	v_mfma_f32_16x16x32_bf16 v[10:13], v[120:123], v[224:227], v[10:13]
	v_mfma_f32_16x16x32_bf16 v[14:17], v[152:155], v[224:227], v[14:17]
	v_mfma_f32_16x16x32_bf16 v[160:163], v[120:123], v[200:203], v[160:163]
	v_mfma_f32_16x16x32_bf16 v[164:167], v[152:155], v[200:203], v[164:167]
	v_mfma_f32_16x16x32_bf16 v[168:171], v[120:123], v[208:211], v[168:171]
	v_mfma_f32_16x16x32_bf16 v[172:175], v[152:155], v[208:211], v[172:175]
	v_mfma_f32_16x16x32_bf16 v[176:179], v[120:123], v[216:219], v[176:179]
	v_mfma_f32_16x16x32_bf16 v[180:183], v[152:155], v[216:219], v[180:183]
	v_mfma_f32_16x16x32_bf16 v[18:21], v[156:159], v[196:199], v[18:21]
	v_mfma_f32_16x16x32_bf16 v[30:33], v[188:191], v[196:199], v[30:33]
	v_mfma_f32_16x16x32_bf16 v[34:37], v[156:159], v[204:207], v[34:37]
	v_mfma_f32_16x16x32_bf16 v[58:61], v[188:191], v[204:207], v[58:61]
	v_mfma_f32_16x16x32_bf16 v[106:109], v[156:159], v[212:215], v[108:111]
	v_mfma_f32_16x16x32_bf16 v[110:113], v[188:191], v[212:215], v[112:115]
	v_mfma_f32_16x16x32_bf16 v[22:25], v[156:159], v[220:223], v[22:25]
	v_mfma_f32_16x16x32_bf16 v[26:29], v[188:191], v[220:223], v[26:29]
	v_mfma_f32_16x16x32_bf16 v[18:21], v[184:187], v[200:203], v[18:21]
	v_mfma_f32_16x16x32_bf16 v[30:33], v[192:195], v[200:203], v[30:33]
	v_mfma_f32_16x16x32_bf16 v[34:37], v[184:187], v[208:211], v[34:37]
	v_mfma_f32_16x16x32_bf16 v[58:61], v[192:195], v[208:211], v[58:61]
	v_mfma_f32_16x16x32_bf16 v[106:109], v[184:187], v[216:219], v[106:109]
	v_mfma_f32_16x16x32_bf16 v[110:113], v[192:195], v[216:219], v[110:113]
	v_mfma_f32_16x16x32_bf16 v[22:25], v[184:187], v[224:227], v[22:25]
	v_mfma_f32_16x16x32_bf16 v[26:29], v[192:195], v[224:227], v[26:29]
	s_barrier
	ds_read_b128 v[114:117], v8
	ds_read_b128 v[118:121], v8 offset:1024
	ds_read_b128 v[122:125], v8 offset:2048
	ds_read_b128 v[152:155], v8 offset:3072
	ds_read_b128 v[156:159], v9
	ds_read_b128 v[184:187], v9 offset:1024
	ds_read_b128 v[188:191], v9 offset:2048
	ds_read_b128 v[192:195], v9 offset:3072
	s_add_u32 s76, s36, 0x18200
	s_addc_u32 s77, s37, 0
	s_mov_b32 m0, s49
	v_lshl_add_u64 v[126:127], s[76:77], 0, v[128:129]
	ds_read_b128 v[196:199], v140 offset:32768
	ds_read_b128 v[200:203], v140 offset:33792
	ds_read_b128 v[204:207], v140 offset:34816
	ds_read_b128 v[208:211], v140 offset:35840
	ds_read_b128 v[212:215], v140 offset:36864
	ds_read_b128 v[216:219], v140 offset:37888
	ds_read_b128 v[220:223], v140 offset:38912
	ds_read_b128 v[224:227], v140 offset:39936
	global_load_lds_dwordx4 v[126:127], off
	v_lshl_add_u64 v[126:127], s[76:77], 0, v[132:133]
	s_mov_b32 m0, s50
	s_nop 0
	global_load_lds_dwordx4 v[126:127], off
	s_waitcnt vmcnt(8)
	s_waitcnt lgkmcnt(0)
	s_barrier
	s_waitcnt lgkmcnt(0)
	v_mfma_f32_16x16x32_bf16 v[62:65], v[114:117], v[196:199], v[62:65]
	v_mfma_f32_16x16x32_bf16 v[66:69], v[122:125], v[196:199], v[66:69]
	v_mfma_f32_16x16x32_bf16 v[70:73], v[114:117], v[204:207], v[70:73]
	v_mfma_f32_16x16x32_bf16 v[74:77], v[122:125], v[204:207], v[74:77]
	v_mfma_f32_16x16x32_bf16 v[78:81], v[114:117], v[212:215], v[78:81]
	v_mfma_f32_16x16x32_bf16 v[82:85], v[122:125], v[212:215], v[82:85]
	v_mfma_f32_16x16x32_bf16 v[86:89], v[114:117], v[220:223], v[86:89]
	v_mfma_f32_16x16x32_bf16 v[90:93], v[122:125], v[220:223], v[90:93]
	v_mfma_f32_16x16x32_bf16 v[62:65], v[118:121], v[200:203], v[62:65]
	v_mfma_f32_16x16x32_bf16 v[66:69], v[152:155], v[200:203], v[66:69]
	v_mfma_f32_16x16x32_bf16 v[70:73], v[118:121], v[208:211], v[70:73]
	v_mfma_f32_16x16x32_bf16 v[74:77], v[152:155], v[208:211], v[74:77]
	v_mfma_f32_16x16x32_bf16 v[78:81], v[118:121], v[216:219], v[78:81]
	v_mfma_f32_16x16x32_bf16 v[82:85], v[152:155], v[216:219], v[82:85]
	v_mfma_f32_16x16x32_bf16 v[86:89], v[118:121], v[224:227], v[86:89]
	v_mfma_f32_16x16x32_bf16 v[90:93], v[152:155], v[224:227], v[90:93]
	v_mfma_f32_16x16x32_bf16 v[94:97], v[156:159], v[196:199], v[94:97]
	v_mfma_f32_16x16x32_bf16 v[98:101], v[188:191], v[196:199], v[98:101]
	v_mfma_f32_16x16x32_bf16 v[102:105], v[156:159], v[204:207], v[102:105]
	v_mfma_f32_16x16x32_bf16 v[38:41], v[188:191], v[204:207], v[38:41]
	v_mfma_f32_16x16x32_bf16 v[42:45], v[156:159], v[212:215], v[42:45]
	v_mfma_f32_16x16x32_bf16 v[46:49], v[188:191], v[212:215], v[46:49]
	v_mfma_f32_16x16x32_bf16 v[50:53], v[156:159], v[220:223], v[50:53]
	v_mfma_f32_16x16x32_bf16 v[54:57], v[188:191], v[220:223], v[54:57]
	v_mfma_f32_16x16x32_bf16 v[94:97], v[184:187], v[200:203], v[94:97]
	v_mfma_f32_16x16x32_bf16 v[98:101], v[192:195], v[200:203], v[98:101]
	v_mfma_f32_16x16x32_bf16 v[102:105], v[184:187], v[208:211], v[102:105]
	v_mfma_f32_16x16x32_bf16 v[38:41], v[192:195], v[208:211], v[38:41]
	v_mfma_f32_16x16x32_bf16 v[42:45], v[184:187], v[216:219], v[42:45]
	v_mfma_f32_16x16x32_bf16 v[46:49], v[192:195], v[216:219], v[46:49]
	v_mfma_f32_16x16x32_bf16 v[50:53], v[184:187], v[224:227], v[50:53]
	v_mfma_f32_16x16x32_bf16 v[54:57], v[192:195], v[224:227], v[54:57]
	s_barrier
	s_mov_b32 m0, s74
	v_lshl_add_u64 v[0:1], v[0:1], 0, s[24:25]
	s_add_u32 s38, s38, 0x1a80
	ds_read_b128 v[196:199], v140 offset:49152
	ds_read_b128 v[200:203], v140 offset:50176
	ds_read_b128 v[204:207], v140 offset:51200
	ds_read_b128 v[208:211], v140 offset:52224
	ds_read_b128 v[212:215], v140 offset:53248
	ds_read_b128 v[216:219], v140 offset:54272
	ds_read_b128 v[220:223], v140 offset:55296
	ds_read_b128 v[224:227], v140 offset:56320
	global_load_lds_dwordx4 v[0:1], off
	v_lshl_add_u64 v[0:1], v[2:3], 0, s[24:25]
	s_mov_b32 m0, s71
	s_addc_u32 s39, s39, 0
	global_load_lds_dwordx4 v[0:1], off
	v_lshl_add_u64 v[0:1], s[38:39], 0, v[130:131]
	s_mov_b32 m0, s72
	s_nop 0
	global_load_lds_dwordx4 v[0:1], off
	v_lshl_add_u64 v[0:1], s[38:39], 0, v[134:135]
	s_mov_b32 m0, s73
	s_nop 0
	global_load_lds_dwordx4 v[0:1], off
	v_lshl_add_u64 v[0:1], v[4:5], 0, s[24:25]
	s_mov_b32 m0, s52
	s_nop 0
	global_load_lds_dwordx4 v[0:1], off
	v_lshl_add_u64 v[0:1], v[6:7], 0, s[24:25]
	s_mov_b32 m0, s53
	s_nop 0
	global_load_lds_dwordx4 v[0:1], off
	s_waitcnt vmcnt(8)
	s_waitcnt lgkmcnt(0)
	s_barrier
	s_waitcnt lgkmcnt(0)
	v_mfma_f32_16x16x32_bf16 v[0:3], v[114:117], v[196:199], v[160:163]
	v_mfma_f32_16x16x32_bf16 v[4:7], v[122:125], v[196:199], v[164:167]
	v_mfma_f32_16x16x32_bf16 v[10:13], v[114:117], v[220:223], v[10:13]
	v_mfma_f32_16x16x32_bf16 v[14:17], v[122:125], v[220:223], v[14:17]
	v_mfma_f32_16x16x32_bf16 v[0:3], v[118:121], v[200:203], v[0:3]
	v_mfma_f32_16x16x32_bf16 v[4:7], v[152:155], v[200:203], v[4:7]
	v_mfma_f32_16x16x32_bf16 v[160:163], v[114:117], v[204:207], v[168:171]
	v_mfma_f32_16x16x32_bf16 v[164:167], v[122:125], v[204:207], v[172:175]
	v_mfma_f32_16x16x32_bf16 v[168:171], v[114:117], v[212:215], v[176:179]
	v_mfma_f32_16x16x32_bf16 v[172:175], v[122:125], v[212:215], v[180:183]
	v_mfma_f32_16x16x32_bf16 v[10:13], v[118:121], v[224:227], v[10:13]
	v_mfma_f32_16x16x32_bf16 v[14:17], v[152:155], v[224:227], v[14:17]
	v_mfma_f32_16x16x32_bf16 v[160:163], v[118:121], v[208:211], v[160:163]
	v_mfma_f32_16x16x32_bf16 v[164:167], v[152:155], v[208:211], v[164:167]
	v_mfma_f32_16x16x32_bf16 v[168:171], v[118:121], v[216:219], v[168:171]
	v_mfma_f32_16x16x32_bf16 v[172:175], v[152:155], v[216:219], v[172:175]
	v_mfma_f32_16x16x32_bf16 v[18:21], v[156:159], v[196:199], v[18:21]
	v_mfma_f32_16x16x32_bf16 v[30:33], v[188:191], v[196:199], v[30:33]
	v_mfma_f32_16x16x32_bf16 v[34:37], v[156:159], v[204:207], v[34:37]
	v_mfma_f32_16x16x32_bf16 v[58:61], v[188:191], v[204:207], v[58:61]
	v_mfma_f32_16x16x32_bf16 v[106:109], v[156:159], v[212:215], v[106:109]
	v_mfma_f32_16x16x32_bf16 v[110:113], v[188:191], v[212:215], v[110:113]
	v_mfma_f32_16x16x32_bf16 v[22:25], v[156:159], v[220:223], v[22:25]
	v_mfma_f32_16x16x32_bf16 v[26:29], v[188:191], v[220:223], v[26:29]
	v_mfma_f32_16x16x32_bf16 v[18:21], v[184:187], v[200:203], v[18:21]
	v_mfma_f32_16x16x32_bf16 v[30:33], v[192:195], v[200:203], v[30:33]
	v_mfma_f32_16x16x32_bf16 v[34:37], v[184:187], v[208:211], v[34:37]
	v_mfma_f32_16x16x32_bf16 v[58:61], v[192:195], v[208:211], v[58:61]
	v_mfma_f32_16x16x32_bf16 v[106:109], v[184:187], v[216:219], v[106:109]
	v_mfma_f32_16x16x32_bf16 v[110:113], v[192:195], v[216:219], v[110:113]
	v_mfma_f32_16x16x32_bf16 v[22:25], v[184:187], v[224:227], v[22:25]
	v_mfma_f32_16x16x32_bf16 v[26:29], v[192:195], v[224:227], v[26:29]
	s_barrier
	ds_read_b128 v[114:117], v149
	ds_read_b128 v[118:121], v149 offset:1024
	ds_read_b128 v[122:125], v149 offset:2048
	ds_read_b128 v[152:155], v149 offset:3072
	ds_read_b128 v[156:159], v150
	ds_read_b128 v[176:179], v150 offset:1024
	ds_read_b128 v[180:183], v150 offset:2048
	ds_read_b128 v[184:187], v150 offset:3072
	s_add_u32 s36, s36, 0x18280
	s_addc_u32 s37, s37, 0
	s_mov_b32 m0, s61
	v_lshl_add_u64 v[126:127], s[36:37], 0, v[128:129]
	ds_read_b128 v[188:191], v140
	ds_read_b128 v[192:195], v140 offset:1024
	ds_read_b128 v[196:199], v140 offset:2048
	ds_read_b128 v[200:203], v140 offset:3072
	ds_read_b128 v[204:207], v140 offset:4096
	ds_read_b128 v[208:211], v140 offset:5120
	ds_read_b128 v[212:215], v140 offset:6144
	ds_read_b128 v[216:219], v140 offset:7168
	global_load_lds_dwordx4 v[126:127], off
	v_lshl_add_u64 v[126:127], s[36:37], 0, v[132:133]
	s_mov_b32 m0, s62
	s_nop 0
	global_load_lds_dwordx4 v[126:127], off
	s_waitcnt vmcnt(8)
	s_waitcnt lgkmcnt(0)
	s_barrier
	s_waitcnt lgkmcnt(0)
	v_mfma_f32_16x16x32_bf16 v[82:85], v[122:125], v[204:207], v[82:85]
	v_mfma_f32_16x16x32_bf16 v[220:223], v[152:155], v[208:211], v[82:85]
	v_mfma_f32_16x16x32_bf16 v[82:85], v[114:117], v[212:215], v[86:89]
	v_mfma_f32_16x16x32_bf16 v[62:65], v[114:117], v[188:191], v[62:65]
	v_mfma_f32_16x16x32_bf16 v[66:69], v[122:125], v[188:191], v[66:69]
	v_mfma_f32_16x16x32_bf16 v[70:73], v[114:117], v[196:199], v[70:73]
	v_mfma_f32_16x16x32_bf16 v[74:77], v[122:125], v[196:199], v[74:77]
	v_mfma_f32_16x16x32_bf16 v[78:81], v[114:117], v[204:207], v[78:81]
	v_mfma_f32_16x16x32_bf16 v[224:227], v[118:121], v[216:219], v[82:85]
	v_mfma_f32_16x16x32_bf16 v[82:85], v[122:125], v[212:215], v[90:93]
	v_mfma_f32_16x16x32_bf16 v[62:65], v[118:121], v[192:195], v[62:65]
	v_mfma_f32_16x16x32_bf16 v[66:69], v[152:155], v[192:195], v[66:69]
	v_mfma_f32_16x16x32_bf16 v[70:73], v[118:121], v[200:203], v[70:73]
	v_mfma_f32_16x16x32_bf16 v[74:77], v[152:155], v[200:203], v[74:77]
	v_mfma_f32_16x16x32_bf16 v[78:81], v[118:121], v[208:211], v[78:81]
	v_mfma_f32_16x16x32_bf16 v[88:91], v[152:155], v[216:219], v[82:85]
	v_mfma_f32_16x16x32_bf16 v[82:85], v[156:159], v[188:191], v[94:97]
	v_mfma_f32_16x16x32_bf16 v[92:95], v[176:179], v[192:195], v[82:85]
	v_mfma_f32_16x16x32_bf16 v[82:85], v[180:183], v[188:191], v[98:101]
	v_mfma_f32_16x16x32_bf16 v[38:41], v[180:183], v[196:199], v[38:41]
	v_mfma_f32_16x16x32_bf16 v[42:45], v[156:159], v[204:207], v[42:45]
	v_mfma_f32_16x16x32_bf16 v[46:49], v[180:183], v[204:207], v[46:49]
	v_mfma_f32_16x16x32_bf16 v[50:53], v[156:159], v[212:215], v[50:53]
	v_mfma_f32_16x16x32_bf16 v[54:57], v[180:183], v[212:215], v[54:57]
	v_mfma_f32_16x16x32_bf16 v[188:191], v[184:187], v[192:195], v[82:85]
	v_mfma_f32_16x16x32_bf16 v[82:85], v[156:159], v[196:199], v[102:105]
	v_mfma_f32_16x16x32_bf16 v[38:41], v[184:187], v[200:203], v[38:41]
	v_mfma_f32_16x16x32_bf16 v[42:45], v[176:179], v[208:211], v[42:45]
	v_mfma_f32_16x16x32_bf16 v[46:49], v[184:187], v[208:211], v[46:49]
	v_mfma_f32_16x16x32_bf16 v[50:53], v[176:179], v[216:219], v[50:53]
	v_mfma_f32_16x16x32_bf16 v[54:57], v[184:187], v[216:219], v[54:57]
	v_mfma_f32_16x16x32_bf16 v[192:195], v[176:179], v[200:203], v[82:85]
	s_barrier
	s_mov_b32 m0, s70
	v_lshl_add_u64 v[136:137], s[28:29], 0, v[130:131]
	s_add_u32 s36, s28, 0x1800
	ds_read_b128 v[82:85], v140 offset:16384
	ds_read_b128 v[96:99], v140 offset:17408
	ds_read_b128 v[100:103], v140 offset:18432
	ds_read_b128 v[196:199], v140 offset:19456
	ds_read_b128 v[200:203], v140 offset:20480
	ds_read_b128 v[204:207], v140 offset:21504
	ds_read_b128 v[208:211], v140 offset:22528
	ds_read_b128 v[212:215], v140 offset:23552
	global_load_lds_dwordx4 v[136:137], off
	v_lshl_add_u64 v[142:143], s[28:29], 0, v[134:135]
	s_mov_b32 m0, s67
	s_addc_u32 s37, s29, 0
	global_load_lds_dwordx4 v[142:143], off
	v_lshl_add_u64 v[86:87], s[36:37], 0, v[130:131]
	s_mov_b32 m0, s68
	v_lshl_add_u64 v[144:145], s[26:27], 0, v[128:129]
	global_load_lds_dwordx4 v[86:87], off
	v_lshl_add_u64 v[86:87], s[36:37], 0, v[134:135]
	s_mov_b32 m0, s69
	v_lshl_add_u64 v[146:147], s[26:27], 0, v[132:133]
	global_load_lds_dwordx4 v[86:87], off
	s_mov_b32 m0, s46
	s_nop 0
	global_load_lds_dwordx4 v[144:145], off
	s_mov_b32 m0, s47
	s_nop 0
	global_load_lds_dwordx4 v[146:147], off
	s_waitcnt vmcnt(8)
	s_waitcnt lgkmcnt(0)
	s_barrier
	s_waitcnt lgkmcnt(0)
	v_mfma_f32_16x16x32_bf16 v[0:3], v[114:117], v[82:85], v[0:3]
	v_mfma_f32_16x16x32_bf16 v[4:7], v[122:125], v[82:85], v[4:7]
	v_mfma_f32_16x16x32_bf16 v[10:13], v[114:117], v[208:211], v[10:13]
	v_mfma_f32_16x16x32_bf16 v[0:3], v[118:121], v[96:99], v[0:3]
	v_mfma_f32_16x16x32_bf16 v[4:7], v[152:155], v[96:99], v[4:7]
	v_mfma_f32_16x16x32_bf16 v[160:163], v[114:117], v[100:103], v[160:163]
	v_mfma_f32_16x16x32_bf16 v[164:167], v[122:125], v[100:103], v[164:167]
	v_mfma_f32_16x16x32_bf16 v[168:171], v[114:117], v[200:203], v[168:171]
	v_mfma_f32_16x16x32_bf16 v[172:175], v[122:125], v[200:203], v[172:175]
	v_mfma_f32_16x16x32_bf16 v[10:13], v[118:121], v[212:215], v[10:13]
	v_mfma_f32_16x16x32_bf16 v[14:17], v[122:125], v[208:211], v[14:17]
	v_mfma_f32_16x16x32_bf16 v[160:163], v[118:121], v[196:199], v[160:163]
	v_mfma_f32_16x16x32_bf16 v[164:167], v[152:155], v[196:199], v[164:167]
	v_mfma_f32_16x16x32_bf16 v[168:171], v[118:121], v[204:207], v[168:171]
	v_mfma_f32_16x16x32_bf16 v[172:175], v[152:155], v[204:207], v[172:175]
	v_mfma_f32_16x16x32_bf16 v[152:155], v[152:155], v[212:215], v[14:17]
	v_mfma_f32_16x16x32_bf16 v[14:17], v[156:159], v[82:85], v[18:21]
	v_mfma_f32_16x16x32_bf16 v[216:219], v[176:179], v[96:99], v[14:17]
	v_mfma_f32_16x16x32_bf16 v[14:17], v[180:183], v[82:85], v[30:33]
	v_mfma_f32_16x16x32_bf16 v[228:231], v[184:187], v[96:99], v[14:17]
	v_mfma_f32_16x16x32_bf16 v[14:17], v[156:159], v[100:103], v[34:37]
	v_mfma_f32_16x16x32_bf16 v[232:235], v[176:179], v[196:199], v[14:17]
	v_mfma_f32_16x16x32_bf16 v[14:17], v[180:183], v[100:103], v[58:61]
	v_mfma_f32_16x16x32_bf16 v[196:199], v[184:187], v[196:199], v[14:17]
	v_mfma_f32_16x16x32_bf16 v[14:17], v[156:159], v[200:203], v[106:109]
	v_mfma_f32_16x16x32_bf16 v[236:239], v[176:179], v[204:207], v[14:17]
	v_mfma_f32_16x16x32_bf16 v[14:17], v[180:183], v[200:203], v[110:113]
	v_mfma_f32_16x16x32_bf16 v[200:203], v[184:187], v[204:207], v[14:17]
	v_mfma_f32_16x16x32_bf16 v[14:17], v[156:159], v[208:211], v[22:25]
	v_mfma_f32_16x16x32_bf16 v[156:159], v[176:179], v[212:215], v[14:17]
	v_mfma_f32_16x16x32_bf16 v[14:17], v[180:183], v[208:211], v[26:29]
	v_mfma_f32_16x16x32_bf16 v[176:179], v[184:187], v[212:215], v[14:17]
	s_barrier
	ds_read_b128 v[24:27], v8
	ds_read_b128 v[28:31], v8 offset:1024
	ds_read_b128 v[58:61], v8 offset:2048
	ds_read_b128 v[180:183], v8 offset:3072
	ds_read_b128 v[184:187], v9
	ds_read_b128 v[204:207], v9 offset:1024
	ds_read_b128 v[208:211], v9 offset:2048
	ds_read_b128 v[212:215], v9 offset:3072
	s_add_u32 s36, s26, 0x18000
	s_addc_u32 s37, s27, 0
	s_mov_b32 m0, s49
	v_lshl_add_u64 v[8:9], s[36:37], 0, v[128:129]
	ds_read_b128 v[14:17], v140 offset:32768
	ds_read_b128 v[18:21], v140 offset:33792
	ds_read_b128 v[32:35], v140 offset:34816
	ds_read_b128 v[108:111], v140 offset:35840
	ds_read_b128 v[240:243], v140 offset:36864
	ds_read_b128 v[244:247], v140 offset:37888
	ds_read_b128 v[248:251], v140 offset:38912
	ds_read_b128 v[252:255], v140 offset:39936
	global_load_lds_dwordx4 v[8:9], off
	v_lshl_add_u64 v[8:9], s[36:37], 0, v[132:133]
	s_mov_b32 m0, s50
	s_nop 0
	global_load_lds_dwordx4 v[8:9], off
	s_waitcnt vmcnt(8)
	s_waitcnt lgkmcnt(0)
	s_barrier
	s_waitcnt lgkmcnt(0)
	v_mfma_f32_16x16x32_bf16 v[62:65], v[24:27], v[14:17], v[62:65]
	v_mfma_f32_16x16x32_bf16 v[112:115], v[28:31], v[18:21], v[62:65]
	v_mfma_f32_16x16x32_bf16 v[62:65], v[58:61], v[14:17], v[66:69]
	v_mfma_f32_16x16x32_bf16 v[116:119], v[180:183], v[18:21], v[62:65]
	v_mfma_f32_16x16x32_bf16 v[62:65], v[24:27], v[32:35], v[70:73]
	v_mfma_f32_16x16x32_bf16 v[96:99], v[28:31], v[108:111], v[62:65]
	v_mfma_f32_16x16x32_bf16 v[62:65], v[58:61], v[32:35], v[74:77]
	v_mfma_f32_16x16x32_bf16 v[100:103], v[180:183], v[108:111], v[62:65]
	v_mfma_f32_16x16x32_bf16 v[62:65], v[24:27], v[240:243], v[78:81]
	v_mfma_f32_16x16x32_bf16 v[80:83], v[28:31], v[244:247], v[62:65]
	v_mfma_f32_16x16x32_bf16 v[62:65], v[58:61], v[240:243], v[220:223]
	v_mfma_f32_16x16x32_bf16 v[84:87], v[180:183], v[244:247], v[62:65]
	v_mfma_f32_16x16x32_bf16 v[62:65], v[24:27], v[248:251], v[224:227]
	v_mfma_f32_16x16x32_bf16 v[68:71], v[58:61], v[248:251], v[88:91]
	v_mfma_f32_16x16x32_bf16 v[64:67], v[28:31], v[252:255], v[62:65]
	v_mfma_f32_16x16x32_bf16 v[68:71], v[180:183], v[252:255], v[68:71]
	v_mfma_f32_16x16x32_bf16 v[72:75], v[184:187], v[14:17], v[92:95]
	v_mfma_f32_16x16x32_bf16 v[14:17], v[208:211], v[14:17], v[188:191]
	v_mfma_f32_16x16x32_bf16 v[124:127], v[212:215], v[18:21], v[14:17]
	v_mfma_f32_16x16x32_bf16 v[14:17], v[184:187], v[32:35], v[192:195]
	v_mfma_f32_16x16x32_bf16 v[104:107], v[204:207], v[108:111], v[14:17]
	v_mfma_f32_16x16x32_bf16 v[14:17], v[208:211], v[32:35], v[38:41]
	v_mfma_f32_16x16x32_bf16 v[108:111], v[212:215], v[108:111], v[14:17]
	v_mfma_f32_16x16x32_bf16 v[14:17], v[184:187], v[240:243], v[42:45]
	v_mfma_f32_16x16x32_bf16 v[88:91], v[204:207], v[244:247], v[14:17]
	v_mfma_f32_16x16x32_bf16 v[14:17], v[208:211], v[240:243], v[46:49]
	v_mfma_f32_16x16x32_bf16 v[92:95], v[212:215], v[244:247], v[14:17]
	v_mfma_f32_16x16x32_bf16 v[14:17], v[184:187], v[248:251], v[50:53]
	v_mfma_f32_16x16x32_bf16 v[120:123], v[204:207], v[18:21], v[72:75]
	v_mfma_f32_16x16x32_bf16 v[72:75], v[204:207], v[252:255], v[14:17]
	v_mfma_f32_16x16x32_bf16 v[14:17], v[208:211], v[248:251], v[54:57]
	v_mfma_f32_16x16x32_bf16 v[76:79], v[212:215], v[252:255], v[14:17]
	s_barrier
	s_mov_b32 m0, s74
	v_lshl_add_u64 v[8:9], v[136:137], 0, s[14:15]
	s_add_u32 s36, s28, 0x1880
	ds_read_b128 v[40:43], v140 offset:49152
	ds_read_b128 v[44:47], v140 offset:50176
	ds_read_b128 v[188:191], v140 offset:51200
	ds_read_b128 v[192:195], v140 offset:52224
	ds_read_b128 v[220:223], v140 offset:53248
	ds_read_b128 v[224:227], v140 offset:54272
	ds_read_b128 v[240:243], v140 offset:55296
	ds_read_b128 v[244:247], v140 offset:56320
	global_load_lds_dwordx4 v[8:9], off
	v_lshl_add_u64 v[8:9], v[142:143], 0, s[14:15]
	s_mov_b32 m0, s71
	s_addc_u32 s37, s29, 0
	global_load_lds_dwordx4 v[8:9], off
	v_lshl_add_u64 v[8:9], s[36:37], 0, v[130:131]
	s_mov_b32 m0, s72
	s_nop 0
	global_load_lds_dwordx4 v[8:9], off
	v_lshl_add_u64 v[8:9], s[36:37], 0, v[134:135]
	s_mov_b32 m0, s73
	s_nop 0
	global_load_lds_dwordx4 v[8:9], off
	v_lshl_add_u64 v[8:9], v[144:145], 0, s[14:15]
	s_mov_b32 m0, s52
	s_nop 0
	global_load_lds_dwordx4 v[8:9], off
	v_lshl_add_u64 v[8:9], v[146:147], 0, s[14:15]
	s_mov_b32 m0, s53
	s_nop 0
	global_load_lds_dwordx4 v[8:9], off
	s_waitcnt vmcnt(8)
	s_waitcnt lgkmcnt(0)
	s_barrier
	s_waitcnt lgkmcnt(0)
	v_mfma_f32_16x16x32_bf16 v[0:3], v[24:27], v[40:43], v[0:3]
	v_mfma_f32_16x16x32_bf16 v[48:51], v[28:31], v[44:47], v[0:3]
	v_mfma_f32_16x16x32_bf16 v[0:3], v[58:61], v[40:43], v[4:7]
	v_mfma_f32_16x16x32_bf16 v[52:55], v[180:183], v[44:47], v[0:3]
	v_mfma_f32_16x16x32_bf16 v[0:3], v[24:27], v[188:191], v[160:163]
	v_mfma_f32_16x16x32_bf16 v[32:35], v[28:31], v[192:195], v[0:3]
	v_mfma_f32_16x16x32_bf16 v[0:3], v[58:61], v[188:191], v[164:167]
	v_mfma_f32_16x16x32_bf16 v[36:39], v[180:183], v[192:195], v[0:3]
	v_mfma_f32_16x16x32_bf16 v[0:3], v[24:27], v[220:223], v[168:171]
	v_mfma_f32_16x16x32_bf16 v[16:19], v[28:31], v[224:227], v[0:3]
	v_mfma_f32_16x16x32_bf16 v[0:3], v[58:61], v[220:223], v[172:175]
	v_mfma_f32_16x16x32_bf16 v[20:23], v[180:183], v[224:227], v[0:3]
	v_mfma_f32_16x16x32_bf16 v[0:3], v[24:27], v[240:243], v[10:13]
	v_mfma_f32_16x16x32_bf16 v[4:7], v[58:61], v[240:243], v[152:155]
	v_mfma_f32_16x16x32_bf16 v[0:3], v[28:31], v[244:247], v[0:3]
	v_mfma_f32_16x16x32_bf16 v[4:7], v[180:183], v[244:247], v[4:7]
	v_mfma_f32_16x16x32_bf16 v[8:11], v[184:187], v[40:43], v[216:219]
	v_mfma_f32_16x16x32_bf16 v[56:59], v[204:207], v[44:47], v[8:11]
	v_mfma_f32_16x16x32_bf16 v[8:11], v[208:211], v[40:43], v[228:231]
	v_mfma_f32_16x16x32_bf16 v[60:63], v[212:215], v[44:47], v[8:11]
	v_mfma_f32_16x16x32_bf16 v[8:11], v[184:187], v[188:191], v[232:235]
	v_mfma_f32_16x16x32_bf16 v[40:43], v[204:207], v[192:195], v[8:11]
	v_mfma_f32_16x16x32_bf16 v[8:11], v[208:211], v[188:191], v[196:199]
	v_mfma_f32_16x16x32_bf16 v[44:47], v[212:215], v[192:195], v[8:11]
	v_mfma_f32_16x16x32_bf16 v[8:11], v[184:187], v[220:223], v[236:239]
	v_mfma_f32_16x16x32_bf16 v[24:27], v[204:207], v[224:227], v[8:11]
	v_mfma_f32_16x16x32_bf16 v[8:11], v[208:211], v[220:223], v[200:203]
	v_mfma_f32_16x16x32_bf16 v[28:31], v[212:215], v[224:227], v[8:11]
	v_mfma_f32_16x16x32_bf16 v[8:11], v[184:187], v[240:243], v[156:159]
	v_mfma_f32_16x16x32_bf16 v[12:15], v[208:211], v[240:243], v[176:179]
	v_mfma_f32_16x16x32_bf16 v[8:11], v[204:207], v[244:247], v[8:11]
	v_mfma_f32_16x16x32_bf16 v[12:15], v[212:215], v[244:247], v[12:15]
	s_barrier
	s_andn2_b64 vcc, exec, s[16:17]
	s_cbranch_vccnz .LBB0_4461
	s_barrier
